# v15 + nt on read-once dwordx2 row loads in P6 (z rows) and P9 (Y, x1 rows)
# speedup vs baseline: 1.0057x; 1.0057x over previous
; __device__ __forceinline__ float bf_lo(unsigned w) { return __uint_as_float(w << 16); }
; __device__ __forceinline__ float bf_hi(unsigned w) { return __uint_as_float(w & 0xffff0000u); }
; __device__ __forceinline__ void p6_router(Frame& F) {
;     ...
;         for (int q = 0; q < 2; ++q)
; #pragma unroll
;             for (int j = 0; j < 8; ++j) zr[q][j] = ((const u32x2*)(ZB + (size_t)(t0 + wave * 4 + q) * DM))[lane + 64 * j];
;         auto pass = [&](const int rp, f32x4 (&accp)[2]) __attribute__((always_inline)) {
;             const int ta = t0 + wave * 4 + 2 * rp;
;             f32x4 pw[8], pb[8];
;             int lop = lane; asm volatile("" : "+v"(lop));
; #pragma unroll
;             for (int j = 0; j < 8; ++j) { pw[j] = ((const f32x4*)F.in[I_LN1W])[lop + 64 * j]; pb[j] = ((const f32x4*)F.in[I_LN1B])[lop + 64 * j]; }
; #pragma unroll
;             for (int q = 0; q < 2; ++q) {
;                 const int t = ta + q; f32x4 v[8]; float s = 0.f;
; #pragma unroll
;                 for (int j = 0; j < 8; ++j) { const u32x2 zb = zr[q][j]; v[j] = (f32x4){bf_lo(zb.x), bf_hi(zb.x), bf_lo(zb.y), bf_hi(zb.y)}; s += (v[j][0] + v[j][1]) + (v[j][2] + v[j][3]); }
;                 float mean = wave_sum(s) * (1.f / DM), s2 = 0.f;
.LBB0_756:
	s_cmp_lt_i32 s34, 7
	s_cselect_b64 s[12:13], -1, 0
	s_and_b64 s[0:1], s[12:13], s[0:1]
	s_andn2_b64 vcc, exec, s[0:1]
	s_cbranch_vccnz .LBB0_931
	s_lshl_b32 s3, s2, 5
	s_cmpk_gt_i32 s3, 0x1fff
	s_cbranch_scc1 .LBB0_931
	s_add_u32 s6, s82, 0x4a600000
	s_addc_u32 s7, s83, 0
	s_add_u32 s42, s82, 0x4e600000
	v_readlane_b32 s46, v255, 8
	s_addc_u32 s43, s83, 0
	s_lshl_b32 s0, s46, 2
	s_add_i32 s4, s0, s3
	s_ashr_i32 s5, s4, 31
	s_lshl_b64 s[16:17], s[4:5], 12
	s_add_u32 s0, s6, s16
	s_addc_u32 s1, s7, s17
	v_lshlrev_b32_e32 v146, 3, v170
	global_load_dwordx2 v[2:3], v146, s[0:1] offset:512 nt
	global_load_dwordx2 v[4:5], v146, s[0:1] nt
	global_load_dwordx2 v[6:7], v146, s[0:1] offset:1024 nt
	global_load_dwordx2 v[8:9], v146, s[0:1] offset:1536 nt
	global_load_dwordx2 v[10:11], v146, s[0:1] offset:2048 nt
	global_load_dwordx2 v[12:13], v146, s[0:1] offset:2560 nt
	global_load_dwordx2 v[14:15], v146, s[0:1] offset:3072 nt
	global_load_dwordx2 v[16:17], v146, s[0:1] offset:3584 nt
	v_mbcnt_lo_u32_b32 v1, -1, 0
	v_mbcnt_hi_u32_b32 v19, -1, v1
	v_and_b32_e32 v1, 64, v19
	v_xor_b32_e32 v20, 1, v19
	v_add_u32_e32 v26, 64, v1
	v_cmp_lt_i32_e32 vcc, v20, v26
	v_xor_b32_e32 v21, 2, v19
	v_xor_b32_e32 v22, 4, v19
	v_cndmask_b32_e32 v1, v19, v20, vcc
	v_lshlrev_b32_e32 v1, 2, v1
	v_cmp_lt_i32_e32 vcc, v21, v26
	v_xor_b32_e32 v23, 8, v19
	v_xor_b32_e32 v24, 16, v19
	v_cndmask_b32_e32 v20, v19, v21, vcc
	v_lshlrev_b32_e32 v142, 2, v20
	v_cmp_lt_i32_e32 vcc, v22, v26
	v_xor_b32_e32 v25, 32, v19
	s_or_b32 s24, s4, 1
	v_cndmask_b32_e32 v21, v19, v22, vcc
	v_lshlrev_b32_e32 v143, 2, v21
	v_cmp_lt_i32_e32 vcc, v23, v26
	s_ashr_i32 s25, s24, 31
	s_lshl_b64 s[36:37], s[24:25], 12
	v_cndmask_b32_e32 v22, v19, v23, vcc
	v_lshlrev_b32_e32 v144, 2, v22
	v_cmp_lt_i32_e32 vcc, v24, v26
	s_add_u32 s0, s6, s36
	v_mov_b32_e32 v18, v170
	v_cndmask_b32_e32 v23, v19, v24, vcc
	v_lshlrev_b32_e32 v145, 2, v23
	v_cmp_lt_i32_e32 vcc, v25, v26
	s_addc_u32 s1, s7, s37
	global_load_dwordx2 v[86:87], v146, s[0:1] nt
	global_load_dwordx2 v[88:89], v146, s[0:1] offset:512 nt
	global_load_dwordx2 v[84:85], v146, s[0:1] offset:1024 nt
	global_load_dwordx2 v[82:83], v146, s[0:1] offset:1536 nt
	global_load_dwordx2 v[80:81], v146, s[0:1] offset:2048 nt
	global_load_dwordx2 v[78:79], v146, s[0:1] offset:2560 nt
	global_load_dwordx2 v[76:77], v146, s[0:1] offset:3072 nt
	global_load_dwordx2 v[74:75], v146, s[0:1] offset:3584 nt
	s_movk_i32 s41, 0x1000
	v_mov_b32_e32 v148, 0x358637bd
	s_mov_b32 s45, 0xf800000
	v_mov_b32_e32 v149, 0x260
	s_ashr_i32 s20, s3, 12
	s_add_u32 s40, s82, 0x2c000000
	s_addc_u32 s44, s83, 0
	v_lshlrev_b32_e32 v150, 2, v170
	v_and_b32_e32 v151, 15, v0
	v_lshrrev_b32_e32 v154, 4, v170
	s_waitcnt vmcnt(0)
	v_lshlrev_b32_e32 v111, 16, v2
	v_lshlrev_b32_e32 v110, 16, v4
	v_and_b32_e32 v113, 0xffff0000, v2
	v_and_b32_e32 v112, 0xffff0000, v4
	v_lshlrev_b32_e32 v107, 16, v3
	v_lshlrev_b32_e32 v106, 16, v5
	v_and_b32_e32 v109, 0xffff0000, v3
	v_and_b32_e32 v108, 0xffff0000, v5
	v_lshlrev_b32_e32 v105, 16, v7
	v_lshlrev_b32_e32 v104, 16, v6
	v_and_b32_e32 v7, 0xffff0000, v7
	v_and_b32_e32 v6, 0xffff0000, v6
	v_pk_add_f32 v[2:3], v[110:111], v[112:113]
	v_pk_add_f32 v[4:5], v[106:107], v[108:109]
	v_lshlrev_b32_e32 v117, 16, v10
	v_and_b32_e32 v69, 0xffff0000, v10
	v_lshlrev_b32_e32 v101, 16, v11
	v_and_b32_e32 v67, 0xffff0000, v11
	v_pk_add_f32 v[10:11], v[104:105], v[6:7]
	v_pk_add_f32 v[2:3], v[2:3], v[4:5]
	v_lshlrev_b32_e32 v70, 16, v8
	v_and_b32_e32 v71, 0xffff0000, v8
	v_lshlrev_b32_e32 v72, 16, v9
	v_and_b32_e32 v73, 0xffff0000, v9
	v_pk_add_f32 v[4:5], v[10:11], v[10:11] op_sel:[0,1] op_sel_hi:[1,0]
	v_add_f32_e32 v2, 0, v2
	v_add_f32_e32 v100, v70, v71
	v_add_f32_e32 v66, v72, v73
	v_mov_b32_e32 v5, v69
	v_add_f32_e32 v116, v2, v3
	v_lshlrev_b32_e32 v99, 16, v13
	v_lshlrev_b32_e32 v98, 16, v12
	v_and_b32_e32 v9, 0xffff0000, v13
	v_and_b32_e32 v8, 0xffff0000, v12
	v_pk_add_f32 v[10:11], v[100:101], v[66:67]
	v_pk_add_f32 v[2:3], v[116:117], v[4:5]
	v_pk_add_f32 v[12:13], v[98:99], v[8:9]
	v_pk_add_f32 v[2:3], v[2:3], v[10:11]
	v_lshlrev_b32_e32 v94, 16, v14
	v_and_b32_e32 v95, 0xffff0000, v14
	v_lshlrev_b32_e32 v96, 16, v15
	v_and_b32_e32 v97, 0xffff0000, v15
	v_lshlrev_b32_e32 v92, 16, v16
	v_and_b32_e32 v93, 0xffff0000, v16
	v_pk_add_f32 v[12:13], v[12:13], v[12:13] op_sel:[0,1] op_sel_hi:[1,0]
	v_pk_add_f32 v[2:3], v[2:3], v[2:3] op_sel:[0,1] op_sel_hi:[1,0]
	v_lshlrev_b32_e32 v103, 16, v17
	v_and_b32_e32 v91, 0xffff0000, v17
	v_add_f32_e32 v102, v94, v95
	v_add_f32_e32 v90, v96, v97
	v_mov_b32_e32 v13, v93
	v_mov_b32_e32 v3, v92
	v_pk_add_f32 v[14:15], v[102:103], v[90:91]
	v_pk_add_f32 v[2:3], v[2:3], v[12:13]
	v_cndmask_b32_e32 v4, v19, v25, vcc
	v_pk_add_f32 v[2:3], v[2:3], v[14:15]
	v_lshlrev_b32_e32 v147, 2, v4
	v_add_f32_e32 v2, v2, v3
	ds_bpermute_b32 v3, v1, v2
	v_ashrrev_i32_e32 v19, 31, v18
	v_and_b32_e32 v135, 0xffff0000, v79
	v_and_b32_e32 v134, 0xffff0000, v78
	s_waitcnt lgkmcnt(0)
	v_add_f32_e32 v2, v2, v3
	ds_bpermute_b32 v3, v142, v2
	s_waitcnt lgkmcnt(0)
	v_add_f32_e32 v2, v2, v3
	ds_bpermute_b32 v3, v143, v2
	s_waitcnt lgkmcnt(0)
	v_add_f32_e32 v2, v2, v3
	ds_bpermute_b32 v3, v144, v2
	s_waitcnt lgkmcnt(0)
	v_add_f32_e32 v2, v2, v3
	ds_bpermute_b32 v3, v145, v2
	s_waitcnt lgkmcnt(0)
	v_add_f32_e32 v14, v2, v3
	ds_bpermute_b32 v15, v147, v14
	v_lshlrev_b64 v[2:3], 4, v[18:19]
	v_lshl_add_u64 v[10:11], s[8:9], 0, v[2:3]
	v_lshl_add_u64 v[12:13], s[10:11], 0, v[2:3]
	global_load_dwordx4 v[2:5], v[10:11], off
	s_waitcnt lgkmcnt(0)
; __device__ __forceinline__ float bf_lo(unsigned w) { return __uint_as_float(w << 16); }
; __device__ __forceinline__ float bf_hi(unsigned w) { return __uint_as_float(w & 0xffff0000u); }
; __device__ __forceinline__ void p6_router(Frame& F) {
;     ...
;             for (int j = 0; j < 8; ++j) { pw[j] = ((const f32x4*)F.in[I_LN1W])[lop + 64 * j]; pb[j] = ((const f32x4*)F.in[I_LN1B])[lop + 64 * j]; }
; #pragma unroll
;             for (int q = 0; q < 2; ++q) {
;                 const int t = ta + q; f32x4 v[8]; float s = 0.f;
; #pragma unroll
;                 for (int j = 0; j < 8; ++j) { const u32x2 zb = zr[q][j]; v[j] = (f32x4){bf_lo(zb.x), bf_hi(zb.x), bf_lo(zb.y), bf_hi(zb.y)}; s += (v[j][0] + v[j][1]) + (v[j][2] + v[j][3]); }
;                 float mean = wave_sum(s) * (1.f / DM), s2 = 0.f;
; #pragma unroll
;                 for (int j = 0; j < 8; ++j) { v[j] = v[j] - mean; s2 += (v[j][0] * v[j][0] + v[j][1] * v[j][1]) + (v[j][2] * v[j][2] + v[j][3] * v[j][3]); }
;                 float rstd = 1.f / sqrtf(wave_sum(s2) * (1.f / DM) + LN_EPS);
	v_add_f32_e32 v20, v14, v15
	v_fmac_f32_e32 v108, 0xba000000, v20
	v_fmac_f32_e32 v112, 0xba000000, v20
	v_fmac_f32_e32 v109, 0xba000000, v20
	v_fmac_f32_e32 v113, 0xba000000, v20
	v_fmac_f32_e32 v106, 0xba000000, v20
	v_fmac_f32_e32 v110, 0xba000000, v20
	v_fmac_f32_e32 v107, 0xba000000, v20
	v_fmac_f32_e32 v111, 0xba000000, v20
	v_pk_mul_f32 v[14:15], v[112:113], v[112:113]
	v_pk_mul_f32 v[16:17], v[108:109], v[108:109]
	v_fmac_f32_e32 v6, 0xba000000, v20
	v_fmac_f32_e32 v7, 0xba000000, v20
	v_fmac_f32_e32 v105, 0xba000000, v20
	v_pk_fma_f32 v[14:15], v[110:111], v[110:111], v[14:15]
	v_pk_fma_f32 v[16:17], v[106:107], v[106:107], v[16:17]
	v_fmac_f32_e32 v104, 0xba000000, v20
	v_mov_b32_e32 v120, v105
	v_mov_b32_e32 v121, v7
	v_mov_b32_e32 v105, v6
	v_pk_add_f32 v[14:15], v[14:15], v[16:17]
	v_pk_mul_f32 v[16:17], v[120:121], v[120:121]
	v_pk_mul_f32 v[6:7], v[104:105], v[104:105]
	v_fmac_f32_e32 v70, 0xba000000, v20
	v_pk_mov_b32 v[18:19], v[6:7], v[16:17] op_sel:[1,0]
	v_mov_b32_e32 v7, v17
	v_pk_add_f32 v[6:7], v[18:19], v[6:7]
	v_fmac_f32_e32 v71, 0xba000000, v20
	v_pk_add_f32 v[6:7], v[6:7], v[6:7] op_sel_hi:[0,1]
	v_fmac_f32_e32 v72, 0xba000000, v20
	v_mul_f32_e32 v6, v70, v70
	v_fmac_f32_e32 v73, 0xba000000, v20
	v_pk_fma_f32 v[16:17], v[70:71], v[70:71], v[6:7] op_sel_hi:[1,1,0]
	v_mul_f32_e32 v6, v72, v72
	v_pk_add_f32 v[14:15], v[14:15], v[14:15] op_sel_hi:[0,1]
	v_pk_fma_f32 v[18:19], v[72:73], v[72:73], v[6:7] op_sel_hi:[1,1,0]
	v_fmac_f32_e32 v67, 0xba000000, v20
	v_fmac_f32_e32 v101, 0xba000000, v20
	v_fmac_f32_e32 v69, 0xba000000, v20
	v_fmac_f32_e32 v117, 0xba000000, v20
	v_mul_f32_e32 v16, v117, v117
	v_mul_f32_e32 v18, v69, v69
	v_mul_f32_e32 v6, v101, v101
	v_mul_f32_e32 v14, v67, v67
	v_pk_add_f32 v[16:17], v[16:17], v[18:19]
	v_pk_add_f32 v[6:7], v[6:7], v[14:15]
	v_fmac_f32_e32 v8, 0xba000000, v20
	v_fmac_f32_e32 v9, 0xba000000, v20
	v_fmac_f32_e32 v99, 0xba000000, v20
	v_pk_add_f32 v[6:7], v[16:17], v[6:7]
	v_fmac_f32_e32 v98, 0xba000000, v20
	v_mov_b32_e32 v118, v99
	v_mov_b32_e32 v119, v9
	v_mov_b32_e32 v99, v8
	v_pk_add_f32 v[6:7], v[6:7], v[6:7] op_sel_hi:[0,1]
	v_pk_mul_f32 v[14:15], v[118:119], v[118:119]
	v_pk_mul_f32 v[8:9], v[98:99], v[98:99]
	v_fmac_f32_e32 v94, 0xba000000, v20
	v_pk_mov_b32 v[16:17], v[8:9], v[14:15] op_sel:[1,0]
	v_mov_b32_e32 v9, v15
	v_fmac_f32_e32 v95, 0xba000000, v20
	v_fmac_f32_e32 v96, 0xba000000, v20
	v_mul_f32_e32 v6, v94, v94
	v_pk_add_f32 v[8:9], v[16:17], v[8:9]
	v_fmac_f32_e32 v97, 0xba000000, v20
	v_pk_fma_f32 v[14:15], v[94:95], v[94:95], v[6:7] op_sel_hi:[1,1,0]
	v_mul_f32_e32 v6, v96, v96
	v_pk_add_f32 v[8:9], v[8:9], v[8:9] op_sel_hi:[0,1]
	v_pk_fma_f32 v[16:17], v[96:97], v[96:97], v[6:7] op_sel_hi:[1,1,0]
	v_fmac_f32_e32 v91, 0xba000000, v20
	v_fmac_f32_e32 v103, 0xba000000, v20
	v_fmac_f32_e32 v93, 0xba000000, v20
	v_fmac_f32_e32 v92, 0xba000000, v20
	v_mul_f32_e32 v14, v92, v92
	v_mul_f32_e32 v16, v93, v93
	v_mul_f32_e32 v8, v103, v103
	v_mul_f32_e32 v6, v91, v91
	v_pk_add_f32 v[14:15], v[14:15], v[16:17]
	v_pk_add_f32 v[6:7], v[8:9], v[6:7]
	global_load_dwordx4 v[62:65], v[12:13], off
	v_pk_add_f32 v[6:7], v[14:15], v[6:7]
	global_load_dwordx4 v[54:57], v[10:11], off offset:1024
	global_load_dwordx4 v[58:61], v[12:13], off offset:1024
	v_add_f32_e32 v6, v6, v7
	ds_bpermute_b32 v7, v1, v6
	global_load_dwordx4 v[46:49], v[10:11], off offset:2048
	global_load_dwordx4 v[38:41], v[10:11], off offset:3072
	global_load_dwordx4 v[50:53], v[12:13], off offset:2048
	global_load_dwordx4 v[42:45], v[12:13], off offset:3072
	v_mov_b32_e32 v124, v107
	v_mov_b32_e32 v107, v108
	v_mov_b32_e32 v122, v111
	s_waitcnt lgkmcnt(0)
	v_add_f32_e32 v6, v6, v7
	ds_bpermute_b32 v7, v142, v6
	v_mov_b32_e32 v123, v113
	v_mov_b32_e32 v111, v112
	v_mov_b32_e32 v125, v109
	s_waitcnt lgkmcnt(0)
	v_add_f32_e32 v8, v6, v7
	ds_bpermute_b32 v9, v143, v8
	v_add_co_u32_e32 v6, vcc, s41, v10
	s_waitcnt lgkmcnt(0)
	v_add_f32_e32 v8, v8, v9
	ds_bpermute_b32 v9, v144, v8
	v_addc_co_u32_e32 v7, vcc, 0, v11, vcc
	v_add_co_u32_e32 v10, vcc, s41, v12
	global_load_dwordx4 v[30:33], v[6:7], off
	global_load_dwordx4 v[22:25], v[6:7], off offset:1024
	v_addc_co_u32_e32 v11, vcc, 0, v13, vcc
	s_waitcnt lgkmcnt(0)
	v_add_f32_e32 v12, v8, v9
	ds_bpermute_b32 v13, v145, v12
	global_load_dwordx4 v[34:37], v[10:11], off
	global_load_dwordx4 v[26:29], v[10:11], off offset:1024
	global_load_dwordx4 v[14:17], v[6:7], off offset:2048
	s_nop 0
	global_load_dwordx4 v[6:9], v[6:7], off offset:3072
	s_waitcnt lgkmcnt(0)
	v_add_f32_e32 v66, v12, v13
	global_load_dwordx4 v[18:21], v[10:11], off offset:2048
	s_nop 0
	global_load_dwordx4 v[10:13], v[10:11], off offset:3072
	ds_bpermute_b32 v68, v147, v66
	s_waitcnt lgkmcnt(0)
	v_add_f32_e32 v66, v66, v68
	v_fmamk_f32 v66, v66, 0x3a000000, v148
	v_mul_f32_e32 v68, 0x4f800000, v66
	v_cmp_gt_f32_e32 vcc, s45, v66
	s_nop 1
	v_cndmask_b32_e32 v66, v66, v68, vcc
	v_sqrt_f32_e32 v68, v66
	s_nop 0
	v_add_u32_e32 v90, -1, v68
	v_fma_f32 v100, -v90, v68, v66
	v_cmp_ge_f32_e64 s[0:1], 0, v100
	v_add_u32_e32 v100, 1, v68
	s_nop 0
	v_cndmask_b32_e64 v90, v68, v90, s[0:1]
	v_fma_f32 v68, -v100, v68, v66
	v_cmp_lt_f32_e64 s[0:1], 0, v68
	s_nop 1
	v_cndmask_b32_e64 v68, v90, v100, s[0:1]
	v_mul_f32_e32 v90, 0x37800000, v68
	v_cndmask_b32_e32 v68, v68, v90, vcc
	v_cmp_class_f32_e32 vcc, v66, v149
	s_nop 1
	v_cndmask_b32_e32 v66, v68, v66, vcc
	v_div_scale_f32 v68, s[0:1], v66, v66, 1.0
	v_rcp_f32_e32 v90, v68
	s_add_u32 s0, s42, s16
	s_addc_u32 s1, s43, s17
	s_lshl_b64 s[38:39], s[4:5], 11
	v_fma_f32 v100, -v68, v90, 1.0
	v_fmac_f32_e32 v90, v100, v90
	v_div_scale_f32 v100, vcc, 1.0, v66, 1.0
	v_mul_f32_e32 v102, v100, v90
	v_fma_f32 v108, -v68, v102, v100
	v_fmac_f32_e32 v102, v108, v90
	v_fma_f32 v68, -v68, v102, v100
	v_div_fmas_f32 v68, v68, v90, v102
	v_div_fixup_f32 v102, v68, v66, 1.0
	v_pk_mul_f32 v[106:107], v[106:107], v[102:103] op_sel_hi:[1,0]
	v_pk_mul_f32 v[108:109], v[110:111], v[102:103] op_sel_hi:[1,0]
	s_waitcnt vmcnt(14)
; __device__ __forceinline__ unsigned cvt_pk_bf16(float lo, float hi) { unsigned r; asm volatile("v_cvt_pk_bf16_f32 %0, %1, %2" : "=v"(r) : "v"(lo), "v"(hi)); return r; }
; __device__ __forceinline__ void p6_router(Frame& F) {
;     ...
;                 for (int j = 0; j < 8; ++j) { v[j] = v[j] * rstd * pw[j] + pb[j]; { u32x2 xb; xb.x = cvt_pk_bf16(v[j][0], v[j][1]); xb.y = cvt_pk_bf16(v[j][2], v[j][3]); ((u32x2*)(X1 + (size_t)t * DM))[lane + 64 * j] = xb; } s += (v[j][0] + v[j][1]) + (v[j][2] + v[j][3]); }
;                 mean = wave_sum(s) * (1.f / DM); s2 = 0.f;
	v_pk_fma_f32 v[112:113], v[4:5], v[106:107], v[64:65]
	v_pk_mul_f32 v[106:107], v[122:123], v[102:103] op_sel_hi:[1,0]
	v_pk_fma_f32 v[114:115], v[2:3], v[108:109], v[62:63]
	v_pk_mul_f32 v[108:109], v[124:125], v[102:103] op_sel_hi:[1,0]
	s_waitcnt vmcnt(12)
	v_pk_fma_f32 v[110:111], v[54:55], v[106:107], v[58:59]
	v_pk_fma_f32 v[108:109], v[56:57], v[108:109], v[60:61]
	v_mov_b32_e32 v106, v110
	v_mov_b32_e32 v107, v114
	v_mov_b32_e32 v122, v111
	v_mov_b32_e32 v123, v115
	v_pk_add_f32 v[106:107], v[106:107], v[122:123]
	v_mov_b32_e32 v122, v109
	v_mov_b32_e32 v123, v113
	v_mov_b32_e32 v124, v108
	v_mov_b32_e32 v125, v112
	v_pk_add_f32 v[122:123], v[122:123], v[124:125]
	v_mov_b32_e32 v68, v117
	v_pk_add_f32 v[106:107], v[106:107], v[122:123]
	v_pk_mul_f32 v[68:69], v[68:69], v[102:103] op_sel_hi:[1,0]
	v_add_f32_e32 v66, 0, v107
	v_add_f32_e32 v123, v106, v66
	v_pk_mul_f32 v[106:107], v[104:105], v[102:103] op_sel_hi:[1,0]
	v_pk_mul_f32 v[104:105], v[120:121], v[102:103] op_sel_hi:[1,0]
	s_waitcnt vmcnt(9)
	v_pk_fma_f32 v[106:107], v[46:47], v[106:107], v[50:51]
	v_pk_fma_f32 v[104:105], v[48:49], v[104:105], v[52:53]
	v_mov_b32_e32 v120, v106
	v_mov_b32_e32 v121, v105
	v_pk_mov_b32 v[124:125], v[106:107], v[104:105] op_sel:[1,0]
	v_mov_b32_e32 v66, v101
	v_pk_add_f32 v[120:121], v[120:121], v[124:125]
	v_pk_mul_f32 v[124:125], v[70:71], v[102:103] op_sel_hi:[1,0]
	v_pk_mul_f32 v[70:71], v[72:73], v[102:103] op_sel_hi:[1,0]
	v_pk_mul_f32 v[66:67], v[66:67], v[102:103] op_sel_hi:[1,0]
	v_pk_add_f32 v[120:121], v[120:121], v[120:121] op_sel_hi:[0,1]
	s_waitcnt vmcnt(8)
	v_pk_fma_f32 v[70:71], v[40:41], v[70:71], v[44:45]
	v_pk_fma_f32 v[72:73], v[38:39], v[124:125], v[42:43]
	s_waitcnt vmcnt(5)
	v_pk_fma_f32 v[66:67], v[32:33], v[66:67], v[36:37]
	v_pk_fma_f32 v[68:69], v[30:31], v[68:69], v[34:35]
	v_add_f32_e32 v125, v72, v73
	v_add_f32_e32 v129, v71, v70
	v_mov_b32_e32 v124, v68
	v_mov_b32_e32 v128, v69
	v_mov_b32_e32 v120, v67
	v_mov_b32_e32 v122, v66
	v_pk_add_f32 v[100:101], v[124:125], v[128:129]
	v_pk_add_f32 v[116:117], v[120:121], v[122:123]
	v_mov_b32_e32 v90, v103
	v_pk_add_f32 v[100:101], v[100:101], v[116:117]
	v_pk_mul_f32 v[92:93], v[92:93], v[102:103] op_sel_hi:[1,0]
	v_pk_add_f32 v[116:117], v[100:101], v[100:101] op_sel_hi:[0,1]
	v_pk_mul_f32 v[100:101], v[98:99], v[102:103] op_sel_hi:[1,0]
	v_pk_mul_f32 v[98:99], v[118:119], v[102:103] op_sel_hi:[1,0]
	s_waitcnt vmcnt(4)
	v_pk_fma_f32 v[100:101], v[22:23], v[100:101], v[26:27]
	v_pk_fma_f32 v[98:99], v[24:25], v[98:99], v[28:29]
	v_mov_b32_e32 v118, v100
	v_mov_b32_e32 v119, v99
	v_pk_mov_b32 v[120:121], v[100:101], v[98:99] op_sel:[1,0]
	v_pk_mul_f32 v[90:91], v[90:91], v[102:103] op_sel_hi:[1,0]
	v_pk_add_f32 v[118:119], v[118:119], v[120:121]
	v_pk_mul_f32 v[120:121], v[94:95], v[102:103] op_sel_hi:[1,0]
	v_pk_mul_f32 v[94:95], v[96:97], v[102:103] op_sel_hi:[1,0]
	v_pk_add_f32 v[118:119], v[118:119], v[118:119] op_sel_hi:[0,1]
	s_waitcnt vmcnt(1)
	v_pk_fma_f32 v[94:95], v[16:17], v[94:95], v[20:21]
	v_pk_fma_f32 v[96:97], v[14:15], v[120:121], v[18:19]
	s_waitcnt vmcnt(0)
	v_pk_fma_f32 v[90:91], v[8:9], v[90:91], v[12:13]
	v_pk_fma_f32 v[92:93], v[6:7], v[92:93], v[10:11]
	v_add_f32_e32 v121, v96, v97
	v_add_f32_e32 v123, v95, v94
	v_mov_b32_e32 v120, v92
	v_mov_b32_e32 v122, v93
	v_mov_b32_e32 v118, v91
	v_mov_b32_e32 v116, v90
	v_pk_add_f32 v[102:103], v[120:121], v[122:123]
	v_pk_add_f32 v[116:117], v[118:119], v[116:117]
	v_cvt_pk_bf16_f32 v126, v114, v115
	v_cvt_pk_bf16_f32 v127, v112, v113
	global_store_dwordx2 v146, v[126:127], s[0:1]
	v_pk_add_f32 v[102:103], v[102:103], v[116:117]
	s_nop 0
	v_add_f32_e32 v103, v102, v103
	ds_bpermute_b32 v116, v1, v103
	v_cvt_pk_bf16_f32 v102, v110, v111
	s_waitcnt lgkmcnt(0)
	v_add_f32_e32 v116, v103, v116
	ds_bpermute_b32 v117, v142, v116
	v_cvt_pk_bf16_f32 v103, v108, v109
	global_store_dwordx2 v146, v[102:103], s[0:1] offset:512
	v_cvt_pk_bf16_f32 v102, v106, v107
	v_cvt_pk_bf16_f32 v103, v104, v105
	s_waitcnt lgkmcnt(0)
	v_add_f32_e32 v116, v116, v117
	ds_bpermute_b32 v117, v143, v116
	global_store_dwordx2 v146, v[102:103], s[0:1] offset:1024
	v_cvt_pk_bf16_f32 v102, v72, v73
	v_cvt_pk_bf16_f32 v103, v70, v71
	global_store_dwordx2 v146, v[102:103], s[0:1] offset:1536
	s_waitcnt lgkmcnt(0)
	v_add_f32_e32 v116, v116, v117
	ds_bpermute_b32 v117, v144, v116
	v_cvt_pk_bf16_f32 v102, v68, v69
	v_cvt_pk_bf16_f32 v103, v66, v67
	global_store_dwordx2 v146, v[102:103], s[0:1] offset:2048
	v_cvt_pk_bf16_f32 v102, v100, v101
	s_waitcnt lgkmcnt(0)
	v_add_f32_e32 v116, v116, v117
	ds_bpermute_b32 v117, v145, v116
	v_cvt_pk_bf16_f32 v103, v98, v99
	global_store_dwordx2 v146, v[102:103], s[0:1] offset:2560
	v_cvt_pk_bf16_f32 v102, v96, v97
	v_cvt_pk_bf16_f32 v103, v94, v95
	s_waitcnt lgkmcnt(0)
	v_add_f32_e32 v116, v116, v117
	ds_bpermute_b32 v117, v147, v116
	global_store_dwordx2 v146, v[102:103], s[0:1] offset:3072
	v_cvt_pk_bf16_f32 v102, v92, v93
	v_cvt_pk_bf16_f32 v103, v90, v91
	global_store_dwordx2 v146, v[102:103], s[0:1] offset:3584
	s_waitcnt lgkmcnt(0)
; __device__ __forceinline__ void p6_router(Frame& F) {
;     ...
;                 mean = wave_sum(s) * (1.f / DM); s2 = 0.f;
; #pragma unroll
;                 for (int j = 0; j < 8; ++j) { v[j] = v[j] - mean; s2 += (v[j][0] * v[j][0] + v[j][1] * v[j][1]) + (v[j][2] * v[j][2] + v[j][3] * v[j][3]); }
;                 rstd = 1.f / sqrtf(wave_sum(s2) * (1.f / DM) + LN_EPS);
;                 int loq = lane; asm volatile("" : "+v"(loq));
; #pragma unroll
;                 for (int j = 0; j < 8; ++j) { const f32x4 sh = ((const f32x4*)(mod + (size_t)b * 12288 + 6144))[loq + 64 * j], sc = ((const f32x4*)(mod + (size_t)b * 12288 + 8192))[loq + 64 * j];
	v_add_f32_e32 v122, v116, v117
	v_fmamk_f32 v115, v122, 0xba000000, v115
	v_fmamk_f32 v111, v122, 0xba000000, v111
	v_fmamk_f32 v113, v122, 0xba000000, v113
	v_fmac_f32_e32 v114, 0xba000000, v122
	v_fmamk_f32 v109, v122, 0xba000000, v109
	v_fmac_f32_e32 v110, 0xba000000, v122
	v_mov_b32_e32 v116, v115
	v_mov_b32_e32 v117, v111
	v_fmac_f32_e32 v112, 0xba000000, v122
	v_fmac_f32_e32 v108, 0xba000000, v122
	v_mov_b32_e32 v102, v114
	v_mov_b32_e32 v103, v110
	v_pk_mul_f32 v[116:117], v[116:117], v[116:117]
	v_mov_b32_e32 v118, v113
	v_mov_b32_e32 v119, v109
	v_pk_fma_f32 v[102:103], v[102:103], v[102:103], v[116:117]
	v_mov_b32_e32 v116, v112
	v_mov_b32_e32 v117, v108
	v_pk_mul_f32 v[118:119], v[118:119], v[118:119]
	v_fmamk_f32 v107, v122, 0xba000000, v107
	v_pk_fma_f32 v[116:117], v[116:117], v[116:117], v[118:119]
	v_fmac_f32_e32 v106, 0xba000000, v122
	v_pk_add_f32 v[102:103], v[102:103], v[116:117]
	v_fmamk_f32 v105, v122, 0xba000000, v105
	v_fmac_f32_e32 v104, 0xba000000, v122
	v_pk_add_f32 v[102:103], v[102:103], v[102:103] op_sel_hi:[0,1]
	v_pk_mul_f32 v[116:117], v[104:105], v[104:105]
	v_pk_mul_f32 v[118:119], v[106:107], v[106:107]
	v_fmac_f32_e32 v72, 0xba000000, v122
	v_pk_mov_b32 v[120:121], v[118:119], v[116:117] op_sel:[1,0]
	v_mov_b32_e32 v119, v117
	v_fmamk_f32 v73, v122, 0xba000000, v73
	v_fmac_f32_e32 v70, 0xba000000, v122
	v_mul_f32_e32 v102, v72, v72
	v_pk_add_f32 v[116:117], v[120:121], v[118:119]
	v_fmamk_f32 v71, v122, 0xba000000, v71
	v_pk_fma_f32 v[118:119], v[72:73], v[72:73], v[102:103] op_sel_hi:[1,1,0]
	v_mul_f32_e32 v102, v70, v70
	v_pk_add_f32 v[116:117], v[116:117], v[116:117] op_sel_hi:[0,1]
	v_pk_fma_f32 v[120:121], v[70:71], v[70:71], v[102:103] op_sel_hi:[1,1,0]
	v_fmamk_f32 v67, v122, 0xba000000, v67
	v_fmac_f32_e32 v66, 0xba000000, v122
	v_fmamk_f32 v69, v122, 0xba000000, v69
	v_fmac_f32_e32 v68, 0xba000000, v122
	v_mul_f32_e32 v118, v68, v68
	v_mul_f32_e32 v120, v69, v69
	v_mul_f32_e32 v116, v66, v66
	v_mul_f32_e32 v102, v67, v67
	v_pk_add_f32 v[118:119], v[118:119], v[120:121]
	v_pk_add_f32 v[102:103], v[116:117], v[102:103]
	v_fmamk_f32 v101, v122, 0xba000000, v101
	v_fmac_f32_e32 v100, 0xba000000, v122
	v_fmamk_f32 v99, v122, 0xba000000, v99
	v_fmac_f32_e32 v98, 0xba000000, v122
	v_pk_add_f32 v[102:103], v[118:119], v[102:103]
	v_pk_mul_f32 v[116:117], v[98:99], v[98:99]
	v_pk_mul_f32 v[118:119], v[100:101], v[100:101]
	s_mul_hi_i32 s0, s20, 0xc000
	s_mul_i32 s20, s20, 0xc000
	v_pk_mov_b32 v[120:121], v[118:119], v[116:117] op_sel:[1,0]
	v_mov_b32_e32 v119, v117
	s_add_u32 s1, s82, s20
	v_pk_add_f32 v[116:117], v[120:121], v[118:119]
	s_addc_u32 s0, s83, s0
	v_pk_add_f32 v[128:129], v[116:117], v[116:117] op_sel_hi:[0,1]
	v_mov_b32_e32 v116, v170
	s_add_u32 s16, s1, 0x106000
	s_addc_u32 s17, s0, 0
	v_ashrrev_i32_e32 v117, 31, v116
	v_lshlrev_b64 v[118:119], 4, v[116:117]
	s_add_u32 s20, s1, 0x108000
	v_lshl_add_u64 v[116:117], s[16:17], 0, v[118:119]
	s_addc_u32 s21, s0, 0
	v_fmamk_f32 v97, v122, 0xba000000, v97
	v_fmac_f32_e32 v96, 0xba000000, v122
	v_fmamk_f32 v95, v122, 0xba000000, v95
	v_fmac_f32_e32 v94, 0xba000000, v122
	v_fmamk_f32 v91, v122, 0xba000000, v91
	v_fmac_f32_e32 v90, 0xba000000, v122
	v_fmamk_f32 v93, v122, 0xba000000, v93
	v_fmac_f32_e32 v92, 0xba000000, v122
	v_lshl_add_u64 v[118:119], s[20:21], 0, v[118:119]
	global_load_dwordx4 v[120:123], v[116:117], off
	global_load_dwordx4 v[124:127], v[118:119], off
	v_pk_add_f32 v[102:103], v[102:103], v[102:103] op_sel_hi:[0,1]
	v_mul_f32_e32 v102, v96, v96
	v_pk_fma_f32 v[130:131], v[96:97], v[96:97], v[102:103] op_sel_hi:[1,1,0]
	v_mul_f32_e32 v102, v94, v94
	v_pk_fma_f32 v[132:133], v[94:95], v[94:95], v[102:103] op_sel_hi:[1,1,0]
	v_mul_f32_e32 v130, v92, v92
	v_mul_f32_e32 v132, v93, v93
	v_mul_f32_e32 v128, v90, v90
	v_mul_f32_e32 v102, v91, v91
	v_pk_add_f32 v[130:131], v[130:131], v[132:133]
	v_pk_add_f32 v[102:103], v[128:129], v[102:103]
	s_lshl_b32 s5, s46, 5
	v_pk_add_f32 v[102:103], v[130:131], v[102:103]
	v_and_b32_e32 v133, 0xffff0000, v85
	v_add_f32_e32 v102, v102, v103
	ds_bpermute_b32 v103, v1, v102
	v_and_b32_e32 v132, 0xffff0000, v84
	s_waitcnt lgkmcnt(0)
	v_add_f32_e32 v102, v102, v103
	ds_bpermute_b32 v103, v142, v102
	s_waitcnt lgkmcnt(0)
	v_add_f32_e32 v102, v102, v103
	ds_bpermute_b32 v103, v143, v102
	s_waitcnt lgkmcnt(0)
	v_add_f32_e32 v102, v102, v103
	ds_bpermute_b32 v103, v144, v102
	s_waitcnt lgkmcnt(0)
	v_add_f32_e32 v102, v102, v103
	ds_bpermute_b32 v103, v145, v102
	s_waitcnt lgkmcnt(0)
	v_add_f32_e32 v102, v102, v103
	ds_bpermute_b32 v103, v147, v102
	s_waitcnt lgkmcnt(0)
	v_add_f32_e32 v102, v102, v103
	v_fmamk_f32 v102, v102, 0x3a000000, v148
	v_mul_f32_e32 v103, 0x4f800000, v102
	v_cmp_gt_f32_e32 vcc, s45, v102
	s_waitcnt vmcnt(0)
; #define LAS __attribute__((address_space(3)))
; __device__ __forceinline__ unsigned cvt_pk_bf16(float lo, float hi) { unsigned r; asm volatile("v_cvt_pk_bf16_f32 %0, %1, %2" : "=v"(r) : "v"(lo), "v"(hi)); return r; }
; __device__ __forceinline__ unsigned pk4_fp8(float a, float b, float c, float d) { int w = 0; w = __builtin_amdgcn_cvt_pk_fp8_f32(a, b, w, false); w = __builtin_amdgcn_cvt_pk_fp8_f32(c, d, w, true); return (unsigned)w; }
; __device__ __forceinline__ float bf_lo(unsigned w) { return __uint_as_float(w << 16); }
; __device__ __forceinline__ float bf_hi(unsigned w) { return __uint_as_float(w & 0xffff0000u); }
; __device__ __forceinline__ void p6_router(Frame& F) {
;     ...
; #pragma unroll
;                 for (int j = 0; j < 8; ++j) { const f32x4 sh = ((const f32x4*)(mod + (size_t)b * 12288 + 6144))[loq + 64 * j], sc = ((const f32x4*)(mod + (size_t)b * 12288 + 8192))[loq + 64 * j];
;                     const f32x4 y = v[j] * rstd * (sc + 1.0f) + sh;
;                     u32x2 wh; wh.x = cvt_pk_bf16(y[0], y[1]); wh.y = cvt_pk_bf16(y[2], y[3]);
;                     const f32x4 yl = {y[0] - bf_lo(wh.x), y[1] - bf_hi(wh.x), y[2] - bf_lo(wh.y), y[3] - bf_hi(wh.y)};
;                     u32x2 wl; wl.x = cvt_pk_bf16(yl[0], yl[1]); wl.y = cvt_pk_bf16(yl[2], yl[3]);
;                     { const int r = 2 * wave + q; LAS unsigned char* rowp = F.lds + r * 4096 + ((((lane >> 1) + 32 * j) ^ r) << 4) + (lane & 1) * 8;
;                       *(LAS u32x2*)rowp = wh; *(LAS u32x2*)(rowp + 65536) = wl; }
;                     U2F[(size_t)t * (DM / 4) + lane + 64 * j] = pk4_fp8(y[0], y[1], y[2], y[3]); }
	v_pk_add_f32 v[124:125], v[124:125], 1.0 op_sel_hi:[1,0]
	v_cndmask_b32_e32 v102, v102, v103, vcc
	v_sqrt_f32_e32 v103, v102
	v_pk_add_f32 v[126:127], v[126:127], 1.0 op_sel_hi:[1,0]
	v_add_u32_e32 v128, -1, v103
	v_fma_f32 v129, -v128, v103, v102
	v_cmp_ge_f32_e64 s[0:1], 0, v129
	v_add_u32_e32 v129, 1, v103
	s_nop 0
	v_cndmask_b32_e64 v128, v103, v128, s[0:1]
	v_fma_f32 v103, -v129, v103, v102
	v_cmp_lt_f32_e64 s[0:1], 0, v103
	s_nop 1
	v_cndmask_b32_e64 v103, v128, v129, s[0:1]
	v_mul_f32_e32 v128, 0x37800000, v103
	v_cndmask_b32_e32 v103, v103, v128, vcc
	v_cmp_class_f32_e32 vcc, v102, v149
	s_nop 1
	v_cndmask_b32_e32 v102, v103, v102, vcc
	v_div_scale_f32 v103, s[0:1], v102, v102, 1.0
	v_rcp_f32_e32 v128, v103
	s_lshl_b32 s0, s46, 13
	s_add_i32 s0, s0, 0
	s_add_u32 s38, s40, s38
	v_fma_f32 v129, -v103, v128, 1.0
	v_fmac_f32_e32 v128, v129, v128
	v_div_scale_f32 v129, vcc, 1.0, v102, 1.0
	v_mul_f32_e32 v130, v129, v128
	v_fma_f32 v131, -v103, v130, v129
	v_fmac_f32_e32 v130, v131, v128
	v_fma_f32 v103, -v103, v130, v129
	v_div_fmas_f32 v103, v103, v128, v130
	v_div_fixup_f32 v102, v103, v102, 1.0
	v_pk_mul_f32 v[114:115], v[114:115], v[102:103] op_sel_hi:[1,0]
	v_pk_mul_f32 v[112:113], v[112:113], v[102:103] op_sel_hi:[1,0]
	v_pk_fma_f32 v[114:115], v[124:125], v[114:115], v[120:121]
	v_pk_fma_f32 v[112:113], v[126:127], v[112:113], v[122:123]
	v_cvt_pk_bf16_f32 v124, v114, v115
	s_addc_u32 s39, s44, s39
	v_lshlrev_b32_e32 v103, 16, v124
	v_sub_f32_e32 v103, v114, v103
	v_and_b32_e32 v120, 0xffff0000, v124
	v_cvt_pk_bf16_f32 v125, v112, v113
	v_sub_f32_e32 v120, v115, v120
	v_cvt_pk_bf16_f32 v126, v103, v120
	v_mov_b32_e32 v103, 0
	v_cvt_pk_fp8_f32 v103, v114, v115
	v_lshlrev_b32_e32 v121, 16, v125
	v_and_b32_e32 v122, 0xffff0000, v125
	v_sub_f32_e32 v121, v112, v121
	v_cvt_pk_fp8_f32 v103, v112, v113 op_sel:[0,0,1]
	v_sub_f32_e32 v122, v113, v122
	v_cvt_pk_bf16_f32 v127, v121, v122
	v_and_b32_e32 v130, 0x1f0, v146
	global_store_dword v150, v103, s[38:39]
	global_load_dwordx4 v[112:115], v[118:119], off offset:1024
	global_load_dwordx4 v[120:123], v[116:117], off offset:1024
	v_mov_b32_e32 v103, 0x1f0
	v_bitop3_b32 v128, s5, v146, v103 bitop3:0x78
	v_and_b32_e32 v103, 8, v146
	v_pk_mul_f32 v[110:111], v[110:111], v[102:103] op_sel_hi:[1,0]
	v_pk_mul_f32 v[108:109], v[108:109], v[102:103] op_sel_hi:[1,0]
	v_add3_u32 v159, s0, v128, v103
	v_add_u32_e32 v160, 0x10000, v159
	ds_write_b64 v159, v[124:125]
	ds_write_b64 v160, v[126:127]
	v_pk_mul_f32 v[106:107], v[106:107], v[102:103] op_sel_hi:[1,0]
	v_pk_mul_f32 v[104:105], v[104:105], v[102:103] op_sel_hi:[1,0]
	v_mov_b32_e32 v124, 0x200
	v_bitop3_b32 v124, v130, s5, v124 bitop3:0x36
	v_add3_u32 v161, s0, v124, v103
	v_add_u32_e32 v162, 0x10000, v161
	v_pk_mul_f32 v[72:73], v[72:73], v[102:103] op_sel_hi:[1,0]
	v_pk_mul_f32 v[70:71], v[70:71], v[102:103] op_sel_hi:[1,0]
	v_pk_mul_f32 v[68:69], v[68:69], v[102:103] op_sel_hi:[1,0]
	v_pk_mul_f32 v[66:67], v[66:67], v[102:103] op_sel_hi:[1,0]
	v_and_b32_e32 v125, 0xffff0000, v88
	v_and_b32_e32 v124, 0xffff0000, v86
	v_pk_mul_f32 v[100:101], v[100:101], v[102:103] op_sel_hi:[1,0]
	v_pk_mul_f32 v[98:99], v[98:99], v[102:103] op_sel_hi:[1,0]
	v_pk_mul_f32 v[96:97], v[96:97], v[102:103] op_sel_hi:[1,0]
	v_pk_mul_f32 v[94:95], v[94:95], v[102:103] op_sel_hi:[1,0]
	v_pk_mul_f32 v[92:93], v[92:93], v[102:103] op_sel_hi:[1,0]
	v_pk_mul_f32 v[90:91], v[90:91], v[102:103] op_sel_hi:[1,0]
	s_waitcnt vmcnt(1)
	v_pk_add_f32 v[114:115], v[114:115], 1.0 op_sel_hi:[1,0]
	v_pk_add_f32 v[112:113], v[112:113], 1.0 op_sel_hi:[1,0]
	s_waitcnt vmcnt(0)
	v_pk_fma_f32 v[108:109], v[114:115], v[108:109], v[122:123]
	v_pk_fma_f32 v[110:111], v[112:113], v[110:111], v[120:121]
	v_mov_b32_e32 v114, 0
	v_cvt_pk_fp8_f32 v114, v110, v111
	v_cvt_pk_bf16_f32 v120, v110, v111
	v_cvt_pk_bf16_f32 v121, v108, v109
	v_cvt_pk_fp8_f32 v114, v108, v109 op_sel:[0,0,1]
	v_lshlrev_b32_e32 v112, 16, v120
	v_and_b32_e32 v113, 0xffff0000, v120
	v_sub_f32_e32 v112, v110, v112
	v_sub_f32_e32 v113, v111, v113
	v_lshlrev_b32_e32 v110, 16, v121
	v_and_b32_e32 v111, 0xffff0000, v121
	v_sub_f32_e32 v110, v108, v110
	v_sub_f32_e32 v108, v109, v111
	v_cvt_pk_bf16_f32 v122, v112, v113
	v_cvt_pk_bf16_f32 v123, v110, v108
	global_store_dword v150, v114, s[38:39] offset:256
	global_load_dwordx4 v[108:111], v[118:119], off offset:2048
	s_nop 0
	global_load_dwordx4 v[112:115], v[116:117], off offset:2048
	ds_write_b64 v161, v[120:121]
	ds_write_b64 v162, v[122:123]
	v_mov_b32_e32 v120, 0x400
	v_bitop3_b32 v120, v130, s5, v120 bitop3:0x36
	v_add3_u32 v165, s0, v120, v103
	v_add_u32_e32 v166, 0x10000, v165
	v_lshlrev_b32_e32 v123, 16, v88
	v_lshlrev_b32_e32 v122, 16, v86
	v_and_b32_e32 v121, 0xffff0000, v89
	v_and_b32_e32 v120, 0xffff0000, v87
	v_pk_add_f32 v[136:137], v[122:123], v[124:125]
	v_mov_b32_e32 v88, 0
	s_waitcnt vmcnt(1)
	v_pk_add_f32 v[110:111], v[110:111], 1.0 op_sel_hi:[1,0]
	v_pk_add_f32 v[108:109], v[108:109], 1.0 op_sel_hi:[1,0]
	s_waitcnt vmcnt(0)
	v_pk_fma_f32 v[104:105], v[110:111], v[104:105], v[114:115]
	v_pk_fma_f32 v[106:107], v[108:109], v[106:107], v[112:113]
	v_mov_b32_e32 v110, 0
	v_cvt_pk_fp8_f32 v110, v106, v107
	v_cvt_pk_bf16_f32 v112, v106, v107
	v_cvt_pk_bf16_f32 v113, v104, v105
	v_cvt_pk_fp8_f32 v110, v104, v105 op_sel:[0,0,1]
	v_lshlrev_b32_e32 v108, 16, v112
	v_and_b32_e32 v109, 0xffff0000, v112
	v_sub_f32_e32 v108, v106, v108
	v_sub_f32_e32 v109, v107, v109
	v_lshlrev_b32_e32 v106, 16, v113
	v_and_b32_e32 v107, 0xffff0000, v113
	v_sub_f32_e32 v106, v104, v106
	v_sub_f32_e32 v104, v105, v107
	v_cvt_pk_bf16_f32 v114, v108, v109
	v_cvt_pk_bf16_f32 v115, v106, v104
	global_store_dword v150, v110, s[38:39] offset:512
	global_load_dwordx4 v[104:107], v[118:119], off offset:3072
	s_nop 0
	global_load_dwordx4 v[108:111], v[116:117], off offset:3072
	ds_write_b64 v165, v[112:113]
	ds_write_b64 v166, v[114:115]
	s_waitcnt vmcnt(1)
; #define LAS __attribute__((address_space(3)))
; __device__ __forceinline__ unsigned cvt_pk_bf16(float lo, float hi) { unsigned r; asm volatile("v_cvt_pk_bf16_f32 %0, %1, %2" : "=v"(r) : "v"(lo), "v"(hi)); return r; }
; __device__ __forceinline__ unsigned pk4_fp8(float a, float b, float c, float d) { int w = 0; w = __builtin_amdgcn_cvt_pk_fp8_f32(a, b, w, false); w = __builtin_amdgcn_cvt_pk_fp8_f32(c, d, w, true); return (unsigned)w; }
; __device__ __forceinline__ float bf_lo(unsigned w) { return __uint_as_float(w << 16); }
; __device__ __forceinline__ float bf_hi(unsigned w) { return __uint_as_float(w & 0xffff0000u); }
; __device__ __forceinline__ void p6_router(Frame& F) {
;     ...
;                 const int t = ta + q; f32x4 v[8]; float s = 0.f;
; #pragma unroll
;                 for (int j = 0; j < 8; ++j) { const u32x2 zb = zr[q][j]; v[j] = (f32x4){bf_lo(zb.x), bf_hi(zb.x), bf_lo(zb.y), bf_hi(zb.y)}; s += (v[j][0] + v[j][1]) + (v[j][2] + v[j][3]); }
;                 float mean = wave_sum(s) * (1.f / DM), s2 = 0.f;
;     ...
; #pragma unroll
;                 for (int j = 0; j < 8; ++j) { const f32x4 sh = ((const f32x4*)(mod + (size_t)b * 12288 + 6144))[loq + 64 * j], sc = ((const f32x4*)(mod + (size_t)b * 12288 + 8192))[loq + 64 * j];
;                     const f32x4 y = v[j] * rstd * (sc + 1.0f) + sh;
;                     u32x2 wh; wh.x = cvt_pk_bf16(y[0], y[1]); wh.y = cvt_pk_bf16(y[2], y[3]);
;                     const f32x4 yl = {y[0] - bf_lo(wh.x), y[1] - bf_hi(wh.x), y[2] - bf_lo(wh.y), y[3] - bf_hi(wh.y)};
;                     u32x2 wl; wl.x = cvt_pk_bf16(yl[0], yl[1]); wl.y = cvt_pk_bf16(yl[2], yl[3]);
;                     { const int r = 2 * wave + q; LAS unsigned char* rowp = F.lds + r * 4096 + ((((lane >> 1) + 32 * j) ^ r) << 4) + (lane & 1) * 8;
;                       *(LAS u32x2*)rowp = wh; *(LAS u32x2*)(rowp + 65536) = wl; }
;                     U2F[(size_t)t * (DM / 4) + lane + 64 * j] = pk4_fp8(y[0], y[1], y[2], y[3]); }
	v_pk_add_f32 v[106:107], v[106:107], 1.0 op_sel_hi:[1,0]
	v_pk_add_f32 v[104:105], v[104:105], 1.0 op_sel_hi:[1,0]
	s_waitcnt vmcnt(0)
	v_pk_fma_f32 v[70:71], v[70:71], v[106:107], v[110:111]
	v_pk_fma_f32 v[72:73], v[72:73], v[104:105], v[108:109]
	v_mov_b32_e32 v106, 0
	v_cvt_pk_fp8_f32 v106, v72, v73
	v_cvt_pk_bf16_f32 v112, v72, v73
	v_cvt_pk_bf16_f32 v113, v70, v71
	v_cvt_pk_fp8_f32 v106, v70, v71 op_sel:[0,0,1]
	v_lshlrev_b32_e32 v104, 16, v112
	v_sub_f32_e32 v104, v72, v104
	v_and_b32_e32 v105, 0xffff0000, v112
	v_sub_f32_e32 v105, v73, v105
	v_cvt_pk_bf16_f32 v114, v104, v105
	v_add_co_u32_e32 v104, vcc, s41, v118
	v_lshlrev_b32_e32 v72, 16, v113
	v_and_b32_e32 v73, 0xffff0000, v113
	v_addc_co_u32_e32 v105, vcc, 0, v119, vcc
	v_sub_f32_e32 v72, v70, v72
	v_sub_f32_e32 v70, v71, v73
	v_cvt_pk_bf16_f32 v115, v72, v70
	global_store_dword v150, v106, s[38:39] offset:768
	v_add_co_u32_e32 v106, vcc, s41, v116
	global_load_dwordx4 v[70:73], v[104:105], off
	s_nop 0
	v_addc_co_u32_e32 v107, vcc, 0, v117, vcc
	global_load_dwordx4 v[108:111], v[106:107], off
	v_mov_b32_e32 v117, 0
	v_mov_b32_e32 v116, 0x600
	v_bitop3_b32 v116, v130, s5, v116 bitop3:0x36
	v_add3_u32 v155, s0, v116, v103
	v_add_u32_e32 v156, 0x10000, v155
	ds_write_b64 v155, v[112:113]
	ds_write_b64 v156, v[114:115]
	v_lshlrev_b32_e32 v119, 16, v89
	v_lshlrev_b32_e32 v118, 16, v87
	v_lshlrev_b32_e32 v116, 16, v84
	v_lshlrev_b32_e32 v112, 16, v82
	v_and_b32_e32 v113, 0xffff0000, v82
	v_lshlrev_b32_e32 v114, 16, v83
	v_and_b32_e32 v115, 0xffff0000, v83
	v_and_b32_e32 v89, 0xffff0000, v80
	v_and_b32_e32 v87, 0xffff0000, v81
	v_lshlrev_b32_e32 v82, 16, v77
	v_and_b32_e32 v83, 0xffff0000, v77
	v_pk_add_f32 v[138:139], v[118:119], v[120:121]
	v_lshlrev_b32_e32 v84, 16, v78
	v_and_b32_e32 v77, 0xffff0000, v74
	v_pk_add_f32 v[136:137], v[136:137], v[138:139]
	v_add_f32_e32 v86, v114, v115
	s_waitcnt vmcnt(1)
	v_pk_add_f32 v[70:71], v[70:71], 1.0 op_sel_hi:[1,0]
	v_pk_add_f32 v[72:73], v[72:73], 1.0 op_sel_hi:[1,0]
	s_waitcnt vmcnt(0)
	v_pk_fma_f32 v[68:69], v[68:69], v[70:71], v[108:109]
	s_nop 0
	v_cvt_pk_fp8_f32 v117, v68, v69
	v_pk_fma_f32 v[66:67], v[66:67], v[72:73], v[110:111]
	v_cvt_pk_bf16_f32 v126, v68, v69
	v_lshlrev_b32_e32 v111, 16, v80
	v_cvt_pk_fp8_f32 v117, v66, v67 op_sel:[0,0,1]
	v_cvt_pk_bf16_f32 v127, v66, v67
	v_lshlrev_b32_e32 v70, 16, v126
	v_and_b32_e32 v71, 0xffff0000, v126
	v_lshlrev_b32_e32 v72, 16, v127
	v_and_b32_e32 v73, 0xffff0000, v127
	v_sub_f32_e32 v68, v68, v70
	v_sub_f32_e32 v69, v69, v71
	v_sub_f32_e32 v70, v66, v72
	v_sub_f32_e32 v66, v67, v73
	v_cvt_pk_bf16_f32 v128, v68, v69
	v_cvt_pk_bf16_f32 v129, v70, v66
	global_store_dword v150, v117, s[38:39] offset:1024
	global_load_dwordx4 v[70:73], v[104:105], off offset:1024
	global_load_dwordx4 v[66:69], v[106:107], off offset:1024
	v_lshlrev_b32_e32 v117, 16, v85
	v_lshlrev_b32_e32 v109, 16, v81
	v_lshlrev_b32_e32 v80, 16, v76
	v_and_b32_e32 v81, 0xffff0000, v76
	v_lshlrev_b32_e32 v85, 16, v79
	v_lshlrev_b32_e32 v76, 16, v74
	v_lshlrev_b32_e32 v79, 16, v75
	v_and_b32_e32 v75, 0xffff0000, v75
	v_pk_add_f32 v[140:141], v[116:117], v[132:133]
	v_add_f32_e32 v78, v80, v81
	v_add_f32_e32 v74, v82, v83
	v_pk_add_f32 v[138:139], v[140:141], v[140:141] op_sel:[0,1] op_sel_hi:[1,0]
	v_pk_add_f32 v[168:169], v[78:79], v[74:75]
	v_add_f32_e32 v74, 0, v136
	v_add_f32_e32 v108, v112, v113
	v_mov_b32_e32 v139, v89
	v_add_f32_e32 v110, v74, v137
	v_pk_add_f32 v[140:141], v[108:109], v[86:87]
	v_pk_add_f32 v[136:137], v[110:111], v[138:139]
	v_pk_add_f32 v[152:153], v[84:85], v[134:135]
	v_pk_add_f32 v[136:137], v[136:137], v[140:141]
	v_pk_add_f32 v[152:153], v[152:153], v[152:153] op_sel:[0,1] op_sel_hi:[1,0]
	v_pk_add_f32 v[136:137], v[136:137], v[136:137] op_sel:[0,1] op_sel_hi:[1,0]
	v_mov_b32_e32 v153, v77
	v_mov_b32_e32 v137, v76
	v_pk_add_f32 v[136:137], v[136:137], v[152:153]
	v_mov_b32_e32 v86, 0x800
	v_pk_add_f32 v[136:137], v[136:137], v[168:169]
	v_bitop3_b32 v86, v130, s5, v86 bitop3:0x36
	v_add_f32_e32 v74, v136, v137
	ds_bpermute_b32 v78, v1, v74
	v_add3_u32 v169, s0, v86, v103
	v_add_u32_e32 v171, 0x10000, v169
	ds_write_b64 v169, v[126:127]
	ds_write_b64 v171, v[128:129]
	s_waitcnt lgkmcnt(2)
	v_add_f32_e32 v74, v74, v78
	ds_bpermute_b32 v78, v142, v74
	s_waitcnt lgkmcnt(0)
	v_add_f32_e32 v74, v74, v78
	ds_bpermute_b32 v78, v143, v74
	s_waitcnt lgkmcnt(0)
	v_add_f32_e32 v74, v74, v78
	s_waitcnt vmcnt(1)
	v_pk_add_f32 v[70:71], v[70:71], 1.0 op_sel_hi:[1,0]
	s_waitcnt vmcnt(0)
	v_pk_fma_f32 v[66:67], v[100:101], v[70:71], v[66:67]
	v_pk_add_f32 v[72:73], v[72:73], 1.0 op_sel_hi:[1,0]
	v_cvt_pk_fp8_f32 v88, v66, v67
	v_pk_fma_f32 v[68:69], v[98:99], v[72:73], v[68:69]
	v_cvt_pk_bf16_f32 v72, v66, v67
	s_nop 0
	v_cvt_pk_fp8_f32 v88, v68, v69 op_sel:[0,0,1]
	v_cvt_pk_bf16_f32 v73, v68, v69
	v_lshlrev_b32_e32 v70, 16, v72
	v_and_b32_e32 v71, 0xffff0000, v72
	v_lshlrev_b32_e32 v78, 16, v73
	v_and_b32_e32 v86, 0xffff0000, v73
	v_sub_f32_e32 v66, v66, v70
	v_sub_f32_e32 v67, v67, v71
	v_sub_f32_e32 v70, v68, v78
	v_sub_f32_e32 v68, v69, v86
	v_cvt_pk_bf16_f32 v126, v66, v67
	v_cvt_pk_bf16_f32 v127, v70, v68
	global_store_dword v150, v88, s[38:39] offset:1280
	global_load_dwordx4 v[68:71], v[104:105], off offset:2048
	global_load_dwordx4 v[98:101], v[106:107], off offset:2048
	ds_bpermute_b32 v66, v144, v74
	v_mov_b32_e32 v86, 0
	s_waitcnt lgkmcnt(0)
	v_add_f32_e32 v66, v74, v66
	ds_bpermute_b32 v67, v145, v66
	v_mov_b32_e32 v74, 0xa00
	v_bitop3_b32 v74, v130, s5, v74 bitop3:0x36
	v_add3_u32 v152, s0, v74, v103
	v_add_u32_e32 v153, 0x10000, v152
	s_waitcnt lgkmcnt(0)
; #define LAS __attribute__((address_space(3)))
; __device__ __forceinline__ unsigned cvt_pk_bf16(float lo, float hi) { unsigned r; asm volatile("v_cvt_pk_bf16_f32 %0, %1, %2" : "=v"(r) : "v"(lo), "v"(hi)); return r; }
; __device__ __forceinline__ unsigned pk4_fp8(float a, float b, float c, float d) { int w = 0; w = __builtin_amdgcn_cvt_pk_fp8_f32(a, b, w, false); w = __builtin_amdgcn_cvt_pk_fp8_f32(c, d, w, true); return (unsigned)w; }
; __device__ __forceinline__ float bf_lo(unsigned w) { return __uint_as_float(w << 16); }
; __device__ __forceinline__ float bf_hi(unsigned w) { return __uint_as_float(w & 0xffff0000u); }
; __device__ __forceinline__ void p6_router(Frame& F) {
;     ...
;                 float mean = wave_sum(s) * (1.f / DM), s2 = 0.f;
; #pragma unroll
;                 for (int j = 0; j < 8; ++j) { v[j] = v[j] - mean; s2 += (v[j][0] * v[j][0] + v[j][1] * v[j][1]) + (v[j][2] * v[j][2] + v[j][3] * v[j][3]); }
;                 float rstd = 1.f / sqrtf(wave_sum(s2) * (1.f / DM) + LN_EPS);
;     ...
; #pragma unroll
;                 for (int j = 0; j < 8; ++j) { const f32x4 sh = ((const f32x4*)(mod + (size_t)b * 12288 + 6144))[loq + 64 * j], sc = ((const f32x4*)(mod + (size_t)b * 12288 + 8192))[loq + 64 * j];
;                     const f32x4 y = v[j] * rstd * (sc + 1.0f) + sh;
;                     u32x2 wh; wh.x = cvt_pk_bf16(y[0], y[1]); wh.y = cvt_pk_bf16(y[2], y[3]);
;                     const f32x4 yl = {y[0] - bf_lo(wh.x), y[1] - bf_hi(wh.x), y[2] - bf_lo(wh.y), y[3] - bf_hi(wh.y)};
;                     u32x2 wl; wl.x = cvt_pk_bf16(yl[0], yl[1]); wl.y = cvt_pk_bf16(yl[2], yl[3]);
;                     { const int r = 2 * wave + q; LAS unsigned char* rowp = F.lds + r * 4096 + ((((lane >> 1) + 32 * j) ^ r) << 4) + (lane & 1) * 8;
;                       *(LAS u32x2*)rowp = wh; *(LAS u32x2*)(rowp + 65536) = wl; }
;                     U2F[(size_t)t * (DM / 4) + lane + 64 * j] = pk4_fp8(y[0], y[1], y[2], y[3]); }
	v_add_f32_e32 v66, v66, v67
	ds_bpermute_b32 v67, v147, v66
	ds_write_b64 v152, v[72:73]
	ds_write_b64 v153, v[126:127]
	s_waitcnt lgkmcnt(2)
	v_add_f32_e32 v88, v66, v67
	v_fmac_f32_e32 v112, 0xba000000, v88
	v_fmac_f32_e32 v114, 0xba000000, v88
	v_fmac_f32_e32 v113, 0xba000000, v88
	v_fmac_f32_e32 v115, 0xba000000, v88
	v_mul_f32_e32 v74, v112, v112
	v_mul_f32_e32 v78, v114, v114
	v_pk_fma_f32 v[140:141], v[112:113], v[112:113], v[74:75] op_sel_hi:[1,1,0]
	v_pk_fma_f32 v[172:173], v[114:115], v[114:115], v[78:79] op_sel_hi:[1,1,0]
	v_fmac_f32_e32 v120, 0xba000000, v88
	v_fmac_f32_e32 v124, 0xba000000, v88
	v_fmac_f32_e32 v121, 0xba000000, v88
	v_fmac_f32_e32 v125, 0xba000000, v88
	v_fmac_f32_e32 v132, 0xba000000, v88
	v_fmac_f32_e32 v133, 0xba000000, v88
	v_fmac_f32_e32 v117, 0xba000000, v88
	v_fmac_f32_e32 v118, 0xba000000, v88
	v_fmac_f32_e32 v122, 0xba000000, v88
	v_fmac_f32_e32 v119, 0xba000000, v88
	v_fmac_f32_e32 v123, 0xba000000, v88
	v_fmac_f32_e32 v116, 0xba000000, v88
	v_fmac_f32_e32 v134, 0xba000000, v88
	v_fmac_f32_e32 v135, 0xba000000, v88
	v_fmac_f32_e32 v85, 0xba000000, v88
	v_pk_mul_f32 v[128:129], v[124:125], v[124:125]
	v_pk_mul_f32 v[136:137], v[120:121], v[120:121]
	v_mov_b32_e32 v138, v117
	v_mov_b32_e32 v139, v133
	v_mov_b32_e32 v117, v132
	v_mov_b32_e32 v66, v85
	v_mov_b32_e32 v67, v135
	v_mov_b32_e32 v85, v134
	v_pk_fma_f32 v[128:129], v[122:123], v[122:123], v[128:129]
	v_pk_fma_f32 v[132:133], v[118:119], v[118:119], v[136:137]
	v_pk_mul_f32 v[134:135], v[138:139], v[138:139]
	v_pk_mul_f32 v[136:137], v[116:117], v[116:117]
	v_pk_add_f32 v[128:129], v[128:129], v[132:133]
	v_pk_mov_b32 v[132:133], v[136:137], v[134:135] op_sel:[1,0]
	v_mov_b32_e32 v137, v135
	v_pk_add_f32 v[132:133], v[132:133], v[136:137]
	v_fmac_f32_e32 v87, 0xba000000, v88
	v_fmac_f32_e32 v109, 0xba000000, v88
	v_fmac_f32_e32 v89, 0xba000000, v88
	v_fmac_f32_e32 v111, 0xba000000, v88
	v_fmac_f32_e32 v84, 0xba000000, v88
	v_pk_add_f32 v[128:129], v[128:129], v[128:129] op_sel_hi:[0,1]
	v_pk_add_f32 v[132:133], v[132:133], v[132:133] op_sel_hi:[0,1]
	v_pk_mul_f32 v[174:175], v[66:67], v[66:67]
	v_pk_mul_f32 v[176:177], v[84:85], v[84:85]
	v_mul_f32_e32 v140, v111, v111
	v_mul_f32_e32 v172, v89, v89
	v_mul_f32_e32 v128, v87, v87
	v_mul_f32_e32 v132, v109, v109
	v_fmac_f32_e32 v80, 0xba000000, v88
	v_pk_mov_b32 v[134:135], v[176:177], v[174:175] op_sel:[1,0]
	v_pk_add_f32 v[136:137], v[140:141], v[172:173]
	v_pk_add_f32 v[128:129], v[132:133], v[128:129]
	v_mov_b32_e32 v177, v175
	v_fmac_f32_e32 v81, 0xba000000, v88
	v_fmac_f32_e32 v82, 0xba000000, v88
	v_pk_add_f32 v[128:129], v[136:137], v[128:129]
	s_waitcnt vmcnt(1)
	v_pk_add_f32 v[68:69], v[68:69], 1.0 op_sel_hi:[1,0]
	v_pk_add_f32 v[70:71], v[70:71], 1.0 op_sel_hi:[1,0]
	s_waitcnt vmcnt(0)
	v_pk_fma_f32 v[68:69], v[96:97], v[68:69], v[98:99]
	v_pk_fma_f32 v[70:71], v[94:95], v[70:71], v[100:101]
	v_cvt_pk_fp8_f32 v86, v68, v69
	v_cvt_pk_bf16_f32 v72, v68, v69
	v_cvt_pk_bf16_f32 v73, v70, v71
	v_pk_add_f32 v[100:101], v[134:135], v[176:177]
	v_cvt_pk_fp8_f32 v86, v70, v71 op_sel:[0,0,1]
	v_lshlrev_b32_e32 v74, 16, v72
	v_and_b32_e32 v78, 0xffff0000, v72
	v_lshlrev_b32_e32 v94, 16, v73
	v_and_b32_e32 v95, 0xffff0000, v73
	v_sub_f32_e32 v68, v68, v74
	v_sub_f32_e32 v69, v69, v78
	v_sub_f32_e32 v74, v70, v94
	v_sub_f32_e32 v70, v71, v95
	v_cvt_pk_bf16_f32 v98, v68, v69
	v_cvt_pk_bf16_f32 v99, v74, v70
	global_store_dword v150, v86, s[38:39] offset:1536
	global_load_dwordx4 v[68:71], v[106:107], off offset:3072
	global_load_dwordx4 v[94:97], v[104:105], off offset:3072
	v_mul_f32_e32 v74, v80, v80
	v_fmac_f32_e32 v83, 0xba000000, v88
	v_pk_fma_f32 v[104:105], v[80:81], v[80:81], v[74:75] op_sel_hi:[1,1,0]
	v_mul_f32_e32 v74, v82, v82
	v_pk_add_f32 v[128:129], v[128:129], v[128:129] op_sel_hi:[0,1]
	v_pk_add_f32 v[100:101], v[100:101], v[100:101] op_sel_hi:[0,1]
	v_pk_fma_f32 v[106:107], v[82:83], v[82:83], v[74:75] op_sel_hi:[1,1,0]
	v_fmac_f32_e32 v75, 0xba000000, v88
	v_fmac_f32_e32 v79, 0xba000000, v88
	v_fmac_f32_e32 v77, 0xba000000, v88
	v_fmac_f32_e32 v76, 0xba000000, v88
	v_mul_f32_e32 v104, v76, v76
	v_mul_f32_e32 v106, v77, v77
	v_mul_f32_e32 v100, v79, v79
	v_mul_f32_e32 v128, v75, v75
	v_pk_add_f32 v[104:105], v[104:105], v[106:107]
	v_pk_add_f32 v[100:101], v[100:101], v[128:129]
	v_mov_b32_e32 v86, 0xc00
	v_pk_add_f32 v[100:101], v[104:105], v[100:101]
	v_mov_b32_e32 v88, 0xe00
	v_add_f32_e32 v74, v100, v101
	ds_bpermute_b32 v78, v1, v74
	v_bitop3_b32 v86, v130, s5, v86 bitop3:0x36
	v_bitop3_b32 v88, v130, s5, v88 bitop3:0x36
	v_add3_u32 v163, s0, v86, v103
	v_add3_u32 v157, s0, v88, v103
	s_waitcnt lgkmcnt(0)
	v_add_f32_e32 v74, v74, v78
	ds_bpermute_b32 v78, v142, v74
	v_add_u32_e32 v164, 0x10000, v163
	ds_write_b64 v163, v[72:73]
	ds_write_b64 v164, v[98:99]
	v_mov_b32_e32 v105, 0
	v_add_u32_e32 v158, 0x10000, v157
	s_waitcnt lgkmcnt(2)
	v_add_f32_e32 v74, v74, v78
	ds_bpermute_b32 v78, v143, v74
	v_mov_b32_e32 v100, v123
	v_mov_b32_e32 v123, v124
	v_mov_b32_e32 v101, v125
	v_mov_b32_e32 v104, v119
	s_waitcnt lgkmcnt(0)
	v_add_f32_e32 v74, v74, v78
	ds_bpermute_b32 v78, v144, v74
	v_mov_b32_e32 v119, v120
	s_waitcnt lgkmcnt(0)
	v_add_f32_e32 v74, v74, v78
	ds_bpermute_b32 v78, v145, v74
	s_waitcnt lgkmcnt(0)
	v_add_f32_e32 v74, v74, v78
	ds_bpermute_b32 v78, v147, v74
	s_waitcnt lgkmcnt(0)
	v_add_f32_e32 v74, v74, v78
	v_fmamk_f32 v74, v74, 0x3a000000, v148
	v_mul_f32_e32 v78, 0x4f800000, v74
	v_cmp_gt_f32_e32 vcc, s45, v74
	s_waitcnt vmcnt(0)
; #define LAS __attribute__((address_space(3)))
; __device__ __forceinline__ unsigned cvt_pk_bf16(float lo, float hi) { unsigned r; asm volatile("v_cvt_pk_bf16_f32 %0, %1, %2" : "=v"(r) : "v"(lo), "v"(hi)); return r; }
; __device__ __forceinline__ unsigned pk4_fp8(float a, float b, float c, float d) { int w = 0; w = __builtin_amdgcn_cvt_pk_fp8_f32(a, b, w, false); w = __builtin_amdgcn_cvt_pk_fp8_f32(c, d, w, true); return (unsigned)w; }
; __device__ __forceinline__ float bf_lo(unsigned w) { return __uint_as_float(w << 16); }
; __device__ __forceinline__ float bf_hi(unsigned w) { return __uint_as_float(w & 0xffff0000u); }
; __device__ __forceinline__ void p6_router(Frame& F) {
;     ...
;                 float rstd = 1.f / sqrtf(wave_sum(s2) * (1.f / DM) + LN_EPS);
;                 s = 0.f;
; #pragma unroll
;                 for (int j = 0; j < 8; ++j) { v[j] = v[j] * rstd * pw[j] + pb[j]; { u32x2 xb; xb.x = cvt_pk_bf16(v[j][0], v[j][1]); xb.y = cvt_pk_bf16(v[j][2], v[j][3]); ((u32x2*)(X1 + (size_t)t * DM))[lane + 64 * j] = xb; } s += (v[j][0] + v[j][1]) + (v[j][2] + v[j][3]); }
;     ...
;                     const f32x4 y = v[j] * rstd * (sc + 1.0f) + sh;
;                     u32x2 wh; wh.x = cvt_pk_bf16(y[0], y[1]); wh.y = cvt_pk_bf16(y[2], y[3]);
;                     const f32x4 yl = {y[0] - bf_lo(wh.x), y[1] - bf_hi(wh.x), y[2] - bf_lo(wh.y), y[3] - bf_hi(wh.y)};
;                     u32x2 wl; wl.x = cvt_pk_bf16(yl[0], yl[1]); wl.y = cvt_pk_bf16(yl[2], yl[3]);
;                     { const int r = 2 * wave + q; LAS unsigned char* rowp = F.lds + r * 4096 + ((((lane >> 1) + 32 * j) ^ r) << 4) + (lane & 1) * 8;
;                       *(LAS u32x2*)rowp = wh; *(LAS u32x2*)(rowp + 65536) = wl; }
;                     U2F[(size_t)t * (DM / 4) + lane + 64 * j] = pk4_fp8(y[0], y[1], y[2], y[3]); }
	v_pk_add_f32 v[72:73], v[96:97], 1.0 op_sel_hi:[1,0]
	v_cndmask_b32_e32 v74, v74, v78, vcc
	v_sqrt_f32_e32 v78, v74
	v_pk_add_f32 v[94:95], v[94:95], 1.0 op_sel_hi:[1,0]
	v_pk_fma_f32 v[70:71], v[90:91], v[72:73], v[70:71]
	v_pk_fma_f32 v[68:69], v[92:93], v[94:95], v[68:69]
	v_add_u32_e32 v86, -1, v78
	v_add_u32_e32 v88, 1, v78
	v_fma_f32 v106, -v86, v78, v74
	v_fma_f32 v107, -v88, v78, v74
	v_cmp_ge_f32_e64 s[0:1], 0, v106
	v_cvt_pk_bf16_f32 v72, v68, v69
	v_cvt_pk_fp8_f32 v105, v68, v69
	v_cvt_pk_bf16_f32 v73, v70, v71
	v_cvt_pk_fp8_f32 v105, v70, v71 op_sel:[0,0,1]
	v_cndmask_b32_e64 v78, v78, v86, s[0:1]
	v_cmp_lt_f32_e64 s[0:1], 0, v107
	v_lshlrev_b32_e32 v90, 16, v73
	v_and_b32_e32 v91, 0xffff0000, v73
	v_cndmask_b32_e64 v78, v78, v88, s[0:1]
	v_mul_f32_e32 v86, 0x37800000, v78
	v_cndmask_b32_e32 v78, v78, v86, vcc
	v_lshlrev_b32_e32 v86, 16, v72
	v_and_b32_e32 v88, 0xffff0000, v72
	v_sub_f32_e32 v68, v68, v86
	v_sub_f32_e32 v69, v69, v88
	v_cvt_pk_bf16_f32 v68, v68, v69
	v_cmp_class_f32_e32 vcc, v74, v149
	v_sub_f32_e32 v86, v70, v90
	v_sub_f32_e32 v88, v71, v91
	v_cvt_pk_bf16_f32 v69, v86, v88
	ds_write_b64 v157, v[72:73]
	ds_write_b64 v158, v[68:69]
	v_cndmask_b32_e32 v68, v78, v74, vcc
	v_div_scale_f32 v69, s[0:1], v68, v68, 1.0
	v_rcp_f32_e32 v70, v69
	global_store_dword v150, v105, s[38:39] offset:1792
	v_mov_b32_e32 v105, v121
	v_mov_b32_e32 v88, v111
	v_fma_f32 v71, -v69, v70, 1.0
	v_fmac_f32_e32 v70, v71, v70
	v_div_scale_f32 v71, vcc, 1.0, v68, 1.0
	v_mul_f32_e32 v72, v71, v70
	v_fma_f32 v73, -v69, v72, v71
	v_fmac_f32_e32 v72, v73, v70
	v_fma_f32 v69, -v69, v72, v71
	v_div_fmas_f32 v69, v69, v70, v72
	v_div_fixup_f32 v68, v69, v68, 1.0
	v_pk_mul_f32 v[70:71], v[122:123], v[68:69] op_sel_hi:[1,0]
	v_pk_mul_f32 v[72:73], v[118:119], v[68:69] op_sel_hi:[1,0]
	v_pk_fma_f32 v[62:63], v[2:3], v[70:71], v[62:63]
	v_pk_mul_f32 v[2:3], v[100:101], v[68:69] op_sel_hi:[1,0]
	v_pk_fma_f32 v[64:65], v[4:5], v[72:73], v[64:65]
	v_pk_mul_f32 v[4:5], v[104:105], v[68:69] op_sel_hi:[1,0]
	v_pk_fma_f32 v[54:55], v[54:55], v[2:3], v[58:59]
	v_pk_fma_f32 v[56:57], v[56:57], v[4:5], v[60:61]
	v_mov_b32_e32 v2, v54
	v_mov_b32_e32 v3, v62
	v_mov_b32_e32 v4, v55
	v_mov_b32_e32 v5, v63
	v_pk_add_f32 v[2:3], v[2:3], v[4:5]
	v_mov_b32_e32 v4, v57
	v_mov_b32_e32 v5, v65
	v_mov_b32_e32 v58, v56
	v_mov_b32_e32 v59, v64
	v_pk_add_f32 v[4:5], v[4:5], v[58:59]
	v_pk_mul_f32 v[58:59], v[138:139], v[68:69] op_sel_hi:[1,0]
	v_pk_add_f32 v[2:3], v[2:3], v[4:5]
	v_pk_mul_f32 v[4:5], v[116:117], v[68:69] op_sel_hi:[1,0]
	v_pk_fma_f32 v[48:49], v[48:49], v[58:59], v[52:53]
	v_pk_fma_f32 v[46:47], v[46:47], v[4:5], v[50:51]
	v_mov_b32_e32 v5, v49
	v_mov_b32_e32 v4, v46
	v_pk_mov_b32 v[50:51], v[46:47], v[48:49] op_sel:[1,0]
	v_pk_mul_f32 v[52:53], v[114:115], v[68:69] op_sel_hi:[1,0]
	v_pk_add_f32 v[4:5], v[4:5], v[50:51]
	v_pk_mul_f32 v[50:51], v[112:113], v[68:69] op_sel_hi:[1,0]
	v_mov_b32_e32 v86, v109
	v_pk_fma_f32 v[40:41], v[40:41], v[52:53], v[44:45]
	v_pk_fma_f32 v[38:39], v[38:39], v[50:51], v[42:43]
	v_pk_mul_f32 v[50:51], v[88:89], v[68:69] op_sel_hi:[1,0]
	v_pk_mul_f32 v[52:53], v[86:87], v[68:69] op_sel_hi:[1,0]
	v_add_f32_e32 v3, 0, v3
	v_pk_add_f32 v[4:5], v[4:5], v[4:5] op_sel_hi:[0,1]
	v_pk_fma_f32 v[32:33], v[32:33], v[52:53], v[36:37]
	v_pk_fma_f32 v[30:31], v[30:31], v[50:51], v[34:35]
	v_add_f32_e32 v3, v2, v3
	v_add_f32_e32 v43, v38, v39
	v_add_f32_e32 v45, v41, v40
	v_mov_b32_e32 v42, v30
	v_mov_b32_e32 v44, v31
	v_mov_b32_e32 v4, v33
	v_mov_b32_e32 v2, v32
	v_pk_add_f32 v[34:35], v[42:43], v[44:45]
	v_pk_add_f32 v[2:3], v[4:5], v[2:3]
	v_pk_mul_f32 v[4:5], v[66:67], v[68:69] op_sel_hi:[1,0]
	v_pk_add_f32 v[2:3], v[34:35], v[2:3]
	v_pk_fma_f32 v[24:25], v[24:25], v[4:5], v[28:29]
	v_pk_add_f32 v[34:35], v[2:3], v[2:3] op_sel_hi:[0,1]
	v_pk_mul_f32 v[2:3], v[84:85], v[68:69] op_sel_hi:[1,0]
	v_mov_b32_e32 v74, v79
	v_pk_fma_f32 v[22:23], v[22:23], v[2:3], v[26:27]
	v_mov_b32_e32 v3, v25
	v_mov_b32_e32 v2, v22
	v_pk_mov_b32 v[4:5], v[22:23], v[24:25] op_sel:[1,0]
	s_add_u32 s0, s42, s36
	v_pk_add_f32 v[2:3], v[2:3], v[4:5]
	v_pk_mul_f32 v[4:5], v[82:83], v[68:69] op_sel_hi:[1,0]
	v_pk_add_f32 v[26:27], v[2:3], v[2:3] op_sel_hi:[0,1]
	v_pk_mul_f32 v[2:3], v[80:81], v[68:69] op_sel_hi:[1,0]
	v_pk_fma_f32 v[16:17], v[16:17], v[4:5], v[20:21]
	v_pk_fma_f32 v[14:15], v[14:15], v[2:3], v[18:19]
	v_pk_mul_f32 v[4:5], v[76:77], v[68:69] op_sel_hi:[1,0]
	v_pk_mul_f32 v[2:3], v[74:75], v[68:69] op_sel_hi:[1,0]
	v_pk_fma_f32 v[4:5], v[6:7], v[4:5], v[10:11]
	v_pk_fma_f32 v[2:3], v[8:9], v[2:3], v[12:13]
	v_add_f32_e32 v19, v14, v15
	v_add_f32_e32 v21, v17, v16
	v_mov_b32_e32 v18, v4
	v_mov_b32_e32 v20, v5
	v_mov_b32_e32 v26, v3
	v_mov_b32_e32 v34, v2
	v_pk_add_f32 v[6:7], v[18:19], v[20:21]
	v_pk_add_f32 v[8:9], v[26:27], v[34:35]
	s_addc_u32 s1, s43, s37
	v_pk_add_f32 v[6:7], v[6:7], v[8:9]
	v_cvt_pk_bf16_f32 v70, v62, v63
	v_cvt_pk_bf16_f32 v71, v64, v65
	global_store_dwordx2 v146, v[70:71], s[0:1]
	v_add_f32_e32 v7, v6, v7
	ds_bpermute_b32 v8, v1, v7
	v_cvt_pk_bf16_f32 v6, v54, v55
	s_mov_b32 s37, 0
	v_mov_b32_e32 v79, 0
	s_waitcnt lgkmcnt(0)
	v_add_f32_e32 v8, v7, v8
	ds_bpermute_b32 v9, v142, v8
	v_cvt_pk_bf16_f32 v7, v56, v57
	global_store_dwordx2 v146, v[6:7], s[0:1] offset:512
	v_cvt_pk_bf16_f32 v6, v46, v47
	v_cvt_pk_bf16_f32 v7, v48, v49
	s_waitcnt lgkmcnt(0)
	v_add_f32_e32 v8, v8, v9
	ds_bpermute_b32 v9, v143, v8
	global_store_dwordx2 v146, v[6:7], s[0:1] offset:1024
	v_cvt_pk_bf16_f32 v6, v38, v39
	v_cvt_pk_bf16_f32 v7, v40, v41
	global_store_dwordx2 v146, v[6:7], s[0:1] offset:1536
	s_waitcnt lgkmcnt(0)
; __device__ __forceinline__ unsigned cvt_pk_bf16(float lo, float hi) { unsigned r; asm volatile("v_cvt_pk_bf16_f32 %0, %1, %2" : "=v"(r) : "v"(lo), "v"(hi)); return r; }
; __device__ __forceinline__ void p6_router(Frame& F) {
;     ...
;                 for (int j = 0; j < 8; ++j) { v[j] = v[j] * rstd * pw[j] + pb[j]; { u32x2 xb; xb.x = cvt_pk_bf16(v[j][0], v[j][1]); xb.y = cvt_pk_bf16(v[j][2], v[j][3]); ((u32x2*)(X1 + (size_t)t * DM))[lane + 64 * j] = xb; } s += (v[j][0] + v[j][1]) + (v[j][2] + v[j][3]); }
;                 mean = wave_sum(s) * (1.f / DM); s2 = 0.f;
; #pragma unroll
;                 for (int j = 0; j < 8; ++j) { v[j] = v[j] - mean; s2 += (v[j][0] * v[j][0] + v[j][1] * v[j][1]) + (v[j][2] * v[j][2] + v[j][3] * v[j][3]); }
;                 rstd = 1.f / sqrtf(wave_sum(s2) * (1.f / DM) + LN_EPS);
;                 int loq = lane; asm volatile("" : "+v"(loq));
; #pragma unroll
;                 for (int j = 0; j < 8; ++j) { const f32x4 sh = ((const f32x4*)(mod + (size_t)b * 12288 + 6144))[loq + 64 * j], sc = ((const f32x4*)(mod + (size_t)b * 12288 + 8192))[loq + 64 * j];
	v_add_f32_e32 v8, v8, v9
	ds_bpermute_b32 v9, v144, v8
	v_cvt_pk_bf16_f32 v6, v30, v31
	v_cvt_pk_bf16_f32 v7, v32, v33
	global_store_dwordx2 v146, v[6:7], s[0:1] offset:2048
	v_cvt_pk_bf16_f32 v6, v22, v23
	s_waitcnt lgkmcnt(0)
	v_add_f32_e32 v8, v8, v9
	ds_bpermute_b32 v9, v145, v8
	v_cvt_pk_bf16_f32 v7, v24, v25
	global_store_dwordx2 v146, v[6:7], s[0:1] offset:2560
	v_cvt_pk_bf16_f32 v6, v14, v15
	v_cvt_pk_bf16_f32 v7, v16, v17
	s_waitcnt lgkmcnt(0)
	v_add_f32_e32 v8, v8, v9
	ds_bpermute_b32 v9, v147, v8
	global_store_dwordx2 v146, v[6:7], s[0:1] offset:3072
	v_cvt_pk_bf16_f32 v6, v4, v5
	v_cvt_pk_bf16_f32 v7, v2, v3
	global_store_dwordx2 v146, v[6:7], s[0:1] offset:3584
	s_waitcnt lgkmcnt(0)
	v_add_f32_e32 v18, v8, v9
	v_fmamk_f32 v63, v18, 0xba000000, v63
	v_fmamk_f32 v55, v18, 0xba000000, v55
	v_fmamk_f32 v65, v18, 0xba000000, v65
	v_fmac_f32_e32 v62, 0xba000000, v18
	v_fmamk_f32 v57, v18, 0xba000000, v57
	v_fmac_f32_e32 v54, 0xba000000, v18
	v_mov_b32_e32 v8, v63
	v_mov_b32_e32 v9, v55
	v_fmac_f32_e32 v64, 0xba000000, v18
	v_fmac_f32_e32 v56, 0xba000000, v18
	v_mov_b32_e32 v6, v62
	v_mov_b32_e32 v7, v54
	v_pk_mul_f32 v[8:9], v[8:9], v[8:9]
	v_mov_b32_e32 v10, v65
	v_mov_b32_e32 v11, v57
	v_pk_fma_f32 v[6:7], v[6:7], v[6:7], v[8:9]
	v_mov_b32_e32 v8, v64
	v_mov_b32_e32 v9, v56
	v_pk_mul_f32 v[10:11], v[10:11], v[10:11]
	v_fmamk_f32 v47, v18, 0xba000000, v47
	v_pk_fma_f32 v[8:9], v[8:9], v[8:9], v[10:11]
	v_fmac_f32_e32 v46, 0xba000000, v18
	v_pk_add_f32 v[6:7], v[6:7], v[8:9]
	v_fmamk_f32 v49, v18, 0xba000000, v49
	v_fmac_f32_e32 v48, 0xba000000, v18
	v_pk_add_f32 v[6:7], v[6:7], v[6:7] op_sel_hi:[0,1]
	v_pk_mul_f32 v[8:9], v[48:49], v[48:49]
	v_pk_mul_f32 v[10:11], v[46:47], v[46:47]
	v_fmac_f32_e32 v38, 0xba000000, v18
	v_pk_mov_b32 v[12:13], v[10:11], v[8:9] op_sel:[1,0]
	v_mov_b32_e32 v11, v9
	v_fmamk_f32 v39, v18, 0xba000000, v39
	v_fmac_f32_e32 v40, 0xba000000, v18
	v_mul_f32_e32 v6, v38, v38
	v_pk_add_f32 v[8:9], v[12:13], v[10:11]
	v_fmamk_f32 v41, v18, 0xba000000, v41
	v_pk_fma_f32 v[10:11], v[38:39], v[38:39], v[6:7] op_sel_hi:[1,1,0]
	v_mul_f32_e32 v6, v40, v40
	v_pk_add_f32 v[8:9], v[8:9], v[8:9] op_sel_hi:[0,1]
	v_pk_fma_f32 v[12:13], v[40:41], v[40:41], v[6:7] op_sel_hi:[1,1,0]
	v_fmamk_f32 v33, v18, 0xba000000, v33
	v_fmac_f32_e32 v32, 0xba000000, v18
	v_fmamk_f32 v31, v18, 0xba000000, v31
	v_fmac_f32_e32 v30, 0xba000000, v18
	v_mul_f32_e32 v10, v30, v30
	v_mul_f32_e32 v12, v31, v31
	v_mul_f32_e32 v8, v32, v32
	v_mul_f32_e32 v6, v33, v33
	v_pk_add_f32 v[10:11], v[10:11], v[12:13]
	v_pk_add_f32 v[6:7], v[8:9], v[6:7]
	v_fmamk_f32 v23, v18, 0xba000000, v23
	v_fmac_f32_e32 v22, 0xba000000, v18
	v_fmamk_f32 v25, v18, 0xba000000, v25
	v_fmac_f32_e32 v24, 0xba000000, v18
	v_pk_add_f32 v[6:7], v[10:11], v[6:7]
	v_pk_mul_f32 v[8:9], v[24:25], v[24:25]
	v_pk_mul_f32 v[10:11], v[22:23], v[22:23]
	v_pk_add_f32 v[6:7], v[6:7], v[6:7] op_sel_hi:[0,1]
	v_pk_mov_b32 v[12:13], v[10:11], v[8:9] op_sel:[1,0]
	v_mov_b32_e32 v11, v9
	v_fmac_f32_e32 v14, 0xba000000, v18
	v_pk_add_f32 v[8:9], v[12:13], v[10:11]
	v_fmamk_f32 v15, v18, 0xba000000, v15
	v_fmac_f32_e32 v16, 0xba000000, v18
	v_mul_f32_e32 v6, v14, v14
	v_pk_add_f32 v[12:13], v[8:9], v[8:9] op_sel_hi:[0,1]
	v_fmamk_f32 v17, v18, 0xba000000, v17
	v_pk_fma_f32 v[8:9], v[14:15], v[14:15], v[6:7] op_sel_hi:[1,1,0]
	v_mul_f32_e32 v6, v16, v16
	v_pk_fma_f32 v[10:11], v[16:17], v[16:17], v[6:7] op_sel_hi:[1,1,0]
	v_fmamk_f32 v5, v18, 0xba000000, v5
	v_fmac_f32_e32 v4, 0xba000000, v18
	v_mul_f32_e32 v8, v4, v4
	v_mul_f32_e32 v10, v5, v5
	v_pk_add_f32 v[34:35], v[8:9], v[10:11]
	v_mov_b32_e32 v8, v170
	v_fmamk_f32 v3, v18, 0xba000000, v3
	v_ashrrev_i32_e32 v9, 31, v8
	v_lshlrev_b64 v[10:11], 4, v[8:9]
	v_lshl_add_u64 v[8:9], s[16:17], 0, v[10:11]
	v_fmac_f32_e32 v2, 0xba000000, v18
	v_lshl_add_u64 v[10:11], s[20:21], 0, v[10:11]
	global_load_dwordx4 v[18:21], v[8:9], off
	global_load_dwordx4 v[26:29], v[10:11], off
	v_mul_f32_e32 v12, v2, v2
	v_mul_f32_e32 v6, v3, v3
	v_pk_add_f32 v[6:7], v[12:13], v[6:7]
	s_waitcnt vmcnt(0)
	v_pk_add_f32 v[28:29], v[28:29], 1.0 op_sel_hi:[1,0]
	v_pk_add_f32 v[6:7], v[34:35], v[6:7]
	v_pk_add_f32 v[26:27], v[26:27], 1.0 op_sel_hi:[1,0]
	v_add_f32_e32 v6, v6, v7
	ds_bpermute_b32 v7, v1, v6
	s_waitcnt lgkmcnt(0)
	v_add_f32_e32 v6, v6, v7
	ds_bpermute_b32 v7, v142, v6
	s_waitcnt lgkmcnt(0)
	v_add_f32_e32 v6, v6, v7
	ds_bpermute_b32 v7, v143, v6
	s_waitcnt lgkmcnt(0)
	v_add_f32_e32 v6, v6, v7
	ds_bpermute_b32 v7, v144, v6
	s_waitcnt lgkmcnt(0)
	v_add_f32_e32 v6, v6, v7
	ds_bpermute_b32 v7, v145, v6
	s_waitcnt lgkmcnt(0)
	v_add_f32_e32 v6, v6, v7
	ds_bpermute_b32 v7, v147, v6
	s_waitcnt lgkmcnt(0)
; #define LAS __attribute__((address_space(3)))
; __device__ __forceinline__ unsigned cvt_pk_bf16(float lo, float hi) { unsigned r; asm volatile("v_cvt_pk_bf16_f32 %0, %1, %2" : "=v"(r) : "v"(lo), "v"(hi)); return r; }
; __device__ __forceinline__ unsigned pk4_fp8(float a, float b, float c, float d) { int w = 0; w = __builtin_amdgcn_cvt_pk_fp8_f32(a, b, w, false); w = __builtin_amdgcn_cvt_pk_fp8_f32(c, d, w, true); return (unsigned)w; }
; __device__ __forceinline__ float bf_lo(unsigned w) { return __uint_as_float(w << 16); }
; __device__ __forceinline__ float bf_hi(unsigned w) { return __uint_as_float(w & 0xffff0000u); }
; __device__ __forceinline__ void p6_router(Frame& F) {
;     ...
;                 rstd = 1.f / sqrtf(wave_sum(s2) * (1.f / DM) + LN_EPS);
;                 int loq = lane; asm volatile("" : "+v"(loq));
; #pragma unroll
;                 for (int j = 0; j < 8; ++j) { const f32x4 sh = ((const f32x4*)(mod + (size_t)b * 12288 + 6144))[loq + 64 * j], sc = ((const f32x4*)(mod + (size_t)b * 12288 + 8192))[loq + 64 * j];
;                     const f32x4 y = v[j] * rstd * (sc + 1.0f) + sh;
;                     u32x2 wh; wh.x = cvt_pk_bf16(y[0], y[1]); wh.y = cvt_pk_bf16(y[2], y[3]);
;                     const f32x4 yl = {y[0] - bf_lo(wh.x), y[1] - bf_hi(wh.x), y[2] - bf_lo(wh.y), y[3] - bf_hi(wh.y)};
;                     u32x2 wl; wl.x = cvt_pk_bf16(yl[0], yl[1]); wl.y = cvt_pk_bf16(yl[2], yl[3]);
;                     { const int r = 2 * wave + q; LAS unsigned char* rowp = F.lds + r * 4096 + ((((lane >> 1) + 32 * j) ^ r) << 4) + (lane & 1) * 8;
;                       *(LAS u32x2*)rowp = wh; *(LAS u32x2*)(rowp + 65536) = wl; }
;                     U2F[(size_t)t * (DM / 4) + lane + 64 * j] = pk4_fp8(y[0], y[1], y[2], y[3]); }
	v_add_f32_e32 v6, v6, v7
	v_fmamk_f32 v6, v6, 0x3a000000, v148
	v_mul_f32_e32 v7, 0x4f800000, v6
	v_cmp_gt_f32_e32 vcc, s45, v6
	s_nop 1
	v_cndmask_b32_e32 v6, v6, v7, vcc
	v_sqrt_f32_e32 v7, v6
	s_nop 0
	v_add_u32_e32 v12, -1, v7
	v_fma_f32 v13, -v12, v7, v6
	v_cmp_ge_f32_e64 s[0:1], 0, v13
	v_add_u32_e32 v13, 1, v7
	s_nop 0
	v_cndmask_b32_e64 v12, v7, v12, s[0:1]
	v_fma_f32 v7, -v13, v7, v6
	v_cmp_lt_f32_e64 s[0:1], 0, v7
	s_nop 1
	v_cndmask_b32_e64 v7, v12, v13, s[0:1]
	v_mul_f32_e32 v12, 0x37800000, v7
	v_cndmask_b32_e32 v7, v7, v12, vcc
	v_cmp_class_f32_e32 vcc, v6, v149
	s_nop 1
	v_cndmask_b32_e32 v6, v7, v6, vcc
	v_div_scale_f32 v7, s[0:1], v6, v6, 1.0
	v_rcp_f32_e32 v12, v7
	s_lshl_b64 s[0:1], s[24:25], 11
	s_lshl_b32 s25, s46, 1
	s_or_b32 s24, s25, 1
	v_fma_f32 v13, -v7, v12, 1.0
	v_fmac_f32_e32 v12, v13, v12
	v_div_scale_f32 v13, vcc, 1.0, v6, 1.0
	v_mul_f32_e32 v34, v13, v12
	v_fma_f32 v35, -v7, v34, v13
	v_fmac_f32_e32 v34, v35, v12
	v_fma_f32 v7, -v7, v34, v13
	v_div_fmas_f32 v7, v7, v12, v34
	v_div_fixup_f32 v6, v7, v6, 1.0
	v_pk_mul_f32 v[12:13], v[62:63], v[6:7] op_sel_hi:[1,0]
	v_pk_mul_f32 v[34:35], v[64:65], v[6:7] op_sel_hi:[1,0]
	v_pk_fma_f32 v[12:13], v[26:27], v[12:13], v[18:19]
	v_pk_fma_f32 v[20:21], v[28:29], v[34:35], v[20:21]
	v_cvt_pk_bf16_f32 v34, v12, v13
	s_lshl_b32 s24, s24, 12
	v_lshlrev_b32_e32 v7, 16, v34
	v_sub_f32_e32 v7, v12, v7
	v_and_b32_e32 v18, 0xffff0000, v34
	v_cvt_pk_bf16_f32 v35, v20, v21
	v_sub_f32_e32 v18, v13, v18
	v_cvt_pk_bf16_f32 v36, v7, v18
	v_mov_b32_e32 v7, 0
	v_cvt_pk_fp8_f32 v7, v12, v13
	s_add_i32 s24, s24, 0
	s_add_u32 s0, s40, s0
	v_lshlrev_b32_e32 v19, 16, v35
	v_cvt_pk_fp8_f32 v7, v20, v21 op_sel:[0,0,1]
	v_and_b32_e32 v26, 0xffff0000, v35
	s_addc_u32 s1, s44, s1
	v_sub_f32_e32 v19, v20, v19
	v_sub_f32_e32 v26, v21, v26
	v_cvt_pk_bf16_f32 v37, v19, v26
	global_store_dword v150, v7, s[0:1]
	global_load_dwordx4 v[18:21], v[10:11], off offset:1024
	global_load_dwordx4 v[26:29], v[8:9], off offset:1024
	v_lshrrev_b32_e32 v7, 1, v170
	v_bitop3_b32 v12, s25, v7, 1 bitop3:0x36
	v_lshlrev_b32_e32 v12, 4, v12
	v_add3_u32 v172, s24, v12, v103
	v_pk_mul_f32 v[12:13], v[54:55], v[6:7] op_sel_hi:[1,0]
	ds_write_b64 v172, v[34:35]
	v_pk_mul_f32 v[34:35], v[56:57], v[6:7] op_sel_hi:[1,0]
	v_add_u32_e32 v173, 0x10000, v172
	ds_write_b64 v173, v[36:37]
	v_or_b32_e32 v36, 32, v7
	v_bitop3_b32 v36, s25, v36, 1 bitop3:0x36
	v_lshlrev_b32_e32 v36, 4, v36
	v_add3_u32 v174, s24, v36, v103
	v_add_u32_e32 v175, 0x10000, v174
	v_or_b32_e32 v36, 64, v7
	v_bitop3_b32 v36, s25, v36, 1 bitop3:0x36
	v_lshlrev_b32_e32 v36, 4, v36
	v_add3_u32 v167, s24, v36, v103
	v_add_u32_e32 v168, 0x10000, v167
	v_pk_mul_f32 v[22:23], v[22:23], v[6:7] op_sel_hi:[1,0]
	v_pk_mul_f32 v[24:25], v[24:25], v[6:7] op_sel_hi:[1,0]
	v_pk_mul_f32 v[14:15], v[14:15], v[6:7] op_sel_hi:[1,0]
	v_pk_mul_f32 v[16:17], v[16:17], v[6:7] op_sel_hi:[1,0]
	s_waitcnt vmcnt(1)
	v_pk_add_f32 v[18:19], v[18:19], 1.0 op_sel_hi:[1,0]
	s_waitcnt vmcnt(0)
	v_pk_fma_f32 v[12:13], v[18:19], v[12:13], v[26:27]
	v_mov_b32_e32 v26, 0
	v_cvt_pk_fp8_f32 v26, v12, v13
	v_pk_add_f32 v[20:21], v[20:21], 1.0 op_sel_hi:[1,0]
	s_nop 0
	v_pk_fma_f32 v[20:21], v[20:21], v[34:35], v[28:29]
	v_cvt_pk_bf16_f32 v34, v12, v13
	s_nop 0
	v_cvt_pk_fp8_f32 v26, v20, v21 op_sel:[0,0,1]
	v_lshlrev_b32_e32 v18, 16, v34
	v_cvt_pk_bf16_f32 v35, v20, v21
	v_sub_f32_e32 v18, v12, v18
	v_and_b32_e32 v19, 0xffff0000, v34
	v_lshlrev_b32_e32 v12, 16, v35
	v_sub_f32_e32 v19, v13, v19
	v_sub_f32_e32 v13, v20, v12
	v_and_b32_e32 v12, 0xffff0000, v35
	v_sub_f32_e32 v20, v21, v12
	v_cvt_pk_bf16_f32 v12, v18, v19
	v_cvt_pk_bf16_f32 v13, v13, v20
	global_store_dword v150, v26, s[0:1] offset:256
	global_load_dwordx4 v[18:21], v[10:11], off offset:2048
	s_nop 0
	global_load_dwordx4 v[26:29], v[8:9], off offset:2048
	ds_write_b64 v175, v[12:13]
	v_pk_mul_f32 v[12:13], v[46:47], v[6:7] op_sel_hi:[1,0]
	ds_write_b64 v174, v[34:35]
	v_pk_mul_f32 v[34:35], v[48:49], v[6:7] op_sel_hi:[1,0]
	s_waitcnt vmcnt(1)
	v_pk_add_f32 v[18:19], v[18:19], 1.0 op_sel_hi:[1,0]
	s_waitcnt vmcnt(0)
	v_pk_fma_f32 v[12:13], v[18:19], v[12:13], v[26:27]
	v_mov_b32_e32 v26, 0
	v_cvt_pk_fp8_f32 v26, v12, v13
	v_pk_add_f32 v[20:21], v[20:21], 1.0 op_sel_hi:[1,0]
	s_nop 0
	v_pk_fma_f32 v[20:21], v[20:21], v[34:35], v[28:29]
	v_cvt_pk_bf16_f32 v34, v12, v13
	s_nop 0
	v_cvt_pk_fp8_f32 v26, v20, v21 op_sel:[0,0,1]
	v_lshlrev_b32_e32 v18, 16, v34
	v_cvt_pk_bf16_f32 v35, v20, v21
	v_sub_f32_e32 v18, v12, v18
	v_and_b32_e32 v19, 0xffff0000, v34
	v_lshlrev_b32_e32 v12, 16, v35
	v_sub_f32_e32 v19, v13, v19
	v_sub_f32_e32 v13, v20, v12
	v_and_b32_e32 v12, 0xffff0000, v35
	v_sub_f32_e32 v20, v21, v12
	v_cvt_pk_bf16_f32 v12, v18, v19
	v_cvt_pk_bf16_f32 v13, v13, v20
	global_store_dword v150, v26, s[0:1] offset:512
	global_load_dwordx4 v[18:21], v[10:11], off offset:3072
	s_nop 0
	global_load_dwordx4 v[26:29], v[8:9], off offset:3072
	ds_write_b64 v167, v[34:35]
	ds_write_b64 v168, v[12:13]
	v_pk_mul_f32 v[12:13], v[38:39], v[6:7] op_sel_hi:[1,0]
	v_pk_mul_f32 v[34:35], v[40:41], v[6:7] op_sel_hi:[1,0]
	v_mov_b32_e32 v38, 0
	s_waitcnt vmcnt(1)
	v_pk_add_f32 v[20:21], v[20:21], 1.0 op_sel_hi:[1,0]
	v_pk_add_f32 v[18:19], v[18:19], 1.0 op_sel_hi:[1,0]
	s_waitcnt vmcnt(0)
; #define LAS __attribute__((address_space(3)))
; __device__ __forceinline__ unsigned cvt_pk_bf16(float lo, float hi) { unsigned r; asm volatile("v_cvt_pk_bf16_f32 %0, %1, %2" : "=v"(r) : "v"(lo), "v"(hi)); return r; }
; __device__ __forceinline__ unsigned pk4_fp8(float a, float b, float c, float d) { int w = 0; w = __builtin_amdgcn_cvt_pk_fp8_f32(a, b, w, false); w = __builtin_amdgcn_cvt_pk_fp8_f32(c, d, w, true); return (unsigned)w; }
; __device__ __forceinline__ float bf_lo(unsigned w) { return __uint_as_float(w << 16); }
; __device__ __forceinline__ float bf_hi(unsigned w) { return __uint_as_float(w & 0xffff0000u); }
; __device__ __forceinline__ void p6_router(Frame& F) {
;     ...
;                 for (int j = 0; j < 8; ++j) { const f32x4 sh = ((const f32x4*)(mod + (size_t)b * 12288 + 6144))[loq + 64 * j], sc = ((const f32x4*)(mod + (size_t)b * 12288 + 8192))[loq + 64 * j];
;                     const f32x4 y = v[j] * rstd * (sc + 1.0f) + sh;
;                     u32x2 wh; wh.x = cvt_pk_bf16(y[0], y[1]); wh.y = cvt_pk_bf16(y[2], y[3]);
;                     const f32x4 yl = {y[0] - bf_lo(wh.x), y[1] - bf_hi(wh.x), y[2] - bf_lo(wh.y), y[3] - bf_hi(wh.y)};
;                     u32x2 wl; wl.x = cvt_pk_bf16(yl[0], yl[1]); wl.y = cvt_pk_bf16(yl[2], yl[3]);
;                     { const int r = 2 * wave + q; LAS unsigned char* rowp = F.lds + r * 4096 + ((((lane >> 1) + 32 * j) ^ r) << 4) + (lane & 1) * 8;
;                       *(LAS u32x2*)rowp = wh; *(LAS u32x2*)(rowp + 65536) = wl; }
;                     U2F[(size_t)t * (DM / 4) + lane + 64 * j] = pk4_fp8(y[0], y[1], y[2], y[3]); }
	v_pk_fma_f32 v[20:21], v[34:35], v[20:21], v[28:29]
	v_pk_fma_f32 v[12:13], v[12:13], v[18:19], v[26:27]
	v_mov_b32_e32 v34, 0
	v_cvt_pk_fp8_f32 v34, v12, v13
	v_cvt_pk_bf16_f32 v26, v12, v13
	v_cvt_pk_bf16_f32 v27, v20, v21
	v_cvt_pk_fp8_f32 v34, v20, v21 op_sel:[0,0,1]
	v_lshlrev_b32_e32 v18, 16, v26
	v_and_b32_e32 v19, 0xffff0000, v26
	v_sub_f32_e32 v18, v12, v18
	v_sub_f32_e32 v19, v13, v19
	v_lshlrev_b32_e32 v12, 16, v27
	v_and_b32_e32 v13, 0xffff0000, v27
	v_sub_f32_e32 v12, v20, v12
	v_sub_f32_e32 v13, v21, v13
	v_cvt_pk_bf16_f32 v28, v18, v19
	v_cvt_pk_bf16_f32 v29, v12, v13
	global_store_dword v150, v34, s[0:1] offset:768
	v_add_co_u32_e32 v34, vcc, s41, v10
	s_nop 1
	v_addc_co_u32_e32 v35, vcc, 0, v11, vcc
	v_add_co_u32_e32 v36, vcc, s41, v8
	global_load_dwordx4 v[10:13], v[34:35], off
	s_nop 0
	v_addc_co_u32_e32 v37, vcc, 0, v9, vcc
	global_load_dwordx4 v[18:21], v[36:37], off
	v_or_b32_e32 v8, 0x60, v7
	v_bitop3_b32 v8, s25, v8, 1 bitop3:0x36
	v_lshlrev_b32_e32 v8, 4, v8
	v_add3_u32 v176, s24, v8, v103
	v_pk_mul_f32 v[8:9], v[30:31], v[6:7] op_sel_hi:[1,0]
	v_pk_mul_f32 v[30:31], v[32:33], v[6:7] op_sel_hi:[1,0]
	v_add_u32_e32 v177, 0x10000, v176
	ds_write_b64 v176, v[26:27]
	ds_write_b64 v177, v[28:29]
	v_mov_b32_e32 v28, 0
	v_or_b32_e32 v29, 0x80, v7
	v_bitop3_b32 v29, s25, v29, 1 bitop3:0x36
	v_lshlrev_b32_e32 v29, 4, v29
	v_add3_u32 v178, s24, v29, v103
	v_add_u32_e32 v179, 0x10000, v178
	s_waitcnt vmcnt(1)
	v_pk_add_f32 v[10:11], v[10:11], 1.0 op_sel_hi:[1,0]
	v_pk_add_f32 v[12:13], v[12:13], 1.0 op_sel_hi:[1,0]
	s_waitcnt vmcnt(0)
	v_pk_fma_f32 v[8:9], v[8:9], v[10:11], v[18:19]
	s_nop 0
	v_cvt_pk_fp8_f32 v38, v8, v9
	v_pk_fma_f32 v[12:13], v[30:31], v[12:13], v[20:21]
	v_cvt_pk_bf16_f32 v26, v8, v9
	s_nop 0
	v_cvt_pk_fp8_f32 v38, v12, v13 op_sel:[0,0,1]
	v_cvt_pk_bf16_f32 v27, v12, v13
	v_lshlrev_b32_e32 v10, 16, v26
	v_and_b32_e32 v11, 0xffff0000, v26
	v_lshlrev_b32_e32 v18, 16, v27
	v_and_b32_e32 v19, 0xffff0000, v27
	v_sub_f32_e32 v8, v8, v10
	v_sub_f32_e32 v9, v9, v11
	v_sub_f32_e32 v10, v12, v18
	v_sub_f32_e32 v11, v13, v19
	v_cvt_pk_bf16_f32 v12, v8, v9
	v_cvt_pk_bf16_f32 v13, v10, v11
	global_store_dword v150, v38, s[0:1] offset:1024
	global_load_dwordx4 v[8:11], v[34:35], off offset:1024
	global_load_dwordx4 v[18:21], v[36:37], off offset:1024
	ds_write_b64 v178, v[26:27]
	ds_write_b64 v179, v[12:13]
	s_waitcnt vmcnt(1)
	v_pk_add_f32 v[8:9], v[8:9], 1.0 op_sel_hi:[1,0]
	s_waitcnt vmcnt(0)
	v_pk_fma_f32 v[8:9], v[22:23], v[8:9], v[18:19]
	v_pk_add_f32 v[10:11], v[10:11], 1.0 op_sel_hi:[1,0]
	v_cvt_pk_fp8_f32 v28, v8, v9
	v_pk_fma_f32 v[10:11], v[24:25], v[10:11], v[20:21]
	v_cvt_pk_bf16_f32 v12, v8, v9
	v_mov_b32_e32 v24, 0
	v_cvt_pk_fp8_f32 v28, v10, v11 op_sel:[0,0,1]
	v_cvt_pk_bf16_f32 v13, v10, v11
	v_lshlrev_b32_e32 v18, 16, v12
	v_and_b32_e32 v19, 0xffff0000, v12
	v_lshlrev_b32_e32 v20, 16, v13
	v_and_b32_e32 v21, 0xffff0000, v13
	v_sub_f32_e32 v8, v8, v18
	v_sub_f32_e32 v9, v9, v19
	v_sub_f32_e32 v18, v10, v20
	v_sub_f32_e32 v10, v11, v21
	v_cvt_pk_bf16_f32 v22, v8, v9
	v_cvt_pk_bf16_f32 v23, v18, v10
	global_store_dword v150, v28, s[0:1] offset:1280
	global_load_dwordx4 v[8:11], v[34:35], off offset:2048
	global_load_dwordx4 v[18:21], v[36:37], off offset:2048
	v_or_b32_e32 v25, 0xa0, v7
	v_bitop3_b32 v25, s25, v25, 1 bitop3:0x36
	v_lshlrev_b32_e32 v25, 4, v25
	v_add3_u32 v180, s24, v25, v103
	v_add_u32_e32 v181, 0x10000, v180
	ds_write_b64 v180, v[12:13]
	ds_write_b64 v181, v[22:23]
	s_waitcnt vmcnt(1)
	v_pk_add_f32 v[8:9], v[8:9], 1.0 op_sel_hi:[1,0]
	s_waitcnt vmcnt(0)
	v_pk_fma_f32 v[8:9], v[14:15], v[8:9], v[18:19]
	v_pk_add_f32 v[10:11], v[10:11], 1.0 op_sel_hi:[1,0]
	v_cvt_pk_fp8_f32 v24, v8, v9
	v_pk_fma_f32 v[10:11], v[16:17], v[10:11], v[20:21]
	v_cvt_pk_bf16_f32 v16, v8, v9
	v_or_b32_e32 v21, 0xc0, v7
	v_cvt_pk_fp8_f32 v24, v10, v11 op_sel:[0,0,1]
	v_cvt_pk_bf16_f32 v17, v10, v11
	v_lshlrev_b32_e32 v12, 16, v16
	v_and_b32_e32 v13, 0xffff0000, v16
	v_lshlrev_b32_e32 v14, 16, v17
	v_and_b32_e32 v15, 0xffff0000, v17
	v_sub_f32_e32 v8, v8, v12
	v_sub_f32_e32 v9, v9, v13
	v_sub_f32_e32 v12, v10, v14
	v_sub_f32_e32 v10, v11, v15
	v_cvt_pk_bf16_f32 v18, v8, v9
	v_cvt_pk_bf16_f32 v19, v12, v10
	global_store_dword v150, v24, s[0:1] offset:1536
	global_load_dwordx4 v[8:11], v[34:35], off offset:3072
	global_load_dwordx4 v[12:15], v[36:37], off offset:3072
	v_or_b32_e32 v7, 0xe0, v7
	v_bitop3_b32 v7, s25, v7, 1 bitop3:0x36
	v_pk_mul_f32 v[4:5], v[4:5], v[6:7] op_sel_hi:[1,0]
	v_mov_b32_e32 v20, 0
	v_lshlrev_b32_e32 v22, 4, v7
	v_pk_mul_f32 v[2:3], v[2:3], v[6:7] op_sel_hi:[1,0]
	v_bitop3_b32 v21, s25, v21, 1 bitop3:0x36
	v_lshlrev_b32_e32 v21, 4, v21
	v_add3_u32 v184, s24, v21, v103
	v_add_u32_e32 v185, 0x10000, v184
	ds_write_b64 v184, v[16:17]
	ds_write_b64 v185, v[18:19]
	v_add3_u32 v182, s24, v22, v103
	v_add_u32_e32 v183, 0x10000, v182
	s_waitcnt vmcnt(1)
	v_pk_add_f32 v[8:9], v[8:9], 1.0 op_sel_hi:[1,0]
	s_waitcnt vmcnt(0)
; #define LAS __attribute__((address_space(3)))
; __device__ __forceinline__ void p6_router(Frame& F) {
;     ...
;             bf16x8 bh[2][2], bl[2][2]; f32x4 cur[2] = {(f32x4){0.f, 0.f, 0.f, 0.f}, (f32x4){0.f, 0.f, 0.f, 0.f}};
;             const bf16_t* wbh = WRH + (size_t)fr * DM + wave * 256 + fq * 8; const bf16_t* wbl = WRL + (size_t)fr * DM + wave * 256 + fq * 8;
; #pragma unroll
;             for (int n = 0; n < 2; ++n) { bh[0][n] = *(const bf16x8*)(wbh + (size_t)(16 * n) * DM); bl[0][n] = *(const bf16x8*)(wbl + (size_t)(16 * n) * DM); }
;             if (rp == 0) {
; #pragma unroll
;                 for (int q = 0; q < 2; ++q)
; #pragma unroll
;                     for (int j = 0; j < 8; ++j) zr[q][j] = ((const u32x2*)(ZB + (size_t)(ta + 2 + q) * DM))[lane + 64 * j];
;             }
;             __syncthreads();
; #pragma unroll
;             for (int ks = 0; ks < 8; ++ks) {
;                 if (ks < 7) {
; #pragma unroll
;                     for (int n = 0; n < 2; ++n) { bh[(ks + 1) & 1][n] = *(const bf16x8*)(wbh + (size_t)(16 * n) * DM + (ks + 1) * 32); bl[(ks + 1) & 1][n] = *(const bf16x8*)(wbl + (size_t)(16 * n) * DM + (ks + 1) * 32); }
;                 }
;                 const LAS unsigned char* ap = F.lds + fr * 4096 + (((wave * 32 + ks * 4 + fq) ^ fr) << 4);
;                 const bf16x8 ah = *(const LAS bf16x8*)ap, al = *(const LAS bf16x8*)(ap + 65536);
; #pragma unroll
;                 for (int n = 0; n < 2; ++n) {
;                     cur[n] = __builtin_amdgcn_mfma_f32_16x16x32_bf16(ah, bh[ks & 1][n], cur[n], 0, 0, 0);
;                     cur[n] = __builtin_amdgcn_mfma_f32_16x16x32_bf16(ah, bl[ks & 1][n], cur[n], 0, 0, 0);
;                     cur[n] = __builtin_amdgcn_mfma_f32_16x16x32_bf16(al, bh[ks & 1][n], cur[n], 0, 0, 0);
;                 }
;                 __builtin_amdgcn_sched_barrier(0);
	v_pk_fma_f32 v[4:5], v[4:5], v[8:9], v[12:13]
	v_pk_add_f32 v[6:7], v[10:11], 1.0 op_sel_hi:[1,0]
	v_cvt_pk_fp8_f32 v20, v4, v5
	v_pk_fma_f32 v[2:3], v[2:3], v[6:7], v[14:15]
	v_cvt_pk_bf16_f32 v6, v4, v5
	s_nop 0
	v_cvt_pk_fp8_f32 v20, v2, v3 op_sel:[0,0,1]
	v_lshlrev_b32_e32 v8, 16, v6
	v_and_b32_e32 v9, 0xffff0000, v6
	v_cvt_pk_bf16_f32 v7, v2, v3
	v_sub_f32_e32 v4, v4, v8
	v_lshlrev_b32_e32 v10, 16, v7
	v_and_b32_e32 v11, 0xffff0000, v7
	v_sub_f32_e32 v5, v5, v9
	v_sub_f32_e32 v8, v2, v10
	v_sub_f32_e32 v9, v3, v11
	v_cvt_pk_bf16_f32 v4, v4, v5
	v_cvt_pk_bf16_f32 v5, v8, v9
	ds_write_b64 v182, v[6:7]
	ds_write_b64 v183, v[4:5]
	global_store_dword v150, v20, s[0:1] offset:1792
	v_lshlrev_b32_e32 v78, 12, v151
	s_lshl_b32 s36, s46, 9
	v_lshl_add_u64 v[4:5], s[82:83], 0, v[78:79]
	v_and_b32_e32 v2, 48, v170
	v_mov_b32_e32 v3, v79
	v_lshl_add_u64 v[4:5], v[4:5], 0, s[36:37]
	v_lshl_add_u64 v[44:45], v[4:5], 0, v[2:3]
	s_mov_b32 s0, 0x3c00000
	v_add_co_u32_e32 v84, vcc, s0, v44
	s_mov_b32 s1, 0x3c10000
	s_nop 0
	v_addc_co_u32_e32 v85, vcc, 0, v45, vcc
	global_load_dwordx4 v[2:5], v[84:85], off
	v_add_co_u32_e32 v74, vcc, s1, v44
	s_mov_b32 s0, 0x3c20000
	s_nop 0
	v_addc_co_u32_e32 v75, vcc, 0, v45, vcc
	v_add_co_u32_e32 v86, vcc, s0, v44
	global_load_dwordx4 v[6:9], v[74:75], off
	s_nop 0
	v_addc_co_u32_e32 v87, vcc, 0, v45, vcc
	global_load_dwordx4 v[20:23], v[86:87], off
	s_mov_b32 s0, 0x3c30000
	v_add_co_u32_e32 v76, vcc, s0, v44
	s_or_b32 s0, s4, 2
	s_nop 0
	v_addc_co_u32_e32 v77, vcc, 0, v45, vcc
	global_load_dwordx4 v[24:27], v[76:77], off
	s_ashr_i32 s1, s0, 31
	s_lshl_b64 s[0:1], s[0:1], 12
	s_add_u32 s0, s6, s0
	s_addc_u32 s1, s7, s1
	s_or_b32 s24, s4, 3
	v_bitop3_b32 v10, s5, v151, v154 bitop3:0x36
	v_add_u32_e32 v52, 0, v78
	s_ashr_i32 s25, s24, 31
	v_lshl_add_u32 v186, v10, 4, v52
	global_load_dwordx2 v[46:47], v146, s[0:1] nt
	global_load_dwordx2 v[48:49], v146, s[0:1] offset:512 nt
	global_load_dwordx2 v[50:51], v146, s[0:1] offset:1024 nt
	global_load_dwordx2 v[18:19], v146, s[0:1] offset:1536 nt
	global_load_dwordx2 v[16:17], v146, s[0:1] offset:2048 nt
	global_load_dwordx2 v[14:15], v146, s[0:1] offset:2560 nt
	global_load_dwordx2 v[12:13], v146, s[0:1] offset:3072 nt
	global_load_dwordx2 v[10:11], v146, s[0:1] offset:3584 nt
	s_lshl_b64 s[0:1], s[24:25], 12
	s_add_u32 s0, s6, s0
	s_addc_u32 s1, s7, s1
	global_load_dwordx2 v[100:101], v146, s[0:1] nt
	global_load_dwordx2 v[102:103], v146, s[0:1] offset:512 nt
	global_load_dwordx2 v[98:99], v146, s[0:1] offset:1024 nt
	global_load_dwordx2 v[96:97], v146, s[0:1] offset:1536 nt
	global_load_dwordx2 v[94:95], v146, s[0:1] offset:2048 nt
	global_load_dwordx2 v[92:93], v146, s[0:1] offset:2560 nt
	global_load_dwordx2 v[90:91], v146, s[0:1] offset:3072 nt
	global_load_dwordx2 v[88:89], v146, s[0:1] offset:3584 nt
	s_waitcnt lgkmcnt(0)
	s_barrier
	ds_read_b128 v[28:31], v186
	v_add_u32_e32 v187, 0x10000, v186
	ds_read_b128 v[32:35], v187
	s_mov_b64 s[0:1], 0x3c00000
	s_mov_b64 s[6:7], 0x3c20000
	v_lshl_add_u64 v[80:81], v[44:45], 0, s[0:1]
	v_lshl_add_u64 v[82:83], v[44:45], 0, s[6:7]
	v_or_b32_e32 v44, s5, v154
	s_waitcnt vmcnt(19) lgkmcnt(1)
	v_mfma_f32_16x16x32_bf16 v[36:39], v[28:31], v[2:5], 0
	s_waitcnt vmcnt(18)
	v_mfma_f32_16x16x32_bf16 v[40:43], v[28:31], v[6:9], 0
	s_waitcnt vmcnt(17)
	v_mfma_f32_16x16x32_bf16 v[20:23], v[28:31], v[20:23], v[36:39]
	s_waitcnt vmcnt(16)
	v_mfma_f32_16x16x32_bf16 v[24:27], v[28:31], v[24:27], v[40:43]
	global_load_dwordx4 v[28:31], v[80:81], off offset:64
	s_nop 0
	global_load_dwordx4 v[36:39], v[82:83], off offset:64
	s_waitcnt lgkmcnt(0)
	v_mfma_f32_16x16x32_bf16 v[2:5], v[32:35], v[2:5], v[20:23]
	s_nop 2
	global_load_dwordx4 v[20:23], v[74:75], off offset:64
	global_load_dwordx4 v[40:43], v[76:77], off offset:64
	v_mfma_f32_16x16x32_bf16 v[6:9], v[32:35], v[6:9], v[24:27]
	s_nop 2
	v_bitop3_b32 v24, v44, v151, 4 bitop3:0x36
	v_lshl_add_u32 v188, v24, 4, v52
	ds_read_b128 v[24:27], v188
	v_add_u32_e32 v189, 0x10000, v188
	ds_read_b128 v[32:35], v189
	s_waitcnt vmcnt(3) lgkmcnt(1)
	v_mfma_f32_16x16x32_bf16 v[2:5], v[24:27], v[28:31], v[2:5]
	s_waitcnt vmcnt(1)
	v_mfma_f32_16x16x32_bf16 v[6:9], v[24:27], v[20:23], v[6:9]
	v_mfma_f32_16x16x32_bf16 v[2:5], v[24:27], v[36:39], v[2:5]
	s_waitcnt vmcnt(0)
	v_mfma_f32_16x16x32_bf16 v[6:9], v[24:27], v[40:43], v[6:9]
	global_load_dwordx4 v[24:27], v[80:81], off offset:128
	global_load_dwordx4 v[36:39], v[82:83], off offset:128
	s_waitcnt lgkmcnt(0)
	v_mfma_f32_16x16x32_bf16 v[2:5], v[32:35], v[28:31], v[2:5]
	global_load_dwordx4 v[28:31], v[74:75], off offset:128
	global_load_dwordx4 v[40:43], v[76:77], off offset:128
	v_mfma_f32_16x16x32_bf16 v[6:9], v[32:35], v[20:23], v[6:9]
	v_bitop3_b32 v20, v44, v151, 8 bitop3:0x36
	v_lshl_add_u32 v190, v20, 4, v52
	ds_read_b128 v[20:23], v190
	v_add_u32_e32 v191, 0x10000, v190
	ds_read_b128 v[32:35], v191
	s_waitcnt vmcnt(3) lgkmcnt(1)
	v_mfma_f32_16x16x32_bf16 v[2:5], v[20:23], v[24:27], v[2:5]
	s_waitcnt vmcnt(1)
	v_mfma_f32_16x16x32_bf16 v[6:9], v[20:23], v[28:31], v[6:9]
	v_mfma_f32_16x16x32_bf16 v[2:5], v[20:23], v[36:39], v[2:5]
	s_waitcnt vmcnt(0)
	v_mfma_f32_16x16x32_bf16 v[6:9], v[20:23], v[40:43], v[6:9]
	global_load_dwordx4 v[20:23], v[80:81], off offset:192
	global_load_dwordx4 v[36:39], v[82:83], off offset:192
	s_waitcnt lgkmcnt(0)
	v_mfma_f32_16x16x32_bf16 v[2:5], v[32:35], v[24:27], v[2:5]
	global_load_dwordx4 v[24:27], v[74:75], off offset:192
	global_load_dwordx4 v[40:43], v[76:77], off offset:192
	v_mfma_f32_16x16x32_bf16 v[6:9], v[32:35], v[28:31], v[6:9]
	v_bitop3_b32 v28, v44, v151, 12 bitop3:0x36
	v_lshl_add_u32 v192, v28, 4, v52
	ds_read_b128 v[28:31], v192
	v_add_u32_e32 v193, 0x10000, v192
	ds_read_b128 v[32:35], v193
	s_waitcnt vmcnt(3) lgkmcnt(1)
; #define LAS __attribute__((address_space(3)))
; __device__ __forceinline__ float bf_lo(unsigned w) { return __uint_as_float(w << 16); }
; __device__ __forceinline__ float bf_hi(unsigned w) { return __uint_as_float(w & 0xffff0000u); }
; __device__ __forceinline__ void p6_router(Frame& F) {
;     ...
;             for (int q = 0; q < 2; ++q) {
;                 const int t = ta + q; f32x4 v[8]; float s = 0.f;
; #pragma unroll
;                 for (int j = 0; j < 8; ++j) { const u32x2 zb = zr[q][j]; v[j] = (f32x4){bf_lo(zb.x), bf_hi(zb.x), bf_lo(zb.y), bf_hi(zb.y)}; s += (v[j][0] + v[j][1]) + (v[j][2] + v[j][3]); }
;                 float mean = wave_sum(s) * (1.f / DM), s2 = 0.f;
;     ...
; #pragma unroll
;             for (int ks = 0; ks < 8; ++ks) {
;                 if (ks < 7) {
; #pragma unroll
;                     for (int n = 0; n < 2; ++n) { bh[(ks + 1) & 1][n] = *(const bf16x8*)(wbh + (size_t)(16 * n) * DM + (ks + 1) * 32); bl[(ks + 1) & 1][n] = *(const bf16x8*)(wbl + (size_t)(16 * n) * DM + (ks + 1) * 32); }
;                 }
;                 const LAS unsigned char* ap = F.lds + fr * 4096 + (((wave * 32 + ks * 4 + fq) ^ fr) << 4);
;                 const bf16x8 ah = *(const LAS bf16x8*)ap, al = *(const LAS bf16x8*)(ap + 65536);
; #pragma unroll
;                 for (int n = 0; n < 2; ++n) {
;                     cur[n] = __builtin_amdgcn_mfma_f32_16x16x32_bf16(ah, bh[ks & 1][n], cur[n], 0, 0, 0);
;                     cur[n] = __builtin_amdgcn_mfma_f32_16x16x32_bf16(ah, bl[ks & 1][n], cur[n], 0, 0, 0);
;                     cur[n] = __builtin_amdgcn_mfma_f32_16x16x32_bf16(al, bh[ks & 1][n], cur[n], 0, 0, 0);
;                 }
;                 __builtin_amdgcn_sched_barrier(0);
;             }
	v_mfma_f32_16x16x32_bf16 v[2:5], v[28:31], v[20:23], v[2:5]
	s_waitcnt vmcnt(1)
	v_mfma_f32_16x16x32_bf16 v[6:9], v[28:31], v[24:27], v[6:9]
	v_mfma_f32_16x16x32_bf16 v[2:5], v[28:31], v[36:39], v[2:5]
	s_waitcnt vmcnt(0)
	v_mfma_f32_16x16x32_bf16 v[6:9], v[28:31], v[40:43], v[6:9]
	global_load_dwordx4 v[28:31], v[80:81], off offset:256
	global_load_dwordx4 v[36:39], v[82:83], off offset:256
	s_waitcnt lgkmcnt(0)
	v_mfma_f32_16x16x32_bf16 v[2:5], v[32:35], v[20:23], v[2:5]
	global_load_dwordx4 v[20:23], v[74:75], off offset:256
	global_load_dwordx4 v[40:43], v[76:77], off offset:256
	v_mfma_f32_16x16x32_bf16 v[6:9], v[32:35], v[24:27], v[6:9]
	v_bitop3_b32 v24, v44, v151, 16 bitop3:0x36
	v_lshl_add_u32 v194, v24, 4, v52
	ds_read_b128 v[24:27], v194
	v_add_u32_e32 v195, 0x10000, v194
	ds_read_b128 v[32:35], v195
	s_waitcnt vmcnt(3) lgkmcnt(1)
	v_mfma_f32_16x16x32_bf16 v[2:5], v[24:27], v[28:31], v[2:5]
	s_waitcnt vmcnt(1)
	v_mfma_f32_16x16x32_bf16 v[6:9], v[24:27], v[20:23], v[6:9]
	v_mfma_f32_16x16x32_bf16 v[2:5], v[24:27], v[36:39], v[2:5]
	s_waitcnt vmcnt(0)
	v_mfma_f32_16x16x32_bf16 v[6:9], v[24:27], v[40:43], v[6:9]
	global_load_dwordx4 v[24:27], v[80:81], off offset:320
	global_load_dwordx4 v[36:39], v[82:83], off offset:320
	s_waitcnt lgkmcnt(0)
	v_mfma_f32_16x16x32_bf16 v[2:5], v[32:35], v[28:31], v[2:5]
	global_load_dwordx4 v[28:31], v[74:75], off offset:320
	global_load_dwordx4 v[40:43], v[76:77], off offset:320
	v_mfma_f32_16x16x32_bf16 v[6:9], v[32:35], v[20:23], v[6:9]
	v_bitop3_b32 v20, v44, v151, 20 bitop3:0x36
	v_lshl_add_u32 v196, v20, 4, v52
	ds_read_b128 v[20:23], v196
	v_add_u32_e32 v197, 0x10000, v196
	ds_read_b128 v[32:35], v197
	s_waitcnt vmcnt(3) lgkmcnt(1)
	v_mfma_f32_16x16x32_bf16 v[2:5], v[20:23], v[24:27], v[2:5]
	s_waitcnt vmcnt(1)
	v_mfma_f32_16x16x32_bf16 v[6:9], v[20:23], v[28:31], v[6:9]
	v_mfma_f32_16x16x32_bf16 v[2:5], v[20:23], v[36:39], v[2:5]
	s_waitcnt vmcnt(0)
	v_mfma_f32_16x16x32_bf16 v[6:9], v[20:23], v[40:43], v[6:9]
	global_load_dwordx4 v[20:23], v[80:81], off offset:384
	global_load_dwordx4 v[36:39], v[82:83], off offset:384
	s_waitcnt lgkmcnt(0)
	v_mfma_f32_16x16x32_bf16 v[2:5], v[32:35], v[24:27], v[2:5]
	global_load_dwordx4 v[24:27], v[74:75], off offset:384
	global_load_dwordx4 v[40:43], v[76:77], off offset:384
	v_mfma_f32_16x16x32_bf16 v[6:9], v[32:35], v[28:31], v[6:9]
	v_bitop3_b32 v28, v44, v151, 24 bitop3:0x36
	v_lshl_add_u32 v199, v28, 4, v52
	ds_read_b128 v[28:31], v199
	v_add_u32_e32 v201, 0x10000, v199
	ds_read_b128 v[32:35], v201
	s_waitcnt vmcnt(3) lgkmcnt(1)
	v_mfma_f32_16x16x32_bf16 v[2:5], v[28:31], v[20:23], v[2:5]
	s_waitcnt vmcnt(1)
	v_mfma_f32_16x16x32_bf16 v[6:9], v[28:31], v[24:27], v[6:9]
	v_mfma_f32_16x16x32_bf16 v[2:5], v[28:31], v[36:39], v[2:5]
	s_waitcnt vmcnt(0)
	v_mfma_f32_16x16x32_bf16 v[6:9], v[28:31], v[40:43], v[6:9]
	global_load_dwordx4 v[28:31], v[80:81], off offset:448
	global_load_dwordx4 v[36:39], v[82:83], off offset:448
	s_waitcnt lgkmcnt(0)
	v_mfma_f32_16x16x32_bf16 v[2:5], v[32:35], v[20:23], v[2:5]
	global_load_dwordx4 v[20:23], v[74:75], off offset:448
	global_load_dwordx4 v[40:43], v[76:77], off offset:448
	v_mfma_f32_16x16x32_bf16 v[6:9], v[32:35], v[24:27], v[6:9]
	v_bitop3_b32 v24, v44, v151, 28 bitop3:0x36
	v_lshl_add_u32 v198, v24, 4, v52
	ds_read_b128 v[24:27], v198
	v_add_u32_e32 v200, 0x10000, v198
	ds_read_b128 v[32:35], v200
	s_waitcnt vmcnt(3) lgkmcnt(1)
	v_mfma_f32_16x16x32_bf16 v[2:5], v[24:27], v[28:31], v[2:5]
	s_waitcnt vmcnt(1)
	v_mfma_f32_16x16x32_bf16 v[6:9], v[24:27], v[20:23], v[6:9]
	v_mfma_f32_16x16x32_bf16 v[2:5], v[24:27], v[36:39], v[2:5]
	s_waitcnt vmcnt(0)
	v_mfma_f32_16x16x32_bf16 v[6:9], v[24:27], v[40:43], v[6:9]
	s_waitcnt lgkmcnt(0)
	v_mfma_f32_16x16x32_bf16 v[2:5], v[32:35], v[28:31], v[2:5]
	v_mfma_f32_16x16x32_bf16 v[6:9], v[32:35], v[20:23], v[6:9]
	v_lshlrev_b32_e32 v131, 16, v48
	v_lshlrev_b32_e32 v130, 16, v46
	v_and_b32_e32 v133, 0xffff0000, v48
	v_and_b32_e32 v132, 0xffff0000, v46
	v_lshlrev_b32_e32 v127, 16, v49
	v_lshlrev_b32_e32 v126, 16, v47
	v_and_b32_e32 v129, 0xffff0000, v49
	v_and_b32_e32 v128, 0xffff0000, v47
	v_pk_add_f32 v[20:21], v[130:131], v[132:133]
	v_pk_add_f32 v[22:23], v[126:127], v[128:129]
	v_lshlrev_b32_e32 v125, 16, v51
	v_pk_add_f32 v[20:21], v[20:21], v[22:23]
	v_lshlrev_b32_e32 v124, 16, v50
	v_add_f32_e32 v20, 0, v20
	v_add_f32_e32 v114, v20, v21
	v_and_b32_e32 v21, 0xffff0000, v51
	v_and_b32_e32 v20, 0xffff0000, v50
	v_pk_add_f32 v[22:23], v[124:125], v[20:21]
	v_lshlrev_b32_e32 v120, 16, v18
	v_and_b32_e32 v121, 0xffff0000, v18
	v_lshlrev_b32_e32 v122, 16, v19
	v_and_b32_e32 v123, 0xffff0000, v19
	v_lshlrev_b32_e32 v115, 16, v16
	v_and_b32_e32 v139, 0xffff0000, v16
	v_lshlrev_b32_e32 v119, 16, v17
	v_and_b32_e32 v117, 0xffff0000, v17
	v_pk_add_f32 v[16:17], v[22:23], v[22:23] op_sel:[0,1] op_sel_hi:[1,0]
	v_add_f32_e32 v118, v120, v121
	v_add_f32_e32 v116, v122, v123
	v_mov_b32_e32 v17, v139
	v_pk_add_f32 v[16:17], v[114:115], v[16:17]
	v_pk_add_f32 v[18:19], v[118:119], v[116:117]
	v_lshlrev_b32_e32 v113, 16, v15
	v_lshlrev_b32_e32 v112, 16, v14
	v_and_b32_e32 v15, 0xffff0000, v15
	v_and_b32_e32 v14, 0xffff0000, v14
	v_pk_add_f32 v[16:17], v[16:17], v[18:19]
	v_pk_add_f32 v[18:19], v[112:113], v[14:15]
	v_lshlrev_b32_e32 v108, 16, v12
	v_and_b32_e32 v109, 0xffff0000, v12
	v_lshlrev_b32_e32 v110, 16, v13
	v_and_b32_e32 v111, 0xffff0000, v13
	v_lshlrev_b32_e32 v136, 16, v10
	v_and_b32_e32 v137, 0xffff0000, v10
	v_lshlrev_b32_e32 v107, 16, v11
	v_and_b32_e32 v105, 0xffff0000, v11
	v_pk_add_f32 v[10:11], v[16:17], v[16:17] op_sel:[0,1] op_sel_hi:[1,0]
	v_pk_add_f32 v[12:13], v[18:19], v[18:19] op_sel:[0,1] op_sel_hi:[1,0]
	v_add_f32_e32 v106, v108, v109
	v_add_f32_e32 v104, v110, v111
	v_mov_b32_e32 v11, v136
	v_mov_b32_e32 v13, v137
	v_pk_add_f32 v[10:11], v[10:11], v[12:13]
	v_pk_add_f32 v[12:13], v[106:107], v[104:105]
	s_nop 0
	v_pk_add_f32 v[10:11], v[10:11], v[12:13]
	s_barrier
; __device__ __forceinline__ unsigned cvt_pk_bf16(float lo, float hi) { unsigned r; asm volatile("v_cvt_pk_bf16_f32 %0, %1, %2" : "=v"(r) : "v"(lo), "v"(hi)); return r; }
; __device__ __forceinline__ float bf_lo(unsigned w) { return __uint_as_float(w << 16); }
; __device__ __forceinline__ float bf_hi(unsigned w) { return __uint_as_float(w & 0xffff0000u); }
; __device__ __forceinline__ void p6_router(Frame& F) {
;     ...
;             for (int j = 0; j < 8; ++j) { pw[j] = ((const f32x4*)F.in[I_LN1W])[lop + 64 * j]; pb[j] = ((const f32x4*)F.in[I_LN1B])[lop + 64 * j]; }
; #pragma unroll
;             for (int q = 0; q < 2; ++q) {
;                 const int t = ta + q; f32x4 v[8]; float s = 0.f;
; #pragma unroll
;                 for (int j = 0; j < 8; ++j) { const u32x2 zb = zr[q][j]; v[j] = (f32x4){bf_lo(zb.x), bf_hi(zb.x), bf_lo(zb.y), bf_hi(zb.y)}; s += (v[j][0] + v[j][1]) + (v[j][2] + v[j][3]); }
;                 float mean = wave_sum(s) * (1.f / DM), s2 = 0.f;
; #pragma unroll
;                 for (int j = 0; j < 8; ++j) { v[j] = v[j] - mean; s2 += (v[j][0] * v[j][0] + v[j][1] * v[j][1]) + (v[j][2] * v[j][2] + v[j][3] * v[j][3]); }
;                 float rstd = 1.f / sqrtf(wave_sum(s2) * (1.f / DM) + LN_EPS);
;                 s = 0.f;
; #pragma unroll
;                 for (int j = 0; j < 8; ++j) { v[j] = v[j] * rstd * pw[j] + pb[j]; { u32x2 xb; xb.x = cvt_pk_bf16(v[j][0], v[j][1]); xb.y = cvt_pk_bf16(v[j][2], v[j][3]); ((u32x2*)(X1 + (size_t)t * DM))[lane + 64 * j] = xb; } s += (v[j][0] + v[j][1]) + (v[j][2] + v[j][3]); }
	v_add_f32_e32 v10, v10, v11
	ds_bpermute_b32 v11, v1, v10
	s_waitcnt lgkmcnt(0)
	v_and_b32_e32 v215, 0xffff0000, v93
	v_and_b32_e32 v214, 0xffff0000, v92
	v_add_f32_e32 v10, v10, v11
	ds_bpermute_b32 v11, v142, v10
	s_waitcnt lgkmcnt(0)
	v_add_f32_e32 v10, v10, v11
	ds_bpermute_b32 v11, v143, v10
	s_waitcnt lgkmcnt(0)
	v_add_f32_e32 v10, v10, v11
	ds_bpermute_b32 v11, v144, v10
	s_waitcnt lgkmcnt(0)
	v_add_f32_e32 v12, v10, v11
	ds_bpermute_b32 v13, v145, v12
	v_mov_b32_e32 v10, v170
	s_waitcnt lgkmcnt(0)
	v_add_f32_e32 v22, v12, v13
	ds_bpermute_b32 v23, v147, v22
	v_ashrrev_i32_e32 v11, 31, v10
	v_lshlrev_b64 v[10:11], 4, v[10:11]
	v_lshl_add_u64 v[18:19], s[10:11], 0, v[10:11]
	v_lshl_add_u64 v[16:17], s[8:9], 0, v[10:11]
	s_waitcnt lgkmcnt(0)
	v_add_f32_e32 v28, v22, v23
	v_fmac_f32_e32 v128, 0xba000000, v28
	v_fmac_f32_e32 v132, 0xba000000, v28
	v_fmac_f32_e32 v129, 0xba000000, v28
	v_fmac_f32_e32 v133, 0xba000000, v28
	v_fmac_f32_e32 v126, 0xba000000, v28
	v_fmac_f32_e32 v130, 0xba000000, v28
	v_fmac_f32_e32 v127, 0xba000000, v28
	v_fmac_f32_e32 v131, 0xba000000, v28
	v_pk_mul_f32 v[22:23], v[132:133], v[132:133]
	v_pk_mul_f32 v[24:25], v[128:129], v[128:129]
	v_fmac_f32_e32 v20, 0xba000000, v28
	v_fmac_f32_e32 v21, 0xba000000, v28
	v_fmac_f32_e32 v125, 0xba000000, v28
	v_pk_fma_f32 v[22:23], v[130:131], v[130:131], v[22:23]
	v_pk_fma_f32 v[24:25], v[126:127], v[126:127], v[24:25]
	v_fmac_f32_e32 v124, 0xba000000, v28
	v_mov_b32_e32 v202, v125
	v_mov_b32_e32 v203, v21
	v_mov_b32_e32 v125, v20
	v_pk_add_f32 v[22:23], v[22:23], v[24:25]
	v_pk_mul_f32 v[24:25], v[202:203], v[202:203]
	v_pk_mul_f32 v[20:21], v[124:125], v[124:125]
	v_fmac_f32_e32 v120, 0xba000000, v28
	v_pk_mov_b32 v[26:27], v[20:21], v[24:25] op_sel:[1,0]
	v_mov_b32_e32 v21, v25
	v_pk_add_f32 v[20:21], v[26:27], v[20:21]
	v_fmac_f32_e32 v121, 0xba000000, v28
	v_pk_add_f32 v[20:21], v[20:21], v[20:21] op_sel_hi:[0,1]
	v_fmac_f32_e32 v122, 0xba000000, v28
	v_mul_f32_e32 v20, v120, v120
	v_fmac_f32_e32 v123, 0xba000000, v28
	v_pk_fma_f32 v[24:25], v[120:121], v[120:121], v[20:21] op_sel_hi:[1,1,0]
	v_mul_f32_e32 v20, v122, v122
	v_pk_add_f32 v[22:23], v[22:23], v[22:23] op_sel_hi:[0,1]
	v_pk_fma_f32 v[26:27], v[122:123], v[122:123], v[20:21] op_sel_hi:[1,1,0]
	v_fmac_f32_e32 v117, 0xba000000, v28
	v_fmac_f32_e32 v119, 0xba000000, v28
	v_fmac_f32_e32 v139, 0xba000000, v28
	v_fmac_f32_e32 v115, 0xba000000, v28
	v_fmac_f32_e32 v14, 0xba000000, v28
	v_fmac_f32_e32 v15, 0xba000000, v28
	v_fmac_f32_e32 v113, 0xba000000, v28
	v_mul_f32_e32 v24, v115, v115
	v_mul_f32_e32 v26, v139, v139
	v_mul_f32_e32 v20, v119, v119
	v_mul_f32_e32 v22, v117, v117
	v_fmac_f32_e32 v112, 0xba000000, v28
	v_mov_b32_e32 v140, v113
	v_mov_b32_e32 v141, v15
	v_mov_b32_e32 v113, v14
	v_pk_add_f32 v[24:25], v[24:25], v[26:27]
	v_pk_add_f32 v[20:21], v[20:21], v[22:23]
	v_pk_mul_f32 v[22:23], v[140:141], v[140:141]
	v_pk_mul_f32 v[14:15], v[112:113], v[112:113]
	v_pk_add_f32 v[20:21], v[24:25], v[20:21]
	v_pk_mov_b32 v[24:25], v[14:15], v[22:23] op_sel:[1,0]
	v_mov_b32_e32 v15, v23
	v_pk_add_f32 v[14:15], v[24:25], v[14:15]
	v_fmac_f32_e32 v108, 0xba000000, v28
	v_pk_add_f32 v[14:15], v[14:15], v[14:15] op_sel_hi:[0,1]
	v_fmac_f32_e32 v109, 0xba000000, v28
	v_fmac_f32_e32 v110, 0xba000000, v28
	v_mul_f32_e32 v14, v108, v108
	v_fmac_f32_e32 v111, 0xba000000, v28
	v_pk_fma_f32 v[22:23], v[108:109], v[108:109], v[14:15] op_sel_hi:[1,1,0]
	v_mul_f32_e32 v14, v110, v110
	v_pk_add_f32 v[20:21], v[20:21], v[20:21] op_sel_hi:[0,1]
	v_pk_fma_f32 v[24:25], v[110:111], v[110:111], v[14:15] op_sel_hi:[1,1,0]
	v_fmac_f32_e32 v105, 0xba000000, v28
	v_fmac_f32_e32 v107, 0xba000000, v28
	v_fmac_f32_e32 v137, 0xba000000, v28
	v_fmac_f32_e32 v136, 0xba000000, v28
	v_mul_f32_e32 v22, v136, v136
	v_mul_f32_e32 v24, v137, v137
	v_mul_f32_e32 v14, v107, v107
	v_mul_f32_e32 v20, v105, v105
	v_pk_add_f32 v[22:23], v[22:23], v[24:25]
	v_pk_add_f32 v[14:15], v[14:15], v[20:21]
	global_load_dwordx4 v[10:13], v[18:19], off
	v_pk_add_f32 v[14:15], v[22:23], v[14:15]
	global_load_dwordx4 v[70:73], v[16:17], off
	global_load_dwordx4 v[62:65], v[16:17], off offset:1024
	global_load_dwordx4 v[66:69], v[18:19], off offset:1024
	v_add_f32_e32 v14, v14, v15
	ds_bpermute_b32 v15, v1, v14
	global_load_dwordx4 v[54:57], v[16:17], off offset:2048
	global_load_dwordx4 v[46:49], v[16:17], off offset:3072
	global_load_dwordx4 v[58:61], v[18:19], off offset:2048
	global_load_dwordx4 v[50:53], v[18:19], off offset:3072
	v_mov_b32_e32 v206, v127
	v_mov_b32_e32 v127, v128
	v_mov_b32_e32 v204, v131
	s_waitcnt lgkmcnt(0)
	v_add_f32_e32 v14, v14, v15
	ds_bpermute_b32 v15, v142, v14
	v_mov_b32_e32 v205, v133
	v_mov_b32_e32 v131, v132
	v_mov_b32_e32 v207, v129
	v_mov_b32_e32 v138, v115
	s_waitcnt lgkmcnt(0)
	v_add_f32_e32 v20, v14, v15
	ds_bpermute_b32 v21, v143, v20
	v_add_co_u32_e32 v14, vcc, s41, v16
	s_add_i32 s8, s4, 2
	s_nop 0
	v_addc_co_u32_e32 v15, vcc, 0, v17, vcc
	s_waitcnt lgkmcnt(0)
	v_add_f32_e32 v16, v20, v21
	ds_bpermute_b32 v17, v144, v16
	v_add_co_u32_e32 v18, vcc, s41, v18
	global_load_dwordx4 v[38:41], v[14:15], off
	global_load_dwordx4 v[30:33], v[14:15], off offset:1024
	v_addc_co_u32_e32 v19, vcc, 0, v19, vcc
	s_waitcnt lgkmcnt(0)
	v_add_f32_e32 v20, v16, v17
	ds_bpermute_b32 v21, v145, v20
	global_load_dwordx4 v[42:45], v[18:19], off
	global_load_dwordx4 v[34:37], v[18:19], off offset:1024
	global_load_dwordx4 v[22:25], v[14:15], off offset:2048
	s_nop 0
	global_load_dwordx4 v[14:17], v[14:15], off offset:3072
	s_ashr_i32 s9, s8, 31
	s_waitcnt lgkmcnt(0)
; __device__ __forceinline__ unsigned cvt_pk_bf16(float lo, float hi) { unsigned r; asm volatile("v_cvt_pk_bf16_f32 %0, %1, %2" : "=v"(r) : "v"(lo), "v"(hi)); return r; }
; __device__ __forceinline__ void p6_router(Frame& F) {
;     ...
;                 float rstd = 1.f / sqrtf(wave_sum(s2) * (1.f / DM) + LN_EPS);
;                 s = 0.f;
; #pragma unroll
;                 for (int j = 0; j < 8; ++j) { v[j] = v[j] * rstd * pw[j] + pb[j]; { u32x2 xb; xb.x = cvt_pk_bf16(v[j][0], v[j][1]); xb.y = cvt_pk_bf16(v[j][2], v[j][3]); ((u32x2*)(X1 + (size_t)t * DM))[lane + 64 * j] = xb; } s += (v[j][0] + v[j][1]) + (v[j][2] + v[j][3]); }
;                 mean = wave_sum(s) * (1.f / DM); s2 = 0.f;
	v_add_f32_e32 v78, v20, v21
	global_load_dwordx4 v[26:29], v[18:19], off offset:2048
	s_nop 0
	global_load_dwordx4 v[18:21], v[18:19], off offset:3072
	ds_bpermute_b32 v104, v147, v78
	s_waitcnt lgkmcnt(0)
	v_add_f32_e32 v78, v78, v104
	v_fmamk_f32 v78, v78, 0x3a000000, v148
	v_mul_f32_e32 v104, 0x4f800000, v78
	v_cmp_gt_f32_e32 vcc, s45, v78
	s_nop 1
	v_cndmask_b32_e32 v78, v78, v104, vcc
	v_sqrt_f32_e32 v104, v78
	s_nop 0
	v_add_u32_e32 v106, -1, v104
	v_fma_f32 v114, -v106, v104, v78
	v_cmp_ge_f32_e64 s[0:1], 0, v114
	v_add_u32_e32 v114, 1, v104
	s_nop 0
	v_cndmask_b32_e64 v106, v104, v106, s[0:1]
	v_fma_f32 v104, -v114, v104, v78
	v_cmp_lt_f32_e64 s[0:1], 0, v104
	s_nop 1
	v_cndmask_b32_e64 v104, v106, v114, s[0:1]
	v_mul_f32_e32 v106, 0x37800000, v104
	v_cndmask_b32_e32 v104, v104, v106, vcc
	v_cmp_class_f32_e32 vcc, v78, v149
	s_nop 1
	v_cndmask_b32_e32 v78, v104, v78, vcc
	v_div_scale_f32 v104, s[0:1], v78, v78, 1.0
	v_rcp_f32_e32 v106, v104
	s_lshl_b64 s[0:1], s[8:9], 12
	s_add_u32 s0, s42, s0
	s_addc_u32 s1, s43, s1
	v_fma_f32 v114, -v104, v106, 1.0
	v_fmac_f32_e32 v106, v114, v106
	v_div_scale_f32 v114, vcc, 1.0, v78, 1.0
	v_mul_f32_e32 v116, v114, v106
	v_fma_f32 v118, -v104, v116, v114
	v_fmac_f32_e32 v116, v118, v106
	v_fma_f32 v104, -v104, v116, v114
	v_div_fmas_f32 v104, v104, v106, v116
	v_div_fixup_f32 v78, v104, v78, 1.0
	v_pk_mul_f32 v[126:127], v[126:127], v[78:79] op_sel_hi:[1,0]
	v_pk_mul_f32 v[128:129], v[130:131], v[78:79] op_sel_hi:[1,0]
	s_waitcnt vmcnt(14)
	v_pk_fma_f32 v[132:133], v[72:73], v[126:127], v[12:13]
	v_pk_mul_f32 v[126:127], v[204:205], v[78:79] op_sel_hi:[1,0]
	v_pk_fma_f32 v[134:135], v[70:71], v[128:129], v[10:11]
	v_pk_mul_f32 v[128:129], v[206:207], v[78:79] op_sel_hi:[1,0]
	s_waitcnt vmcnt(12)
	v_pk_fma_f32 v[130:131], v[62:63], v[126:127], v[66:67]
	v_pk_fma_f32 v[128:129], v[64:65], v[128:129], v[68:69]
	v_mov_b32_e32 v126, v130
	v_mov_b32_e32 v127, v134
	v_mov_b32_e32 v204, v131
	v_mov_b32_e32 v205, v135
	v_pk_add_f32 v[126:127], v[126:127], v[204:205]
	v_mov_b32_e32 v204, v129
	v_mov_b32_e32 v205, v133
	v_mov_b32_e32 v206, v128
	v_mov_b32_e32 v207, v132
	v_pk_add_f32 v[204:205], v[204:205], v[206:207]
	v_mov_b32_e32 v116, v119
	v_pk_add_f32 v[126:127], v[126:127], v[204:205]
	v_pk_mul_f32 v[114:115], v[138:139], v[78:79] op_sel_hi:[1,0]
	v_add_f32_e32 v104, 0, v127
	v_add_f32_e32 v205, v126, v104
	v_pk_mul_f32 v[126:127], v[124:125], v[78:79] op_sel_hi:[1,0]
	v_pk_mul_f32 v[124:125], v[202:203], v[78:79] op_sel_hi:[1,0]
	s_waitcnt vmcnt(9)
	v_pk_fma_f32 v[126:127], v[54:55], v[126:127], v[58:59]
	v_pk_fma_f32 v[124:125], v[56:57], v[124:125], v[60:61]
	v_mov_b32_e32 v202, v126
	v_mov_b32_e32 v203, v125
	v_pk_mov_b32 v[206:207], v[126:127], v[124:125] op_sel:[1,0]
	v_pk_mul_f32 v[116:117], v[116:117], v[78:79] op_sel_hi:[1,0]
	v_pk_add_f32 v[202:203], v[202:203], v[206:207]
	v_pk_mul_f32 v[206:207], v[120:121], v[78:79] op_sel_hi:[1,0]
	v_pk_mul_f32 v[120:121], v[122:123], v[78:79] op_sel_hi:[1,0]
	v_pk_add_f32 v[202:203], v[202:203], v[202:203] op_sel_hi:[0,1]
	s_waitcnt vmcnt(8)
	v_pk_fma_f32 v[120:121], v[48:49], v[120:121], v[52:53]
	v_pk_fma_f32 v[122:123], v[46:47], v[206:207], v[50:51]
	s_waitcnt vmcnt(5)
	v_pk_fma_f32 v[116:117], v[40:41], v[116:117], v[44:45]
	v_pk_fma_f32 v[118:119], v[38:39], v[114:115], v[42:43]
	v_add_f32_e32 v207, v122, v123
	v_add_f32_e32 v211, v121, v120
	v_mov_b32_e32 v206, v118
	v_mov_b32_e32 v210, v119
	v_mov_b32_e32 v202, v117
	v_mov_b32_e32 v204, v116
	v_pk_add_f32 v[114:115], v[206:207], v[210:211]
	v_pk_add_f32 v[138:139], v[202:203], v[204:205]
	v_mov_b32_e32 v104, v107
	v_pk_add_f32 v[114:115], v[114:115], v[138:139]
	v_pk_mul_f32 v[136:137], v[136:137], v[78:79] op_sel_hi:[1,0]
	v_pk_add_f32 v[138:139], v[114:115], v[114:115] op_sel_hi:[0,1]
	v_pk_mul_f32 v[114:115], v[112:113], v[78:79] op_sel_hi:[1,0]
	v_pk_mul_f32 v[112:113], v[140:141], v[78:79] op_sel_hi:[1,0]
	s_waitcnt vmcnt(4)
	v_pk_fma_f32 v[114:115], v[30:31], v[114:115], v[34:35]
	v_pk_fma_f32 v[112:113], v[32:33], v[112:113], v[36:37]
	v_mov_b32_e32 v140, v114
	v_mov_b32_e32 v141, v113
	v_pk_mov_b32 v[202:203], v[114:115], v[112:113] op_sel:[1,0]
	v_pk_mul_f32 v[104:105], v[104:105], v[78:79] op_sel_hi:[1,0]
	v_pk_add_f32 v[140:141], v[140:141], v[202:203]
	v_pk_mul_f32 v[202:203], v[108:109], v[78:79] op_sel_hi:[1,0]
	v_pk_mul_f32 v[108:109], v[110:111], v[78:79] op_sel_hi:[1,0]
	v_pk_add_f32 v[140:141], v[140:141], v[140:141] op_sel_hi:[0,1]
	s_waitcnt vmcnt(1)
	v_pk_fma_f32 v[108:109], v[24:25], v[108:109], v[28:29]
	v_pk_fma_f32 v[110:111], v[22:23], v[202:203], v[26:27]
	s_waitcnt vmcnt(0)
	v_pk_fma_f32 v[104:105], v[16:17], v[104:105], v[20:21]
	v_pk_fma_f32 v[106:107], v[14:15], v[136:137], v[18:19]
	v_add_f32_e32 v203, v110, v111
	v_add_f32_e32 v205, v109, v108
	v_mov_b32_e32 v202, v106
	v_mov_b32_e32 v204, v107
	v_mov_b32_e32 v140, v105
	v_mov_b32_e32 v138, v104
	v_pk_add_f32 v[136:137], v[202:203], v[204:205]
	v_pk_add_f32 v[138:139], v[140:141], v[138:139]
	v_cvt_pk_bf16_f32 v208, v134, v135
	v_cvt_pk_bf16_f32 v209, v132, v133
	global_store_dwordx2 v146, v[208:209], s[0:1]
	v_pk_add_f32 v[136:137], v[136:137], v[138:139]
	s_nop 0
	v_add_f32_e32 v78, v136, v137
	ds_bpermute_b32 v137, v1, v78
	v_cvt_pk_bf16_f32 v136, v130, v131
	s_waitcnt lgkmcnt(0)
	v_add_f32_e32 v78, v78, v137
	ds_bpermute_b32 v138, v142, v78
	v_cvt_pk_bf16_f32 v137, v128, v129
	global_store_dwordx2 v146, v[136:137], s[0:1] offset:512
	v_cvt_pk_bf16_f32 v136, v126, v127
	v_cvt_pk_bf16_f32 v137, v124, v125
	s_waitcnt lgkmcnt(0)
; __device__ __forceinline__ unsigned cvt_pk_bf16(float lo, float hi) { unsigned r; asm volatile("v_cvt_pk_bf16_f32 %0, %1, %2" : "=v"(r) : "v"(lo), "v"(hi)); return r; }
; __device__ __forceinline__ void p6_router(Frame& F) {
;     ...
;                 for (int j = 0; j < 8; ++j) { v[j] = v[j] * rstd * pw[j] + pb[j]; { u32x2 xb; xb.x = cvt_pk_bf16(v[j][0], v[j][1]); xb.y = cvt_pk_bf16(v[j][2], v[j][3]); ((u32x2*)(X1 + (size_t)t * DM))[lane + 64 * j] = xb; } s += (v[j][0] + v[j][1]) + (v[j][2] + v[j][3]); }
;                 mean = wave_sum(s) * (1.f / DM); s2 = 0.f;
; #pragma unroll
;                 for (int j = 0; j < 8; ++j) { v[j] = v[j] - mean; s2 += (v[j][0] * v[j][0] + v[j][1] * v[j][1]) + (v[j][2] * v[j][2] + v[j][3] * v[j][3]); }
;                 rstd = 1.f / sqrtf(wave_sum(s2) * (1.f / DM) + LN_EPS);
;                 int loq = lane; asm volatile("" : "+v"(loq));
; #pragma unroll
;                 for (int j = 0; j < 8; ++j) { const f32x4 sh = ((const f32x4*)(mod + (size_t)b * 12288 + 6144))[loq + 64 * j], sc = ((const f32x4*)(mod + (size_t)b * 12288 + 8192))[loq + 64 * j];
	v_add_f32_e32 v78, v78, v138
	ds_bpermute_b32 v138, v143, v78
	global_store_dwordx2 v146, v[136:137], s[0:1] offset:1024
	v_cvt_pk_bf16_f32 v136, v122, v123
	v_cvt_pk_bf16_f32 v137, v120, v121
	global_store_dwordx2 v146, v[136:137], s[0:1] offset:1536
	s_waitcnt lgkmcnt(0)
	v_add_f32_e32 v78, v78, v138
	ds_bpermute_b32 v138, v144, v78
	v_cvt_pk_bf16_f32 v136, v118, v119
	v_cvt_pk_bf16_f32 v137, v116, v117
	global_store_dwordx2 v146, v[136:137], s[0:1] offset:2048
	v_cvt_pk_bf16_f32 v136, v114, v115
	s_waitcnt lgkmcnt(0)
	v_add_f32_e32 v78, v78, v138
	ds_bpermute_b32 v138, v145, v78
	v_cvt_pk_bf16_f32 v137, v112, v113
	global_store_dwordx2 v146, v[136:137], s[0:1] offset:2560
	v_cvt_pk_bf16_f32 v136, v110, v111
	v_cvt_pk_bf16_f32 v137, v108, v109
	s_waitcnt lgkmcnt(0)
	v_add_f32_e32 v78, v78, v138
	ds_bpermute_b32 v138, v147, v78
	global_store_dwordx2 v146, v[136:137], s[0:1] offset:3072
	v_cvt_pk_bf16_f32 v136, v106, v107
	v_cvt_pk_bf16_f32 v137, v104, v105
	global_store_dwordx2 v146, v[136:137], s[0:1] offset:3584
	s_waitcnt lgkmcnt(0)
	v_add_f32_e32 v204, v78, v138
	v_fmamk_f32 v135, v204, 0xba000000, v135
	v_fmamk_f32 v131, v204, 0xba000000, v131
	v_fmamk_f32 v133, v204, 0xba000000, v133
	v_fmac_f32_e32 v134, 0xba000000, v204
	v_fmamk_f32 v129, v204, 0xba000000, v129
	v_fmac_f32_e32 v130, 0xba000000, v204
	v_mov_b32_e32 v138, v135
	v_mov_b32_e32 v139, v131
	v_fmac_f32_e32 v132, 0xba000000, v204
	v_fmac_f32_e32 v128, 0xba000000, v204
	v_mov_b32_e32 v136, v134
	v_mov_b32_e32 v137, v130
	v_pk_mul_f32 v[138:139], v[138:139], v[138:139]
	v_mov_b32_e32 v140, v133
	v_mov_b32_e32 v141, v129
	v_pk_fma_f32 v[136:137], v[136:137], v[136:137], v[138:139]
	v_mov_b32_e32 v138, v132
	v_mov_b32_e32 v139, v128
	v_pk_mul_f32 v[140:141], v[140:141], v[140:141]
	v_fmamk_f32 v127, v204, 0xba000000, v127
	v_pk_fma_f32 v[138:139], v[138:139], v[138:139], v[140:141]
	v_fmac_f32_e32 v126, 0xba000000, v204
	v_fmamk_f32 v125, v204, 0xba000000, v125
	v_fmac_f32_e32 v124, 0xba000000, v204
	v_pk_add_f32 v[136:137], v[136:137], v[138:139]
	v_pk_mul_f32 v[138:139], v[124:125], v[124:125]
	v_pk_mul_f32 v[140:141], v[126:127], v[126:127]
	v_fmac_f32_e32 v122, 0xba000000, v204
	v_pk_mov_b32 v[202:203], v[140:141], v[138:139] op_sel:[1,0]
	v_mov_b32_e32 v141, v139
	v_fmamk_f32 v123, v204, 0xba000000, v123
	v_fmac_f32_e32 v120, 0xba000000, v204
	v_mul_f32_e32 v78, v122, v122
	v_pk_add_f32 v[138:139], v[202:203], v[140:141]
	v_fmamk_f32 v121, v204, 0xba000000, v121
	v_pk_fma_f32 v[140:141], v[122:123], v[122:123], v[78:79] op_sel_hi:[1,1,0]
	v_mul_f32_e32 v78, v120, v120
	v_pk_add_f32 v[136:137], v[136:137], v[136:137] op_sel_hi:[0,1]
	v_pk_add_f32 v[138:139], v[138:139], v[138:139] op_sel_hi:[0,1]
	v_pk_fma_f32 v[202:203], v[120:121], v[120:121], v[78:79] op_sel_hi:[1,1,0]
	v_fmamk_f32 v117, v204, 0xba000000, v117
	v_fmac_f32_e32 v116, 0xba000000, v204
	v_fmamk_f32 v119, v204, 0xba000000, v119
	v_fmac_f32_e32 v118, 0xba000000, v204
	v_mul_f32_e32 v140, v118, v118
	v_mul_f32_e32 v202, v119, v119
	v_mul_f32_e32 v138, v116, v116
	v_mul_f32_e32 v136, v117, v117
	v_pk_add_f32 v[140:141], v[140:141], v[202:203]
	v_pk_add_f32 v[136:137], v[138:139], v[136:137]
	v_fmamk_f32 v115, v204, 0xba000000, v115
	v_pk_add_f32 v[136:137], v[140:141], v[136:137]
	v_fmac_f32_e32 v114, 0xba000000, v204
	v_fmamk_f32 v113, v204, 0xba000000, v113
	v_fmac_f32_e32 v112, 0xba000000, v204
	v_pk_add_f32 v[140:141], v[136:137], v[136:137] op_sel_hi:[0,1]
	v_pk_mul_f32 v[136:137], v[112:113], v[112:113]
	v_pk_mul_f32 v[138:139], v[114:115], v[114:115]
	v_fmac_f32_e32 v110, 0xba000000, v204
	v_pk_mov_b32 v[202:203], v[138:139], v[136:137] op_sel:[1,0]
	v_mov_b32_e32 v139, v137
	v_pk_add_f32 v[136:137], v[202:203], v[138:139]
	v_fmamk_f32 v111, v204, 0xba000000, v111
	v_fmac_f32_e32 v108, 0xba000000, v204
	v_mul_f32_e32 v78, v110, v110
	v_pk_add_f32 v[206:207], v[136:137], v[136:137] op_sel_hi:[0,1]
	v_fmamk_f32 v109, v204, 0xba000000, v109
	v_pk_fma_f32 v[136:137], v[110:111], v[110:111], v[78:79] op_sel_hi:[1,1,0]
	v_mul_f32_e32 v78, v108, v108
	v_pk_fma_f32 v[138:139], v[108:109], v[108:109], v[78:79] op_sel_hi:[1,1,0]
	v_fmamk_f32 v107, v204, 0xba000000, v107
	v_fmac_f32_e32 v106, 0xba000000, v204
	v_mul_f32_e32 v136, v106, v106
	v_mul_f32_e32 v138, v107, v107
	v_pk_add_f32 v[208:209], v[136:137], v[138:139]
	v_mov_b32_e32 v136, v170
	v_fmamk_f32 v105, v204, 0xba000000, v105
	v_ashrrev_i32_e32 v137, 31, v136
	v_lshlrev_b64 v[136:137], 4, v[136:137]
	v_lshl_add_u64 v[210:211], s[16:17], 0, v[136:137]
	v_fmac_f32_e32 v104, 0xba000000, v204
	v_lshl_add_u64 v[212:213], s[20:21], 0, v[136:137]
	global_load_dwordx4 v[136:139], v[210:211], off
	global_load_dwordx4 v[202:205], v[212:213], off
	v_mul_f32_e32 v206, v104, v104
	v_mul_f32_e32 v140, v105, v105
	v_pk_add_f32 v[140:141], v[206:207], v[140:141]
	s_waitcnt vmcnt(0)
	v_pk_add_f32 v[202:203], v[202:203], 1.0 op_sel_hi:[1,0]
	v_pk_add_f32 v[140:141], v[208:209], v[140:141]
	s_nop 0
	v_add_f32_e32 v78, v140, v141
	ds_bpermute_b32 v140, v1, v78
	s_waitcnt lgkmcnt(0)
	v_add_f32_e32 v78, v78, v140
	ds_bpermute_b32 v140, v142, v78
	s_waitcnt lgkmcnt(0)
	v_add_f32_e32 v78, v78, v140
	ds_bpermute_b32 v140, v143, v78
	s_waitcnt lgkmcnt(0)
	v_add_f32_e32 v78, v78, v140
	ds_bpermute_b32 v140, v144, v78
	s_waitcnt lgkmcnt(0)
	v_add_f32_e32 v78, v78, v140
	ds_bpermute_b32 v140, v145, v78
	s_waitcnt lgkmcnt(0)
	v_add_f32_e32 v78, v78, v140
	ds_bpermute_b32 v140, v147, v78
	s_waitcnt lgkmcnt(0)
; #define LAS __attribute__((address_space(3)))
; __device__ __forceinline__ unsigned cvt_pk_bf16(float lo, float hi) { unsigned r; asm volatile("v_cvt_pk_bf16_f32 %0, %1, %2" : "=v"(r) : "v"(lo), "v"(hi)); return r; }
; __device__ __forceinline__ unsigned pk4_fp8(float a, float b, float c, float d) { int w = 0; w = __builtin_amdgcn_cvt_pk_fp8_f32(a, b, w, false); w = __builtin_amdgcn_cvt_pk_fp8_f32(c, d, w, true); return (unsigned)w; }
; __device__ __forceinline__ float bf_lo(unsigned w) { return __uint_as_float(w << 16); }
; __device__ __forceinline__ float bf_hi(unsigned w) { return __uint_as_float(w & 0xffff0000u); }
; __device__ __forceinline__ void p6_router(Frame& F) {
;     ...
;                 rstd = 1.f / sqrtf(wave_sum(s2) * (1.f / DM) + LN_EPS);
;                 int loq = lane; asm volatile("" : "+v"(loq));
; #pragma unroll
;                 for (int j = 0; j < 8; ++j) { const f32x4 sh = ((const f32x4*)(mod + (size_t)b * 12288 + 6144))[loq + 64 * j], sc = ((const f32x4*)(mod + (size_t)b * 12288 + 8192))[loq + 64 * j];
;                     const f32x4 y = v[j] * rstd * (sc + 1.0f) + sh;
;                     u32x2 wh; wh.x = cvt_pk_bf16(y[0], y[1]); wh.y = cvt_pk_bf16(y[2], y[3]);
;                     const f32x4 yl = {y[0] - bf_lo(wh.x), y[1] - bf_hi(wh.x), y[2] - bf_lo(wh.y), y[3] - bf_hi(wh.y)};
;                     u32x2 wl; wl.x = cvt_pk_bf16(yl[0], yl[1]); wl.y = cvt_pk_bf16(yl[2], yl[3]);
;                     { const int r = 2 * wave + q; LAS unsigned char* rowp = F.lds + r * 4096 + ((((lane >> 1) + 32 * j) ^ r) << 4) + (lane & 1) * 8;
;                       *(LAS u32x2*)rowp = wh; *(LAS u32x2*)(rowp + 65536) = wl; }
;                     U2F[(size_t)t * (DM / 4) + lane + 64 * j] = pk4_fp8(y[0], y[1], y[2], y[3]); }
	v_add_f32_e32 v78, v78, v140
	v_fmamk_f32 v78, v78, 0x3a000000, v148
	v_mul_f32_e32 v140, 0x4f800000, v78
	v_cmp_gt_f32_e32 vcc, s45, v78
	s_nop 1
	v_cndmask_b32_e32 v78, v78, v140, vcc
	v_sqrt_f32_e32 v140, v78
	s_nop 0
	v_add_u32_e32 v141, -1, v140
	v_fma_f32 v206, -v141, v140, v78
	v_cmp_ge_f32_e64 s[0:1], 0, v206
	v_add_u32_e32 v206, 1, v140
	s_nop 0
	v_cndmask_b32_e64 v141, v140, v141, s[0:1]
	v_fma_f32 v140, -v206, v140, v78
	v_cmp_lt_f32_e64 s[0:1], 0, v140
	s_nop 1
	v_cndmask_b32_e64 v140, v141, v206, s[0:1]
	v_mul_f32_e32 v141, 0x37800000, v140
	v_cndmask_b32_e32 v140, v140, v141, vcc
	v_cmp_class_f32_e32 vcc, v78, v149
	s_nop 1
	v_cndmask_b32_e32 v78, v140, v78, vcc
	v_div_scale_f32 v140, s[0:1], v78, v78, 1.0
	v_rcp_f32_e32 v141, v140
	s_lshl_b64 s[0:1], s[8:9], 11
	s_add_u32 s8, s40, s0
	s_addc_u32 s9, s44, s1
	v_fma_f32 v206, -v140, v141, 1.0
	v_fmac_f32_e32 v141, v206, v141
	v_div_scale_f32 v206, vcc, 1.0, v78, 1.0
	v_mul_f32_e32 v207, v206, v141
	v_fma_f32 v208, -v140, v207, v206
	v_fmac_f32_e32 v207, v208, v141
	v_fma_f32 v140, -v140, v207, v206
	v_div_fmas_f32 v140, v140, v141, v207
	v_div_fixup_f32 v78, v140, v78, 1.0
	v_pk_mul_f32 v[134:135], v[134:135], v[78:79] op_sel_hi:[1,0]
	v_pk_mul_f32 v[132:133], v[132:133], v[78:79] op_sel_hi:[1,0]
	v_pk_add_f32 v[140:141], v[204:205], 1.0 op_sel_hi:[1,0]
	v_pk_fma_f32 v[134:135], v[202:203], v[134:135], v[136:137]
	v_pk_fma_f32 v[132:133], v[140:141], v[132:133], v[138:139]
	v_mov_b32_e32 v139, v79
	v_cvt_pk_fp8_f32 v139, v134, v135
	v_cvt_pk_bf16_f32 v140, v134, v135
	v_cvt_pk_bf16_f32 v141, v132, v133
	v_pk_mul_f32 v[130:131], v[130:131], v[78:79] op_sel_hi:[1,0]
	v_cvt_pk_fp8_f32 v139, v132, v133 op_sel:[0,0,1]
	v_lshlrev_b32_e32 v136, 16, v140
	v_sub_f32_e32 v136, v134, v136
	v_and_b32_e32 v137, 0xffff0000, v140
	v_lshlrev_b32_e32 v138, 16, v141
	v_and_b32_e32 v134, 0xffff0000, v141
	v_sub_f32_e32 v137, v135, v137
	v_sub_f32_e32 v138, v132, v138
	v_sub_f32_e32 v134, v133, v134
	v_cvt_pk_bf16_f32 v202, v136, v137
	v_cvt_pk_bf16_f32 v203, v138, v134
	global_store_dword v150, v139, s[8:9]
	global_load_dwordx4 v[132:135], v[212:213], off offset:1024
	s_nop 0
	global_load_dwordx4 v[136:139], v[210:211], off offset:1024
	v_pk_mul_f32 v[128:129], v[128:129], v[78:79] op_sel_hi:[1,0]
	ds_write_b64 v159, v[140:141]
	ds_write_b64 v160, v[202:203]
	v_pk_mul_f32 v[126:127], v[126:127], v[78:79] op_sel_hi:[1,0]
	v_pk_mul_f32 v[124:125], v[124:125], v[78:79] op_sel_hi:[1,0]
	v_pk_mul_f32 v[122:123], v[122:123], v[78:79] op_sel_hi:[1,0]
	v_pk_mul_f32 v[120:121], v[120:121], v[78:79] op_sel_hi:[1,0]
	v_pk_mul_f32 v[118:119], v[118:119], v[78:79] op_sel_hi:[1,0]
	v_pk_mul_f32 v[116:117], v[116:117], v[78:79] op_sel_hi:[1,0]
	v_pk_mul_f32 v[112:113], v[112:113], v[78:79] op_sel_hi:[1,0]
	v_pk_mul_f32 v[110:111], v[110:111], v[78:79] op_sel_hi:[1,0]
	v_pk_mul_f32 v[108:109], v[108:109], v[78:79] op_sel_hi:[1,0]
	v_pk_mul_f32 v[106:107], v[106:107], v[78:79] op_sel_hi:[1,0]
	v_pk_mul_f32 v[104:105], v[104:105], v[78:79] op_sel_hi:[1,0]
	s_add_i32 s4, s4, 3
	s_ashr_i32 s5, s4, 31
	s_waitcnt vmcnt(1)
	v_pk_add_f32 v[134:135], v[134:135], 1.0 op_sel_hi:[1,0]
	v_pk_add_f32 v[132:133], v[132:133], 1.0 op_sel_hi:[1,0]
	s_waitcnt vmcnt(0)
	v_pk_fma_f32 v[128:129], v[134:135], v[128:129], v[138:139]
	v_pk_fma_f32 v[130:131], v[132:133], v[130:131], v[136:137]
	v_mov_b32_e32 v134, v79
	v_cvt_pk_fp8_f32 v134, v130, v131
	v_cvt_pk_bf16_f32 v136, v130, v131
	v_cvt_pk_bf16_f32 v137, v128, v129
	v_cvt_pk_fp8_f32 v134, v128, v129 op_sel:[0,0,1]
	v_lshlrev_b32_e32 v132, 16, v136
	v_and_b32_e32 v133, 0xffff0000, v136
	v_sub_f32_e32 v132, v130, v132
	v_sub_f32_e32 v133, v131, v133
	v_lshlrev_b32_e32 v130, 16, v137
	v_and_b32_e32 v131, 0xffff0000, v137
	v_sub_f32_e32 v130, v128, v130
	v_sub_f32_e32 v128, v129, v131
	v_cvt_pk_bf16_f32 v138, v132, v133
	v_cvt_pk_bf16_f32 v139, v130, v128
	global_store_dword v150, v134, s[8:9] offset:256
	global_load_dwordx4 v[128:131], v[212:213], off offset:2048
	s_nop 0
	global_load_dwordx4 v[132:135], v[210:211], off offset:2048
	ds_write_b64 v161, v[136:137]
	ds_write_b64 v162, v[138:139]
	v_and_b32_e32 v137, 0xffff0000, v102
	v_and_b32_e32 v136, 0xffff0000, v100
	s_waitcnt vmcnt(1)
	v_pk_add_f32 v[130:131], v[130:131], 1.0 op_sel_hi:[1,0]
	v_pk_add_f32 v[128:129], v[128:129], 1.0 op_sel_hi:[1,0]
	s_waitcnt vmcnt(0)
	v_pk_fma_f32 v[124:125], v[130:131], v[124:125], v[134:135]
	v_pk_fma_f32 v[126:127], v[128:129], v[126:127], v[132:133]
	v_mov_b32_e32 v130, v79
	v_cvt_pk_fp8_f32 v130, v126, v127
	v_cvt_pk_bf16_f32 v132, v126, v127
	v_cvt_pk_bf16_f32 v133, v124, v125
	v_cvt_pk_fp8_f32 v130, v124, v125 op_sel:[0,0,1]
	v_lshlrev_b32_e32 v128, 16, v132
	v_and_b32_e32 v129, 0xffff0000, v132
	v_sub_f32_e32 v128, v126, v128
	v_sub_f32_e32 v129, v127, v129
	v_lshlrev_b32_e32 v126, 16, v133
	v_and_b32_e32 v127, 0xffff0000, v133
	v_sub_f32_e32 v126, v124, v126
	v_sub_f32_e32 v124, v125, v127
	v_cvt_pk_bf16_f32 v134, v128, v129
	v_cvt_pk_bf16_f32 v135, v126, v124
	global_store_dword v150, v130, s[8:9] offset:512
	global_load_dwordx4 v[124:127], v[212:213], off offset:3072
	s_nop 0
	global_load_dwordx4 v[128:131], v[210:211], off offset:3072
	ds_write_b64 v165, v[132:133]
	ds_write_b64 v166, v[134:135]
	v_mov_b32_e32 v132, v79
	v_lshlrev_b32_e32 v135, 16, v102
	v_lshlrev_b32_e32 v134, 16, v100
	v_lshlrev_b32_e32 v133, 16, v103
	s_waitcnt vmcnt(1)
	v_pk_add_f32 v[126:127], v[126:127], 1.0 op_sel_hi:[1,0]
	v_pk_add_f32 v[124:125], v[124:125], 1.0 op_sel_hi:[1,0]
	s_waitcnt vmcnt(0)
; #define LAS __attribute__((address_space(3)))
; __device__ __forceinline__ unsigned cvt_pk_bf16(float lo, float hi) { unsigned r; asm volatile("v_cvt_pk_bf16_f32 %0, %1, %2" : "=v"(r) : "v"(lo), "v"(hi)); return r; }
; __device__ __forceinline__ unsigned pk4_fp8(float a, float b, float c, float d) { int w = 0; w = __builtin_amdgcn_cvt_pk_fp8_f32(a, b, w, false); w = __builtin_amdgcn_cvt_pk_fp8_f32(c, d, w, true); return (unsigned)w; }
; __device__ __forceinline__ float bf_lo(unsigned w) { return __uint_as_float(w << 16); }
; __device__ __forceinline__ float bf_hi(unsigned w) { return __uint_as_float(w & 0xffff0000u); }
; __device__ __forceinline__ void p6_router(Frame& F) {
;     ...
;                 for (int j = 0; j < 8; ++j) { const u32x2 zb = zr[q][j]; v[j] = (f32x4){bf_lo(zb.x), bf_hi(zb.x), bf_lo(zb.y), bf_hi(zb.y)}; s += (v[j][0] + v[j][1]) + (v[j][2] + v[j][3]); }
;                 float mean = wave_sum(s) * (1.f / DM), s2 = 0.f;
;     ...
;                 for (int j = 0; j < 8; ++j) { const f32x4 sh = ((const f32x4*)(mod + (size_t)b * 12288 + 6144))[loq + 64 * j], sc = ((const f32x4*)(mod + (size_t)b * 12288 + 8192))[loq + 64 * j];
;                     const f32x4 y = v[j] * rstd * (sc + 1.0f) + sh;
;                     u32x2 wh; wh.x = cvt_pk_bf16(y[0], y[1]); wh.y = cvt_pk_bf16(y[2], y[3]);
;                     const f32x4 yl = {y[0] - bf_lo(wh.x), y[1] - bf_hi(wh.x), y[2] - bf_lo(wh.y), y[3] - bf_hi(wh.y)};
;                     u32x2 wl; wl.x = cvt_pk_bf16(yl[0], yl[1]); wl.y = cvt_pk_bf16(yl[2], yl[3]);
;                     { const int r = 2 * wave + q; LAS unsigned char* rowp = F.lds + r * 4096 + ((((lane >> 1) + 32 * j) ^ r) << 4) + (lane & 1) * 8;
;                       *(LAS u32x2*)rowp = wh; *(LAS u32x2*)(rowp + 65536) = wl; }
;                     U2F[(size_t)t * (DM / 4) + lane + 64 * j] = pk4_fp8(y[0], y[1], y[2], y[3]); }
	v_pk_fma_f32 v[120:121], v[120:121], v[126:127], v[130:131]
	v_pk_fma_f32 v[122:123], v[122:123], v[124:125], v[128:129]
	v_mov_b32_e32 v126, v79
	v_cvt_pk_fp8_f32 v126, v122, v123
	v_cvt_pk_bf16_f32 v138, v122, v123
	v_cvt_pk_bf16_f32 v139, v120, v121
	v_cvt_pk_fp8_f32 v126, v120, v121 op_sel:[0,0,1]
	v_lshlrev_b32_e32 v124, 16, v138
	v_and_b32_e32 v125, 0xffff0000, v138
	v_sub_f32_e32 v124, v122, v124
	v_sub_f32_e32 v125, v123, v125
	v_lshlrev_b32_e32 v122, 16, v139
	v_and_b32_e32 v123, 0xffff0000, v139
	v_sub_f32_e32 v122, v120, v122
	v_sub_f32_e32 v120, v121, v123
	v_cvt_pk_bf16_f32 v140, v124, v125
	v_cvt_pk_bf16_f32 v141, v122, v120
	v_add_co_u32_e32 v120, vcc, s41, v212
	global_store_dword v150, v126, s[8:9] offset:768
	s_nop 0
	v_addc_co_u32_e32 v121, vcc, 0, v213, vcc
	v_add_co_u32_e32 v122, vcc, s41, v210
	global_load_dwordx4 v[124:127], v[120:121], off
	s_nop 0
	v_addc_co_u32_e32 v123, vcc, 0, v211, vcc
	global_load_dwordx4 v[128:131], v[122:123], off
	ds_write_b64 v155, v[138:139]
	ds_write_b64 v156, v[140:141]
	v_and_b32_e32 v139, 0xffff0000, v103
	v_and_b32_e32 v138, 0xffff0000, v101
	v_and_b32_e32 v211, 0xffff0000, v99
	v_and_b32_e32 v210, 0xffff0000, v98
	s_waitcnt vmcnt(1)
	v_pk_add_f32 v[124:125], v[124:125], 1.0 op_sel_hi:[1,0]
	v_pk_add_f32 v[126:127], v[126:127], 1.0 op_sel_hi:[1,0]
	s_waitcnt vmcnt(0)
	v_pk_fma_f32 v[118:119], v[118:119], v[124:125], v[128:129]
	s_nop 0
	v_cvt_pk_fp8_f32 v132, v118, v119
	v_pk_fma_f32 v[116:117], v[116:117], v[126:127], v[130:131]
	v_cvt_pk_bf16_f32 v140, v118, v119
	v_lshlrev_b32_e32 v131, 16, v99
	v_cvt_pk_fp8_f32 v132, v116, v117 op_sel:[0,0,1]
	v_cvt_pk_bf16_f32 v141, v116, v117
	v_lshlrev_b32_e32 v100, 16, v140
	v_and_b32_e32 v102, 0xffff0000, v140
	v_lshlrev_b32_e32 v124, 16, v141
	v_and_b32_e32 v125, 0xffff0000, v141
	v_sub_f32_e32 v100, v118, v100
	v_sub_f32_e32 v102, v119, v102
	v_sub_f32_e32 v118, v116, v124
	v_sub_f32_e32 v116, v117, v125
	v_cvt_pk_bf16_f32 v160, v100, v102
	v_cvt_pk_bf16_f32 v161, v118, v116
	global_store_dword v150, v132, s[8:9] offset:1024
	global_load_dwordx4 v[202:205], v[122:123], off offset:1024
	global_load_dwordx4 v[206:209], v[120:121], off offset:1024
	v_lshlrev_b32_e32 v132, 16, v101
	v_pk_add_f32 v[100:101], v[134:135], v[136:137]
	v_pk_add_f32 v[102:103], v[132:133], v[138:139]
	v_lshlrev_b32_e32 v130, 16, v98
	v_pk_add_f32 v[100:101], v[100:101], v[102:103]
	v_pk_add_f32 v[98:99], v[130:131], v[210:211]
	v_add_f32_e32 v100, 0, v100
	v_add_f32_e32 v100, v100, v101
	v_lshlrev_b32_e32 v126, 16, v96
	v_and_b32_e32 v127, 0xffff0000, v96
	v_lshlrev_b32_e32 v128, 16, v97
	v_and_b32_e32 v129, 0xffff0000, v97
	v_lshlrev_b32_e32 v101, 16, v94
	v_and_b32_e32 v125, 0xffff0000, v94
	v_lshlrev_b32_e32 v119, 16, v95
	v_and_b32_e32 v117, 0xffff0000, v95
	v_pk_add_f32 v[94:95], v[98:99], v[98:99] op_sel:[0,1] op_sel_hi:[1,0]
	v_add_f32_e32 v118, v126, v127
	v_add_f32_e32 v116, v128, v129
	v_mov_b32_e32 v95, v125
	v_pk_add_f32 v[94:95], v[100:101], v[94:95]
	v_pk_add_f32 v[96:97], v[118:119], v[116:117]
	v_lshlrev_b32_e32 v103, 16, v93
	v_lshlrev_b32_e32 v102, 16, v92
	v_pk_add_f32 v[212:213], v[94:95], v[96:97]
	v_pk_add_f32 v[216:217], v[102:103], v[214:215]
	v_lshlrev_b32_e32 v96, 16, v90
	v_and_b32_e32 v97, 0xffff0000, v90
	v_lshlrev_b32_e32 v98, 16, v91
	v_and_b32_e32 v99, 0xffff0000, v91
	v_lshlrev_b32_e32 v94, 16, v88
	v_and_b32_e32 v95, 0xffff0000, v88
	v_lshlrev_b32_e32 v93, 16, v89
	v_and_b32_e32 v91, 0xffff0000, v89
	v_pk_add_f32 v[88:89], v[212:213], v[212:213] op_sel:[0,1] op_sel_hi:[1,0]
	v_pk_add_f32 v[212:213], v[216:217], v[216:217] op_sel:[0,1] op_sel_hi:[1,0]
	v_add_f32_e32 v92, v96, v97
	v_add_f32_e32 v90, v98, v99
	v_mov_b32_e32 v89, v94
	v_mov_b32_e32 v213, v95
	v_pk_add_f32 v[88:89], v[88:89], v[212:213]
	v_pk_add_f32 v[212:213], v[92:93], v[90:91]
	ds_write_b64 v169, v[140:141]
	ds_write_b64 v171, v[160:161]
	v_pk_add_f32 v[88:89], v[88:89], v[212:213]
	v_mov_b32_e32 v90, v79
	v_add_f32_e32 v88, v88, v89
	ds_bpermute_b32 v89, v1, v88
	s_waitcnt lgkmcnt(0)
	v_add_f32_e32 v88, v88, v89
	ds_bpermute_b32 v89, v142, v88
	s_waitcnt lgkmcnt(0)
	v_add_f32_e32 v88, v88, v89
	ds_bpermute_b32 v89, v143, v88
	s_waitcnt lgkmcnt(0)
	v_add_f32_e32 v88, v88, v89
	ds_bpermute_b32 v89, v144, v88
	s_waitcnt lgkmcnt(0)
	v_add_f32_e32 v92, v88, v89
	v_pk_mul_f32 v[88:89], v[114:115], v[78:79] op_sel_hi:[1,0]
	ds_bpermute_b32 v100, v145, v92
	s_waitcnt vmcnt(0)
	v_pk_add_f32 v[140:141], v[206:207], 1.0 op_sel_hi:[1,0]
	s_nop 0
	v_pk_fma_f32 v[88:89], v[88:89], v[140:141], v[202:203]
	v_pk_add_f32 v[114:115], v[208:209], 1.0 op_sel_hi:[1,0]
	v_cvt_pk_fp8_f32 v90, v88, v89
	v_pk_fma_f32 v[112:113], v[112:113], v[114:115], v[204:205]
	v_cvt_pk_bf16_f32 v140, v88, v89
	s_nop 0
	v_cvt_pk_fp8_f32 v90, v112, v113 op_sel:[0,0,1]
	v_cvt_pk_bf16_f32 v141, v112, v113
	v_lshlrev_b32_e32 v114, 16, v140
	v_and_b32_e32 v115, 0xffff0000, v140
	v_lshlrev_b32_e32 v116, 16, v141
	v_and_b32_e32 v118, 0xffff0000, v141
	v_sub_f32_e32 v88, v88, v114
	v_sub_f32_e32 v89, v89, v115
	v_sub_f32_e32 v114, v112, v116
	v_sub_f32_e32 v112, v113, v118
	v_cvt_pk_bf16_f32 v160, v88, v89
	v_cvt_pk_bf16_f32 v161, v114, v112
	global_store_dword v150, v90, s[8:9] offset:1280
	global_load_dwordx4 v[112:115], v[120:121], off offset:2048
	global_load_dwordx4 v[202:205], v[122:123], off offset:2048
	s_waitcnt lgkmcnt(0)
	v_add_f32_e32 v88, v92, v100
	ds_bpermute_b32 v89, v147, v88
	v_mov_b32_e32 v118, v79
	ds_write_b64 v152, v[140:141]
	ds_write_b64 v153, v[160:161]
	s_waitcnt lgkmcnt(2)
; #define LAS __attribute__((address_space(3)))
; __device__ __forceinline__ unsigned cvt_pk_bf16(float lo, float hi) { unsigned r; asm volatile("v_cvt_pk_bf16_f32 %0, %1, %2" : "=v"(r) : "v"(lo), "v"(hi)); return r; }
; __device__ __forceinline__ unsigned pk4_fp8(float a, float b, float c, float d) { int w = 0; w = __builtin_amdgcn_cvt_pk_fp8_f32(a, b, w, false); w = __builtin_amdgcn_cvt_pk_fp8_f32(c, d, w, true); return (unsigned)w; }
; __device__ __forceinline__ float bf_lo(unsigned w) { return __uint_as_float(w << 16); }
; __device__ __forceinline__ float bf_hi(unsigned w) { return __uint_as_float(w & 0xffff0000u); }
; __device__ __forceinline__ void p6_router(Frame& F) {
;     ...
;                 float mean = wave_sum(s) * (1.f / DM), s2 = 0.f;
; #pragma unroll
;                 for (int j = 0; j < 8; ++j) { v[j] = v[j] - mean; s2 += (v[j][0] * v[j][0] + v[j][1] * v[j][1]) + (v[j][2] * v[j][2] + v[j][3] * v[j][3]); }
;                 float rstd = 1.f / sqrtf(wave_sum(s2) * (1.f / DM) + LN_EPS);
;     ...
;                     const f32x4 y = v[j] * rstd * (sc + 1.0f) + sh;
;                     u32x2 wh; wh.x = cvt_pk_bf16(y[0], y[1]); wh.y = cvt_pk_bf16(y[2], y[3]);
;                     const f32x4 yl = {y[0] - bf_lo(wh.x), y[1] - bf_hi(wh.x), y[2] - bf_lo(wh.y), y[3] - bf_hi(wh.y)};
;                     u32x2 wl; wl.x = cvt_pk_bf16(yl[0], yl[1]); wl.y = cvt_pk_bf16(yl[2], yl[3]);
;                     { const int r = 2 * wave + q; LAS unsigned char* rowp = F.lds + r * 4096 + ((((lane >> 1) + 32 * j) ^ r) << 4) + (lane & 1) * 8;
;                       *(LAS u32x2*)rowp = wh; *(LAS u32x2*)(rowp + 65536) = wl; }
;                     U2F[(size_t)t * (DM / 4) + lane + 64 * j] = pk4_fp8(y[0], y[1], y[2], y[3]); }
	v_add_f32_e32 v124, v88, v89
	v_fmac_f32_e32 v126, 0xba000000, v124
	v_fmac_f32_e32 v128, 0xba000000, v124
	v_fmac_f32_e32 v96, 0xba000000, v124
	v_fmac_f32_e32 v127, 0xba000000, v124
	v_fmac_f32_e32 v129, 0xba000000, v124
	v_fmac_f32_e32 v101, 0xba000000, v124
	v_fmac_f32_e32 v97, 0xba000000, v124
	v_mul_f32_e32 v90, v126, v126
	v_mul_f32_e32 v92, v128, v128
	v_mul_f32_e32 v100, v96, v96
	v_pk_fma_f32 v[216:217], v[126:127], v[126:127], v[90:91] op_sel_hi:[1,1,0]
	v_pk_fma_f32 v[218:219], v[128:129], v[128:129], v[92:93] op_sel_hi:[1,1,0]
	v_pk_fma_f32 v[224:225], v[96:97], v[96:97], v[100:101] op_sel_hi:[1,1,0]
	v_fmac_f32_e32 v138, 0xba000000, v124
	v_fmac_f32_e32 v136, 0xba000000, v124
	v_fmac_f32_e32 v139, 0xba000000, v124
	v_fmac_f32_e32 v137, 0xba000000, v124
	v_fmac_f32_e32 v210, 0xba000000, v124
	v_fmac_f32_e32 v211, 0xba000000, v124
	v_fmac_f32_e32 v131, 0xba000000, v124
	v_fmac_f32_e32 v132, 0xba000000, v124
	v_fmac_f32_e32 v134, 0xba000000, v124
	v_fmac_f32_e32 v133, 0xba000000, v124
	v_fmac_f32_e32 v135, 0xba000000, v124
	v_fmac_f32_e32 v130, 0xba000000, v124
	v_fmac_f32_e32 v214, 0xba000000, v124
	v_fmac_f32_e32 v215, 0xba000000, v124
	v_fmac_f32_e32 v103, 0xba000000, v124
	v_pk_mul_f32 v[206:207], v[136:137], v[136:137]
	v_pk_mul_f32 v[208:209], v[138:139], v[138:139]
	v_mov_b32_e32 v212, v131
	v_mov_b32_e32 v213, v211
	v_mov_b32_e32 v131, v210
	v_mov_b32_e32 v88, v103
	v_mov_b32_e32 v89, v215
	v_mov_b32_e32 v103, v214
	v_pk_fma_f32 v[206:207], v[134:135], v[134:135], v[206:207]
	v_pk_fma_f32 v[208:209], v[132:133], v[132:133], v[208:209]
	v_pk_mul_f32 v[210:211], v[212:213], v[212:213]
	v_pk_mul_f32 v[214:215], v[130:131], v[130:131]
	v_pk_add_f32 v[206:207], v[206:207], v[208:209]
	v_pk_mov_b32 v[208:209], v[214:215], v[210:211] op_sel:[1,0]
	v_mov_b32_e32 v215, v211
	v_pk_add_f32 v[208:209], v[208:209], v[214:215]
	v_fmac_f32_e32 v117, 0xba000000, v124
	v_fmac_f32_e32 v119, 0xba000000, v124
	v_fmac_f32_e32 v125, 0xba000000, v124
	v_fmac_f32_e32 v102, 0xba000000, v124
	v_pk_add_f32 v[206:207], v[206:207], v[206:207] op_sel_hi:[0,1]
	v_pk_add_f32 v[208:209], v[208:209], v[208:209] op_sel_hi:[0,1]
	v_pk_mul_f32 v[220:221], v[88:89], v[88:89]
	v_pk_mul_f32 v[222:223], v[102:103], v[102:103]
	v_mul_f32_e32 v216, v101, v101
	v_mul_f32_e32 v218, v125, v125
	v_mul_f32_e32 v206, v117, v117
	v_mul_f32_e32 v208, v119, v119
	v_fmac_f32_e32 v98, 0xba000000, v124
	v_pk_mov_b32 v[210:211], v[222:223], v[220:221] op_sel:[1,0]
	v_mov_b32_e32 v223, v221
	v_pk_add_f32 v[214:215], v[216:217], v[218:219]
	v_pk_add_f32 v[206:207], v[208:209], v[206:207]
	v_fmac_f32_e32 v99, 0xba000000, v124
	v_mul_f32_e32 v116, v98, v98
	v_pk_add_f32 v[210:211], v[210:211], v[222:223]
	v_pk_add_f32 v[206:207], v[214:215], v[206:207]
	v_pk_add_f32 v[210:211], v[210:211], v[210:211] op_sel_hi:[0,1]
	v_pk_add_f32 v[206:207], v[206:207], v[206:207] op_sel_hi:[0,1]
	v_fmac_f32_e32 v91, 0xba000000, v124
	v_fmac_f32_e32 v93, 0xba000000, v124
	v_fmac_f32_e32 v95, 0xba000000, v124
	v_fmac_f32_e32 v94, 0xba000000, v124
	s_waitcnt vmcnt(1)
	v_pk_add_f32 v[112:113], v[112:113], 1.0 op_sel_hi:[1,0]
	v_pk_add_f32 v[114:115], v[114:115], 1.0 op_sel_hi:[1,0]
	s_waitcnt vmcnt(0)
	v_pk_fma_f32 v[110:111], v[110:111], v[112:113], v[202:203]
	v_pk_fma_f32 v[108:109], v[108:109], v[114:115], v[204:205]
	v_cvt_pk_fp8_f32 v118, v110, v111
	v_cvt_pk_bf16_f32 v140, v110, v111
	v_cvt_pk_bf16_f32 v141, v108, v109
	v_mul_f32_e32 v224, v94, v94
	v_cvt_pk_fp8_f32 v118, v108, v109 op_sel:[0,0,1]
	v_lshlrev_b32_e32 v90, 16, v140
	v_and_b32_e32 v92, 0xffff0000, v140
	v_lshlrev_b32_e32 v100, 16, v141
	v_and_b32_e32 v112, 0xffff0000, v141
	v_sub_f32_e32 v90, v110, v90
	v_sub_f32_e32 v92, v111, v92
	v_sub_f32_e32 v100, v108, v100
	v_sub_f32_e32 v108, v109, v112
	v_cvt_pk_bf16_f32 v152, v90, v92
	v_cvt_pk_bf16_f32 v153, v100, v108
	global_store_dword v150, v118, s[8:9] offset:1536
	global_load_dwordx4 v[108:111], v[122:123], off offset:3072
	global_load_dwordx4 v[112:115], v[120:121], off offset:3072
	v_pk_fma_f32 v[120:121], v[98:99], v[98:99], v[116:117] op_sel_hi:[1,1,0]
	v_mul_f32_e32 v210, v93, v93
	v_mul_f32_e32 v120, v95, v95
	v_mul_f32_e32 v206, v91, v91
	v_pk_add_f32 v[120:121], v[224:225], v[120:121]
	v_pk_add_f32 v[122:123], v[210:211], v[206:207]
	v_mov_b32_e32 v100, v79
	v_pk_add_f32 v[120:121], v[120:121], v[122:123]
	v_mov_b32_e32 v122, v133
	v_add_f32_e32 v90, v120, v121
	ds_bpermute_b32 v92, v1, v90
	v_mov_b32_e32 v120, v135
	v_mov_b32_e32 v135, v136
	ds_write_b64 v163, v[140:141]
	ds_write_b64 v164, v[152:153]
	v_mov_b32_e32 v121, v137
	s_waitcnt lgkmcnt(2)
	v_add_f32_e32 v90, v90, v92
	ds_bpermute_b32 v92, v142, v90
	v_mov_b32_e32 v123, v139
	s_waitcnt lgkmcnt(0)
	v_add_f32_e32 v90, v90, v92
	ds_bpermute_b32 v92, v143, v90
	s_waitcnt lgkmcnt(0)
	v_add_f32_e32 v90, v90, v92
	ds_bpermute_b32 v92, v144, v90
	s_waitcnt lgkmcnt(0)
	v_add_f32_e32 v90, v90, v92
	ds_bpermute_b32 v92, v145, v90
	s_waitcnt lgkmcnt(0)
	v_add_f32_e32 v90, v90, v92
	ds_bpermute_b32 v92, v147, v90
	s_waitcnt lgkmcnt(0)
	v_add_f32_e32 v90, v90, v92
	v_fmamk_f32 v90, v90, 0x3a000000, v148
	v_mul_f32_e32 v92, 0x4f800000, v90
	v_cmp_gt_f32_e32 vcc, s45, v90
	s_waitcnt vmcnt(0)
; __device__ __forceinline__ unsigned cvt_pk_bf16(float lo, float hi) { unsigned r; asm volatile("v_cvt_pk_bf16_f32 %0, %1, %2" : "=v"(r) : "v"(lo), "v"(hi)); return r; }
; __device__ __forceinline__ void p6_router(Frame& F) {
;     ...
;                 float rstd = 1.f / sqrtf(wave_sum(s2) * (1.f / DM) + LN_EPS);
;                 s = 0.f;
; #pragma unroll
;                 for (int j = 0; j < 8; ++j) { v[j] = v[j] * rstd * pw[j] + pb[j]; { u32x2 xb; xb.x = cvt_pk_bf16(v[j][0], v[j][1]); xb.y = cvt_pk_bf16(v[j][2], v[j][3]); ((u32x2*)(X1 + (size_t)t * DM))[lane + 64 * j] = xb; } s += (v[j][0] + v[j][1]) + (v[j][2] + v[j][3]); }
;                 mean = wave_sum(s) * (1.f / DM); s2 = 0.f;
	v_pk_add_f32 v[112:113], v[112:113], 1.0 op_sel_hi:[1,0]
	v_cndmask_b32_e32 v90, v90, v92, vcc
	v_sqrt_f32_e32 v92, v90
	v_pk_fma_f32 v[106:107], v[106:107], v[112:113], v[108:109]
	v_pk_add_f32 v[114:115], v[114:115], 1.0 op_sel_hi:[1,0]
	v_cvt_pk_fp8_f32 v100, v106, v107
	v_add_u32_e32 v116, -1, v92
	v_add_u32_e32 v118, 1, v92
	v_fma_f32 v124, -v116, v92, v90
	v_fma_f32 v133, -v118, v92, v90
	v_cmp_ge_f32_e64 s[0:1], 0, v124
	v_pk_fma_f32 v[104:105], v[104:105], v[114:115], v[110:111]
	v_cvt_pk_bf16_f32 v108, v106, v107
	s_nop 0
	v_cndmask_b32_e64 v92, v92, v116, s[0:1]
	v_cmp_lt_f32_e64 s[0:1], 0, v133
	v_lshlrev_b32_e32 v78, 16, v108
	v_and_b32_e32 v110, 0xffff0000, v108
	v_cndmask_b32_e64 v92, v92, v118, s[0:1]
	v_mul_f32_e32 v116, 0x37800000, v92
	v_cndmask_b32_e32 v92, v92, v116, vcc
	v_cmp_class_f32_e32 vcc, v90, v149
	v_cvt_pk_bf16_f32 v109, v104, v105
	v_sub_f32_e32 v78, v106, v78
	v_lshlrev_b32_e32 v111, 16, v109
	v_cndmask_b32_e32 v90, v92, v90, vcc
	v_div_scale_f32 v92, s[0:1], v90, v90, 1.0
	v_rcp_f32_e32 v116, v92
	v_div_scale_f32 v118, vcc, 1.0, v90, 1.0
	v_sub_f32_e32 v106, v107, v110
	v_fma_f32 v124, -v92, v116, 1.0
	v_fmac_f32_e32 v116, v124, v116
	v_mul_f32_e32 v124, v118, v116
	v_fma_f32 v136, -v92, v124, v118
	v_fmac_f32_e32 v124, v136, v116
	v_fma_f32 v92, -v92, v124, v118
	v_div_fmas_f32 v92, v92, v116, v124
	v_and_b32_e32 v112, 0xffff0000, v109
	v_sub_f32_e32 v107, v104, v111
	v_cvt_pk_bf16_f32 v106, v78, v106
	v_div_fixup_f32 v78, v92, v90, 1.0
	v_mov_b32_e32 v133, v138
	v_sub_f32_e32 v110, v105, v112
	v_cvt_pk_fp8_f32 v100, v104, v105 op_sel:[0,0,1]
	v_cvt_pk_bf16_f32 v107, v107, v110
	v_pk_mul_f32 v[104:105], v[134:135], v[78:79] op_sel_hi:[1,0]
	ds_write_b64 v157, v[108:109]
	ds_write_b64 v158, v[106:107]
	v_pk_mul_f32 v[106:107], v[132:133], v[78:79] op_sel_hi:[1,0]
	v_pk_fma_f32 v[70:71], v[70:71], v[104:105], v[10:11]
	v_pk_mul_f32 v[10:11], v[120:121], v[78:79] op_sel_hi:[1,0]
	v_pk_fma_f32 v[72:73], v[72:73], v[106:107], v[12:13]
	v_pk_mul_f32 v[12:13], v[122:123], v[78:79] op_sel_hi:[1,0]
	v_pk_fma_f32 v[62:63], v[62:63], v[10:11], v[66:67]
	v_pk_fma_f32 v[64:65], v[64:65], v[12:13], v[68:69]
	v_mov_b32_e32 v10, v62
	v_mov_b32_e32 v11, v70
	v_mov_b32_e32 v12, v63
	v_mov_b32_e32 v13, v71
	v_pk_add_f32 v[10:11], v[10:11], v[12:13]
	v_mov_b32_e32 v12, v65
	v_mov_b32_e32 v13, v73
	v_mov_b32_e32 v66, v64
	v_mov_b32_e32 v67, v72
	v_pk_add_f32 v[12:13], v[12:13], v[66:67]
	v_pk_mul_f32 v[66:67], v[212:213], v[78:79] op_sel_hi:[1,0]
	v_pk_add_f32 v[10:11], v[10:11], v[12:13]
	v_pk_mul_f32 v[12:13], v[130:131], v[78:79] op_sel_hi:[1,0]
	v_pk_fma_f32 v[56:57], v[56:57], v[66:67], v[60:61]
	v_pk_fma_f32 v[54:55], v[54:55], v[12:13], v[58:59]
	v_mov_b32_e32 v13, v57
	v_mov_b32_e32 v12, v54
	v_pk_mov_b32 v[58:59], v[54:55], v[56:57] op_sel:[1,0]
	v_pk_mul_f32 v[60:61], v[128:129], v[78:79] op_sel_hi:[1,0]
	v_pk_add_f32 v[12:13], v[12:13], v[58:59]
	v_pk_mul_f32 v[58:59], v[126:127], v[78:79] op_sel_hi:[1,0]
	v_mov_b32_e32 v124, v101
	v_mov_b32_e32 v116, v119
	v_pk_fma_f32 v[48:49], v[48:49], v[60:61], v[52:53]
	v_pk_fma_f32 v[46:47], v[46:47], v[58:59], v[50:51]
	v_pk_mul_f32 v[58:59], v[124:125], v[78:79] op_sel_hi:[1,0]
	v_pk_mul_f32 v[60:61], v[116:117], v[78:79] op_sel_hi:[1,0]
	v_add_f32_e32 v11, 0, v11
	v_pk_add_f32 v[12:13], v[12:13], v[12:13] op_sel_hi:[0,1]
	v_pk_fma_f32 v[40:41], v[40:41], v[60:61], v[44:45]
	v_pk_fma_f32 v[38:39], v[38:39], v[58:59], v[42:43]
	v_add_f32_e32 v11, v10, v11
	v_add_f32_e32 v51, v46, v47
	v_add_f32_e32 v53, v49, v48
	v_mov_b32_e32 v50, v38
	v_mov_b32_e32 v52, v39
	v_mov_b32_e32 v12, v41
	v_mov_b32_e32 v10, v40
	v_pk_add_f32 v[42:43], v[50:51], v[52:53]
	v_pk_add_f32 v[10:11], v[12:13], v[10:11]
	v_pk_mul_f32 v[12:13], v[88:89], v[78:79] op_sel_hi:[1,0]
	v_pk_add_f32 v[10:11], v[42:43], v[10:11]
	v_pk_fma_f32 v[32:33], v[32:33], v[12:13], v[36:37]
	v_pk_add_f32 v[42:43], v[10:11], v[10:11] op_sel_hi:[0,1]
	v_pk_mul_f32 v[10:11], v[102:103], v[78:79] op_sel_hi:[1,0]
	v_mov_b32_e32 v90, v93
	v_pk_fma_f32 v[30:31], v[30:31], v[10:11], v[34:35]
	v_mov_b32_e32 v11, v33
	v_mov_b32_e32 v10, v30
	v_pk_mov_b32 v[12:13], v[30:31], v[32:33] op_sel:[1,0]
	s_lshl_b64 s[0:1], s[4:5], 12
	v_pk_add_f32 v[10:11], v[10:11], v[12:13]
	v_pk_mul_f32 v[12:13], v[98:99], v[78:79] op_sel_hi:[1,0]
	v_pk_add_f32 v[34:35], v[10:11], v[10:11] op_sel_hi:[0,1]
	v_pk_mul_f32 v[10:11], v[96:97], v[78:79] op_sel_hi:[1,0]
	v_pk_fma_f32 v[24:25], v[24:25], v[12:13], v[28:29]
	v_pk_fma_f32 v[22:23], v[22:23], v[10:11], v[26:27]
	v_pk_mul_f32 v[12:13], v[94:95], v[78:79] op_sel_hi:[1,0]
	v_pk_mul_f32 v[10:11], v[90:91], v[78:79] op_sel_hi:[1,0]
	v_pk_fma_f32 v[12:13], v[14:15], v[12:13], v[18:19]
	v_pk_fma_f32 v[10:11], v[16:17], v[10:11], v[20:21]
	v_add_f32_e32 v27, v22, v23
	v_add_f32_e32 v29, v25, v24
	v_mov_b32_e32 v26, v12
	v_mov_b32_e32 v28, v13
	v_mov_b32_e32 v34, v11
	v_mov_b32_e32 v42, v10
	v_pk_add_f32 v[14:15], v[26:27], v[28:29]
	v_pk_add_f32 v[16:17], v[34:35], v[42:43]
	s_add_u32 s0, s42, s0
	v_pk_add_f32 v[14:15], v[14:15], v[16:17]
	s_addc_u32 s1, s43, s1
	v_add_f32_e32 v15, v14, v15
	ds_bpermute_b32 v16, v1, v15
	global_store_dword v150, v100, s[8:9] offset:1792
	v_cvt_pk_bf16_f32 v104, v70, v71
	v_cvt_pk_bf16_f32 v105, v72, v73
	global_store_dwordx2 v146, v[104:105], s[0:1]
	s_waitcnt lgkmcnt(0)
	v_add_f32_e32 v16, v15, v16
	ds_bpermute_b32 v17, v142, v16
	v_cvt_pk_bf16_f32 v14, v62, v63
	v_cvt_pk_bf16_f32 v15, v64, v65
	global_store_dwordx2 v146, v[14:15], s[0:1] offset:512
	v_cvt_pk_bf16_f32 v14, v54, v55
	s_waitcnt lgkmcnt(0)
; __device__ __forceinline__ unsigned cvt_pk_bf16(float lo, float hi) { unsigned r; asm volatile("v_cvt_pk_bf16_f32 %0, %1, %2" : "=v"(r) : "v"(lo), "v"(hi)); return r; }
; __device__ __forceinline__ void p6_router(Frame& F) {
;     ...
;                 for (int j = 0; j < 8; ++j) { v[j] = v[j] * rstd * pw[j] + pb[j]; { u32x2 xb; xb.x = cvt_pk_bf16(v[j][0], v[j][1]); xb.y = cvt_pk_bf16(v[j][2], v[j][3]); ((u32x2*)(X1 + (size_t)t * DM))[lane + 64 * j] = xb; } s += (v[j][0] + v[j][1]) + (v[j][2] + v[j][3]); }
;                 mean = wave_sum(s) * (1.f / DM); s2 = 0.f;
; #pragma unroll
;                 for (int j = 0; j < 8; ++j) { v[j] = v[j] - mean; s2 += (v[j][0] * v[j][0] + v[j][1] * v[j][1]) + (v[j][2] * v[j][2] + v[j][3] * v[j][3]); }
;                 rstd = 1.f / sqrtf(wave_sum(s2) * (1.f / DM) + LN_EPS);
;                 int loq = lane; asm volatile("" : "+v"(loq));
; #pragma unroll
;                 for (int j = 0; j < 8; ++j) { const f32x4 sh = ((const f32x4*)(mod + (size_t)b * 12288 + 6144))[loq + 64 * j], sc = ((const f32x4*)(mod + (size_t)b * 12288 + 8192))[loq + 64 * j];
	v_add_f32_e32 v16, v16, v17
	ds_bpermute_b32 v17, v143, v16
	v_cvt_pk_bf16_f32 v15, v56, v57
	global_store_dwordx2 v146, v[14:15], s[0:1] offset:1024
	v_cvt_pk_bf16_f32 v14, v46, v47
	v_cvt_pk_bf16_f32 v15, v48, v49
	s_waitcnt lgkmcnt(0)
	v_add_f32_e32 v16, v16, v17
	ds_bpermute_b32 v17, v144, v16
	global_store_dwordx2 v146, v[14:15], s[0:1] offset:1536
	v_cvt_pk_bf16_f32 v14, v38, v39
	v_cvt_pk_bf16_f32 v15, v40, v41
	global_store_dwordx2 v146, v[14:15], s[0:1] offset:2048
	s_waitcnt lgkmcnt(0)
	v_add_f32_e32 v16, v16, v17
	ds_bpermute_b32 v17, v145, v16
	v_cvt_pk_bf16_f32 v14, v30, v31
	v_cvt_pk_bf16_f32 v15, v32, v33
	global_store_dwordx2 v146, v[14:15], s[0:1] offset:2560
	v_cvt_pk_bf16_f32 v14, v22, v23
	s_waitcnt lgkmcnt(0)
	v_add_f32_e32 v16, v16, v17
	ds_bpermute_b32 v17, v147, v16
	v_cvt_pk_bf16_f32 v15, v24, v25
	global_store_dwordx2 v146, v[14:15], s[0:1] offset:3072
	v_cvt_pk_bf16_f32 v14, v12, v13
	v_cvt_pk_bf16_f32 v15, v10, v11
	s_waitcnt lgkmcnt(0)
	v_add_f32_e32 v26, v16, v17
	v_fmamk_f32 v71, v26, 0xba000000, v71
	v_fmamk_f32 v63, v26, 0xba000000, v63
	v_fmamk_f32 v73, v26, 0xba000000, v73
	v_fmac_f32_e32 v70, 0xba000000, v26
	v_fmamk_f32 v65, v26, 0xba000000, v65
	v_fmac_f32_e32 v62, 0xba000000, v26
	v_mov_b32_e32 v16, v71
	v_mov_b32_e32 v17, v63
	global_store_dwordx2 v146, v[14:15], s[0:1] offset:3584
	v_fmac_f32_e32 v72, 0xba000000, v26
	v_fmac_f32_e32 v64, 0xba000000, v26
	v_mov_b32_e32 v14, v70
	v_mov_b32_e32 v15, v62
	v_pk_mul_f32 v[16:17], v[16:17], v[16:17]
	v_mov_b32_e32 v18, v73
	v_mov_b32_e32 v19, v65
	v_pk_fma_f32 v[14:15], v[14:15], v[14:15], v[16:17]
	v_mov_b32_e32 v16, v72
	v_mov_b32_e32 v17, v64
	v_pk_mul_f32 v[18:19], v[18:19], v[18:19]
	v_fmamk_f32 v55, v26, 0xba000000, v55
	v_pk_fma_f32 v[16:17], v[16:17], v[16:17], v[18:19]
	v_fmac_f32_e32 v54, 0xba000000, v26
	v_pk_add_f32 v[14:15], v[14:15], v[16:17]
	v_fmamk_f32 v57, v26, 0xba000000, v57
	v_fmac_f32_e32 v56, 0xba000000, v26
	v_pk_add_f32 v[14:15], v[14:15], v[14:15] op_sel_hi:[0,1]
	v_pk_mul_f32 v[16:17], v[56:57], v[56:57]
	v_pk_mul_f32 v[18:19], v[54:55], v[54:55]
	v_fmac_f32_e32 v46, 0xba000000, v26
	v_pk_mov_b32 v[20:21], v[18:19], v[16:17] op_sel:[1,0]
	v_mov_b32_e32 v19, v17
	v_fmamk_f32 v47, v26, 0xba000000, v47
	v_fmac_f32_e32 v48, 0xba000000, v26
	v_mul_f32_e32 v14, v46, v46
	v_pk_add_f32 v[16:17], v[20:21], v[18:19]
	v_fmamk_f32 v49, v26, 0xba000000, v49
	v_pk_fma_f32 v[18:19], v[46:47], v[46:47], v[14:15] op_sel_hi:[1,1,0]
	v_mul_f32_e32 v14, v48, v48
	v_pk_add_f32 v[16:17], v[16:17], v[16:17] op_sel_hi:[0,1]
	v_pk_fma_f32 v[20:21], v[48:49], v[48:49], v[14:15] op_sel_hi:[1,1,0]
	v_fmamk_f32 v41, v26, 0xba000000, v41
	v_fmac_f32_e32 v40, 0xba000000, v26
	v_fmamk_f32 v39, v26, 0xba000000, v39
	v_fmac_f32_e32 v38, 0xba000000, v26
	v_mul_f32_e32 v18, v38, v38
	v_mul_f32_e32 v20, v39, v39
	v_mul_f32_e32 v16, v40, v40
	v_mul_f32_e32 v14, v41, v41
	v_pk_add_f32 v[18:19], v[18:19], v[20:21]
	v_pk_add_f32 v[14:15], v[16:17], v[14:15]
	v_fmamk_f32 v31, v26, 0xba000000, v31
	v_fmac_f32_e32 v30, 0xba000000, v26
	v_fmamk_f32 v33, v26, 0xba000000, v33
	v_fmac_f32_e32 v32, 0xba000000, v26
	v_pk_add_f32 v[14:15], v[18:19], v[14:15]
	v_pk_mul_f32 v[16:17], v[32:33], v[32:33]
	v_pk_mul_f32 v[18:19], v[30:31], v[30:31]
	v_pk_add_f32 v[14:15], v[14:15], v[14:15] op_sel_hi:[0,1]
	v_pk_mov_b32 v[20:21], v[18:19], v[16:17] op_sel:[1,0]
	v_mov_b32_e32 v19, v17
	v_fmac_f32_e32 v22, 0xba000000, v26
	v_pk_add_f32 v[16:17], v[20:21], v[18:19]
	v_fmamk_f32 v23, v26, 0xba000000, v23
	v_fmac_f32_e32 v24, 0xba000000, v26
	v_mul_f32_e32 v14, v22, v22
	v_pk_add_f32 v[34:35], v[16:17], v[16:17] op_sel_hi:[0,1]
	v_fmamk_f32 v25, v26, 0xba000000, v25
	v_pk_fma_f32 v[16:17], v[22:23], v[22:23], v[14:15] op_sel_hi:[1,1,0]
	v_mul_f32_e32 v14, v24, v24
	v_pk_fma_f32 v[18:19], v[24:25], v[24:25], v[14:15] op_sel_hi:[1,1,0]
	v_fmamk_f32 v13, v26, 0xba000000, v13
	v_fmac_f32_e32 v12, 0xba000000, v26
	v_mul_f32_e32 v16, v12, v12
	v_mul_f32_e32 v18, v13, v13
	v_pk_add_f32 v[36:37], v[16:17], v[18:19]
	v_mov_b32_e32 v16, v170
	v_fmamk_f32 v11, v26, 0xba000000, v11
	v_ashrrev_i32_e32 v17, 31, v16
	v_lshlrev_b64 v[18:19], 4, v[16:17]
	v_lshl_add_u64 v[16:17], s[16:17], 0, v[18:19]
	v_fmac_f32_e32 v10, 0xba000000, v26
	v_lshl_add_u64 v[42:43], s[20:21], 0, v[18:19]
	global_load_dwordx4 v[18:21], v[16:17], off
	global_load_dwordx4 v[26:29], v[42:43], off
	v_mul_f32_e32 v34, v10, v10
	v_mul_f32_e32 v14, v11, v11
	v_pk_add_f32 v[14:15], v[34:35], v[14:15]
	s_waitcnt vmcnt(0)
	v_pk_add_f32 v[28:29], v[28:29], 1.0 op_sel_hi:[1,0]
	v_pk_add_f32 v[14:15], v[36:37], v[14:15]
	v_pk_add_f32 v[26:27], v[26:27], 1.0 op_sel_hi:[1,0]
	v_add_f32_e32 v14, v14, v15
	ds_bpermute_b32 v15, v1, v14
	s_waitcnt lgkmcnt(0)
	v_add_f32_e32 v14, v14, v15
	ds_bpermute_b32 v15, v142, v14
	s_waitcnt lgkmcnt(0)
	v_add_f32_e32 v14, v14, v15
	ds_bpermute_b32 v15, v143, v14
	s_waitcnt lgkmcnt(0)
	v_add_f32_e32 v14, v14, v15
	ds_bpermute_b32 v15, v144, v14
	s_waitcnt lgkmcnt(0)
	v_add_f32_e32 v14, v14, v15
	ds_bpermute_b32 v15, v145, v14
	s_waitcnt lgkmcnt(0)
	v_add_f32_e32 v14, v14, v15
	ds_bpermute_b32 v15, v147, v14
	s_waitcnt lgkmcnt(0)
; #define LAS __attribute__((address_space(3)))
; __device__ __forceinline__ unsigned cvt_pk_bf16(float lo, float hi) { unsigned r; asm volatile("v_cvt_pk_bf16_f32 %0, %1, %2" : "=v"(r) : "v"(lo), "v"(hi)); return r; }
; __device__ __forceinline__ unsigned pk4_fp8(float a, float b, float c, float d) { int w = 0; w = __builtin_amdgcn_cvt_pk_fp8_f32(a, b, w, false); w = __builtin_amdgcn_cvt_pk_fp8_f32(c, d, w, true); return (unsigned)w; }
; __device__ __forceinline__ float bf_lo(unsigned w) { return __uint_as_float(w << 16); }
; __device__ __forceinline__ float bf_hi(unsigned w) { return __uint_as_float(w & 0xffff0000u); }
; __device__ __forceinline__ void p6_router(Frame& F) {
;     ...
;                 rstd = 1.f / sqrtf(wave_sum(s2) * (1.f / DM) + LN_EPS);
;                 int loq = lane; asm volatile("" : "+v"(loq));
; #pragma unroll
;                 for (int j = 0; j < 8; ++j) { const f32x4 sh = ((const f32x4*)(mod + (size_t)b * 12288 + 6144))[loq + 64 * j], sc = ((const f32x4*)(mod + (size_t)b * 12288 + 8192))[loq + 64 * j];
;                     const f32x4 y = v[j] * rstd * (sc + 1.0f) + sh;
;                     u32x2 wh; wh.x = cvt_pk_bf16(y[0], y[1]); wh.y = cvt_pk_bf16(y[2], y[3]);
;                     const f32x4 yl = {y[0] - bf_lo(wh.x), y[1] - bf_hi(wh.x), y[2] - bf_lo(wh.y), y[3] - bf_hi(wh.y)};
;                     u32x2 wl; wl.x = cvt_pk_bf16(yl[0], yl[1]); wl.y = cvt_pk_bf16(yl[2], yl[3]);
;                     { const int r = 2 * wave + q; LAS unsigned char* rowp = F.lds + r * 4096 + ((((lane >> 1) + 32 * j) ^ r) << 4) + (lane & 1) * 8;
;                       *(LAS u32x2*)rowp = wh; *(LAS u32x2*)(rowp + 65536) = wl; }
;                     U2F[(size_t)t * (DM / 4) + lane + 64 * j] = pk4_fp8(y[0], y[1], y[2], y[3]); }
	v_add_f32_e32 v14, v14, v15
	v_fmac_f32_e32 v148, 0x3a000000, v14
	v_mul_f32_e32 v14, 0x4f800000, v148
	v_cmp_gt_f32_e32 vcc, s45, v148
	s_nop 1
	v_cndmask_b32_e32 v14, v148, v14, vcc
	v_sqrt_f32_e32 v15, v14
	s_nop 0
	v_add_u32_e32 v34, -1, v15
	v_fma_f32 v35, -v34, v15, v14
	v_cmp_ge_f32_e64 s[0:1], 0, v35
	v_add_u32_e32 v35, 1, v15
	s_nop 0
	v_cndmask_b32_e64 v34, v15, v34, s[0:1]
	v_fma_f32 v15, -v35, v15, v14
	v_cmp_lt_f32_e64 s[0:1], 0, v15
	s_nop 1
	v_cndmask_b32_e64 v15, v34, v35, s[0:1]
	v_mul_f32_e32 v34, 0x37800000, v15
	v_cndmask_b32_e32 v15, v15, v34, vcc
	v_cmp_class_f32_e32 vcc, v14, v149
	s_nop 1
	v_cndmask_b32_e32 v14, v15, v14, vcc
	v_div_scale_f32 v15, s[0:1], v14, v14, 1.0
	v_rcp_f32_e32 v34, v15
	s_lshl_b64 s[0:1], s[4:5], 11
	s_add_u32 s0, s40, s0
	s_addc_u32 s1, s44, s1
	v_fma_f32 v35, -v15, v34, 1.0
	v_fmac_f32_e32 v34, v35, v34
	v_div_scale_f32 v35, vcc, 1.0, v14, 1.0
	v_mul_f32_e32 v36, v35, v34
	v_fma_f32 v37, -v15, v36, v35
	v_fmac_f32_e32 v36, v37, v34
	v_fma_f32 v15, -v15, v36, v35
	v_div_fmas_f32 v15, v15, v34, v36
	v_div_fixup_f32 v14, v15, v14, 1.0
	v_pk_mul_f32 v[34:35], v[70:71], v[14:15] op_sel_hi:[1,0]
	v_pk_mul_f32 v[36:37], v[72:73], v[14:15] op_sel_hi:[1,0]
	v_pk_fma_f32 v[18:19], v[26:27], v[34:35], v[18:19]
	v_pk_fma_f32 v[20:21], v[28:29], v[36:37], v[20:21]
	v_mov_b32_e32 v28, v79
	v_cvt_pk_fp8_f32 v28, v18, v19
	v_cvt_pk_bf16_f32 v34, v18, v19
	v_cvt_pk_bf16_f32 v35, v20, v21
	v_cvt_pk_fp8_f32 v28, v20, v21 op_sel:[0,0,1]
	v_lshlrev_b32_e32 v15, 16, v34
	v_sub_f32_e32 v15, v18, v15
	v_and_b32_e32 v26, 0xffff0000, v34
	v_lshlrev_b32_e32 v27, 16, v35
	v_and_b32_e32 v18, 0xffff0000, v35
	v_sub_f32_e32 v26, v19, v26
	v_sub_f32_e32 v27, v20, v27
	v_sub_f32_e32 v18, v21, v18
	v_cvt_pk_bf16_f32 v36, v15, v26
	v_cvt_pk_bf16_f32 v37, v27, v18
	global_store_dword v150, v28, s[0:1]
	global_load_dwordx4 v[18:21], v[42:43], off offset:1024
	s_nop 0
	global_load_dwordx4 v[26:29], v[16:17], off offset:1024
	ds_write_b64 v172, v[34:35]
	ds_write_b64 v173, v[36:37]
	v_pk_mul_f32 v[34:35], v[62:63], v[14:15] op_sel_hi:[1,0]
	v_pk_mul_f32 v[36:37], v[64:65], v[14:15] op_sel_hi:[1,0]
	s_waitcnt vmcnt(1)
	v_pk_add_f32 v[18:19], v[18:19], 1.0 op_sel_hi:[1,0]
	s_waitcnt vmcnt(0)
	v_pk_fma_f32 v[18:19], v[18:19], v[34:35], v[26:27]
	v_mov_b32_e32 v27, v79
	v_cvt_pk_fp8_f32 v27, v18, v19
	v_pk_add_f32 v[20:21], v[20:21], 1.0 op_sel_hi:[1,0]
	v_cvt_pk_bf16_f32 v34, v18, v19
	s_nop 0
	v_pk_fma_f32 v[20:21], v[20:21], v[36:37], v[28:29]
	v_lshlrev_b32_e32 v15, 16, v34
	v_cvt_pk_fp8_f32 v27, v20, v21 op_sel:[0,0,1]
	v_and_b32_e32 v26, 0xffff0000, v34
	v_cvt_pk_bf16_f32 v35, v20, v21
	v_sub_f32_e32 v15, v18, v15
	v_sub_f32_e32 v26, v19, v26
	v_lshlrev_b32_e32 v18, 16, v35
	v_and_b32_e32 v19, 0xffff0000, v35
	v_sub_f32_e32 v18, v20, v18
	v_sub_f32_e32 v19, v21, v19
	v_cvt_pk_bf16_f32 v36, v15, v26
	v_cvt_pk_bf16_f32 v37, v18, v19
	global_store_dword v150, v27, s[0:1] offset:256
	global_load_dwordx4 v[18:21], v[42:43], off offset:2048
	s_nop 0
	global_load_dwordx4 v[26:29], v[16:17], off offset:2048
	ds_write_b64 v174, v[34:35]
	ds_write_b64 v175, v[36:37]
	v_pk_mul_f32 v[34:35], v[54:55], v[14:15] op_sel_hi:[1,0]
	v_pk_mul_f32 v[36:37], v[56:57], v[14:15] op_sel_hi:[1,0]
	s_waitcnt vmcnt(1)
	v_pk_add_f32 v[18:19], v[18:19], 1.0 op_sel_hi:[1,0]
	s_waitcnt vmcnt(0)
	v_pk_fma_f32 v[18:19], v[18:19], v[34:35], v[26:27]
	v_mov_b32_e32 v27, v79
	v_cvt_pk_fp8_f32 v27, v18, v19
	v_pk_add_f32 v[20:21], v[20:21], 1.0 op_sel_hi:[1,0]
	v_cvt_pk_bf16_f32 v34, v18, v19
	s_nop 0
	v_pk_fma_f32 v[20:21], v[20:21], v[36:37], v[28:29]
	v_lshlrev_b32_e32 v15, 16, v34
	v_cvt_pk_fp8_f32 v27, v20, v21 op_sel:[0,0,1]
	v_and_b32_e32 v26, 0xffff0000, v34
	v_cvt_pk_bf16_f32 v35, v20, v21
	v_sub_f32_e32 v15, v18, v15
	v_sub_f32_e32 v26, v19, v26
	v_lshlrev_b32_e32 v18, 16, v35
	v_and_b32_e32 v19, 0xffff0000, v35
	v_sub_f32_e32 v18, v20, v18
	v_sub_f32_e32 v19, v21, v19
	v_cvt_pk_bf16_f32 v36, v15, v26
	v_cvt_pk_bf16_f32 v37, v18, v19
	global_store_dword v150, v27, s[0:1] offset:512
	global_load_dwordx4 v[18:21], v[42:43], off offset:3072
	s_nop 0
	global_load_dwordx4 v[26:29], v[16:17], off offset:3072
	v_mov_b32_e32 v15, v79
	v_pk_mul_f32 v[44:45], v[46:47], v[14:15] op_sel_hi:[1,0]
	v_pk_mul_f32 v[46:47], v[48:49], v[14:15] op_sel_hi:[1,0]
	v_add_co_u32_e32 v42, vcc, s41, v42
	ds_write_b64 v167, v[34:35]
	ds_write_b64 v168, v[36:37]
	v_addc_co_u32_e32 v43, vcc, 0, v43, vcc
	s_waitcnt vmcnt(1)
	v_pk_add_f32 v[18:19], v[18:19], 1.0 op_sel_hi:[1,0]
	s_waitcnt vmcnt(0)
	v_pk_fma_f32 v[18:19], v[44:45], v[18:19], v[26:27]
	v_pk_add_f32 v[20:21], v[20:21], 1.0 op_sel_hi:[1,0]
	v_cvt_pk_fp8_f32 v15, v18, v19
	v_pk_fma_f32 v[20:21], v[46:47], v[20:21], v[28:29]
	v_cvt_pk_bf16_f32 v34, v18, v19
	v_add_co_u32_e32 v44, vcc, s41, v16
	v_cvt_pk_fp8_f32 v15, v20, v21 op_sel:[0,0,1]
	v_cvt_pk_bf16_f32 v35, v20, v21
	v_lshlrev_b32_e32 v26, 16, v34
	v_and_b32_e32 v27, 0xffff0000, v34
	v_lshlrev_b32_e32 v28, 16, v35
	v_and_b32_e32 v29, 0xffff0000, v35
	v_sub_f32_e32 v18, v18, v26
	v_sub_f32_e32 v19, v19, v27
	v_sub_f32_e32 v26, v20, v28
	v_sub_f32_e32 v20, v21, v29
	v_cvt_pk_bf16_f32 v36, v18, v19
	v_cvt_pk_bf16_f32 v37, v26, v20
	global_store_dword v150, v15, s[0:1] offset:768
	global_load_dwordx4 v[18:21], v[42:43], off
	v_addc_co_u32_e32 v45, vcc, 0, v17, vcc
	global_load_dwordx4 v[26:29], v[44:45], off
	v_mov_b32_e32 v15, v79
	v_pk_mul_f32 v[16:17], v[38:39], v[14:15] op_sel_hi:[1,0]
	v_pk_mul_f32 v[38:39], v[40:41], v[14:15] op_sel_hi:[1,0]
	ds_write_b64 v176, v[34:35]
	ds_write_b64 v177, v[36:37]
	s_waitcnt vmcnt(1)
; #define LAS __attribute__((address_space(3)))
; __device__ __forceinline__ unsigned cvt_pk_bf16(float lo, float hi) { unsigned r; asm volatile("v_cvt_pk_bf16_f32 %0, %1, %2" : "=v"(r) : "v"(lo), "v"(hi)); return r; }
; __device__ __forceinline__ unsigned pk4_fp8(float a, float b, float c, float d) { int w = 0; w = __builtin_amdgcn_cvt_pk_fp8_f32(a, b, w, false); w = __builtin_amdgcn_cvt_pk_fp8_f32(c, d, w, true); return (unsigned)w; }
; __device__ __forceinline__ float bf_lo(unsigned w) { return __uint_as_float(w << 16); }
; __device__ __forceinline__ float bf_hi(unsigned w) { return __uint_as_float(w & 0xffff0000u); }
; __device__ __forceinline__ void p6_router(Frame& F) {
;     ...
;                 for (int j = 0; j < 8; ++j) { const f32x4 sh = ((const f32x4*)(mod + (size_t)b * 12288 + 6144))[loq + 64 * j], sc = ((const f32x4*)(mod + (size_t)b * 12288 + 8192))[loq + 64 * j];
;                     const f32x4 y = v[j] * rstd * (sc + 1.0f) + sh;
;                     u32x2 wh; wh.x = cvt_pk_bf16(y[0], y[1]); wh.y = cvt_pk_bf16(y[2], y[3]);
;                     const f32x4 yl = {y[0] - bf_lo(wh.x), y[1] - bf_hi(wh.x), y[2] - bf_lo(wh.y), y[3] - bf_hi(wh.y)};
;                     u32x2 wl; wl.x = cvt_pk_bf16(yl[0], yl[1]); wl.y = cvt_pk_bf16(yl[2], yl[3]);
;                     { const int r = 2 * wave + q; LAS unsigned char* rowp = F.lds + r * 4096 + ((((lane >> 1) + 32 * j) ^ r) << 4) + (lane & 1) * 8;
;                       *(LAS u32x2*)rowp = wh; *(LAS u32x2*)(rowp + 65536) = wl; }
;                     U2F[(size_t)t * (DM / 4) + lane + 64 * j] = pk4_fp8(y[0], y[1], y[2], y[3]); }
;             }
;             __builtin_amdgcn_sched_barrier(0);
;             bf16x8 bh[2][2], bl[2][2]; f32x4 cur[2] = {(f32x4){0.f, 0.f, 0.f, 0.f}, (f32x4){0.f, 0.f, 0.f, 0.f}};
;             const bf16_t* wbh = WRH + (size_t)fr * DM + wave * 256 + fq * 8; const bf16_t* wbl = WRL + (size_t)fr * DM + wave * 256 + fq * 8;
; #pragma unroll
;             for (int n = 0; n < 2; ++n) { bh[0][n] = *(const bf16x8*)(wbh + (size_t)(16 * n) * DM); bl[0][n] = *(const bf16x8*)(wbl + (size_t)(16 * n) * DM); }
;             if (rp == 0) {
; #pragma unroll
;                 for (int q = 0; q < 2; ++q)
; #pragma unroll
;                     for (int j = 0; j < 8; ++j) zr[q][j] = ((const u32x2*)(ZB + (size_t)(ta + 2 + q) * DM))[lane + 64 * j];
;             }
;             __syncthreads();
	v_pk_add_f32 v[18:19], v[18:19], 1.0 op_sel_hi:[1,0]
	v_pk_add_f32 v[20:21], v[20:21], 1.0 op_sel_hi:[1,0]
	s_waitcnt vmcnt(0)
	v_pk_fma_f32 v[16:17], v[16:17], v[18:19], v[26:27]
	s_nop 0
	v_cvt_pk_fp8_f32 v15, v16, v17
	v_pk_fma_f32 v[20:21], v[38:39], v[20:21], v[28:29]
	v_cvt_pk_bf16_f32 v34, v16, v17
	s_nop 0
	v_cvt_pk_fp8_f32 v15, v20, v21 op_sel:[0,0,1]
	v_cvt_pk_bf16_f32 v35, v20, v21
	v_lshlrev_b32_e32 v18, 16, v34
	v_and_b32_e32 v19, 0xffff0000, v34
	v_lshlrev_b32_e32 v26, 16, v35
	v_and_b32_e32 v27, 0xffff0000, v35
	v_sub_f32_e32 v16, v16, v18
	v_sub_f32_e32 v17, v17, v19
	v_sub_f32_e32 v18, v20, v26
	v_sub_f32_e32 v19, v21, v27
	v_cvt_pk_bf16_f32 v20, v16, v17
	v_cvt_pk_bf16_f32 v21, v18, v19
	global_store_dword v150, v15, s[0:1] offset:1024
	global_load_dwordx4 v[16:19], v[42:43], off offset:1024
	global_load_dwordx4 v[26:29], v[44:45], off offset:1024
	v_mov_b32_e32 v15, v79
	v_pk_mul_f32 v[30:31], v[30:31], v[14:15] op_sel_hi:[1,0]
	v_pk_mul_f32 v[32:33], v[32:33], v[14:15] op_sel_hi:[1,0]
	ds_write_b64 v178, v[34:35]
	ds_write_b64 v179, v[20:21]
	s_waitcnt vmcnt(1)
	v_pk_add_f32 v[16:17], v[16:17], 1.0 op_sel_hi:[1,0]
	s_waitcnt vmcnt(0)
	v_pk_fma_f32 v[16:17], v[30:31], v[16:17], v[26:27]
	v_pk_add_f32 v[18:19], v[18:19], 1.0 op_sel_hi:[1,0]
	v_cvt_pk_fp8_f32 v15, v16, v17
	v_pk_fma_f32 v[18:19], v[32:33], v[18:19], v[28:29]
	v_cvt_pk_bf16_f32 v20, v16, v17
	s_nop 0
	v_cvt_pk_fp8_f32 v15, v18, v19 op_sel:[0,0,1]
	v_cvt_pk_bf16_f32 v21, v18, v19
	v_lshlrev_b32_e32 v26, 16, v20
	v_and_b32_e32 v27, 0xffff0000, v20
	v_lshlrev_b32_e32 v28, 16, v21
	v_and_b32_e32 v29, 0xffff0000, v21
	v_sub_f32_e32 v16, v16, v26
	v_sub_f32_e32 v17, v17, v27
	v_sub_f32_e32 v26, v18, v28
	v_sub_f32_e32 v18, v19, v29
	v_cvt_pk_bf16_f32 v30, v16, v17
	v_cvt_pk_bf16_f32 v31, v26, v18
	global_store_dword v150, v15, s[0:1] offset:1280
	global_load_dwordx4 v[16:19], v[42:43], off offset:2048
	global_load_dwordx4 v[26:29], v[44:45], off offset:2048
	v_mov_b32_e32 v15, v79
	v_pk_mul_f32 v[22:23], v[22:23], v[14:15] op_sel_hi:[1,0]
	v_pk_mul_f32 v[24:25], v[24:25], v[14:15] op_sel_hi:[1,0]
	ds_write_b64 v180, v[20:21]
	ds_write_b64 v181, v[30:31]
	s_waitcnt vmcnt(1)
	v_pk_add_f32 v[16:17], v[16:17], 1.0 op_sel_hi:[1,0]
	s_waitcnt vmcnt(0)
	v_pk_fma_f32 v[16:17], v[22:23], v[16:17], v[26:27]
	v_pk_add_f32 v[18:19], v[18:19], 1.0 op_sel_hi:[1,0]
	v_cvt_pk_fp8_f32 v15, v16, v17
	v_pk_fma_f32 v[18:19], v[24:25], v[18:19], v[28:29]
	v_cvt_pk_bf16_f32 v24, v16, v17
	s_nop 0
	v_cvt_pk_fp8_f32 v15, v18, v19 op_sel:[0,0,1]
	v_cvt_pk_bf16_f32 v25, v18, v19
	v_lshlrev_b32_e32 v20, 16, v24
	v_and_b32_e32 v21, 0xffff0000, v24
	v_lshlrev_b32_e32 v22, 16, v25
	v_and_b32_e32 v23, 0xffff0000, v25
	v_sub_f32_e32 v16, v16, v20
	v_sub_f32_e32 v17, v17, v21
	v_sub_f32_e32 v20, v18, v22
	v_sub_f32_e32 v18, v19, v23
	v_cvt_pk_bf16_f32 v26, v16, v17
	v_cvt_pk_bf16_f32 v27, v20, v18
	global_store_dword v150, v15, s[0:1] offset:1536
	global_load_dwordx4 v[16:19], v[42:43], off offset:3072
	global_load_dwordx4 v[20:23], v[44:45], off offset:3072
	v_pk_mul_f32 v[12:13], v[12:13], v[14:15] op_sel_hi:[1,0]
	v_pk_mul_f32 v[10:11], v[10:11], v[14:15] op_sel_hi:[1,0]
	ds_write_b64 v184, v[24:25]
	ds_write_b64 v185, v[26:27]
	s_waitcnt vmcnt(1)
	v_pk_add_f32 v[16:17], v[16:17], 1.0 op_sel_hi:[1,0]
	s_waitcnt vmcnt(0)
	v_pk_fma_f32 v[12:13], v[12:13], v[16:17], v[20:21]
	v_pk_add_f32 v[14:15], v[18:19], 1.0 op_sel_hi:[1,0]
	v_cvt_pk_fp8_f32 v79, v12, v13
	v_pk_fma_f32 v[10:11], v[10:11], v[14:15], v[22:23]
	v_cvt_pk_bf16_f32 v14, v12, v13
	s_nop 0
	v_cvt_pk_fp8_f32 v79, v10, v11 op_sel:[0,0,1]
	v_lshlrev_b32_e32 v16, 16, v14
	v_and_b32_e32 v17, 0xffff0000, v14
	v_cvt_pk_bf16_f32 v15, v10, v11
	v_sub_f32_e32 v12, v12, v16
	v_lshlrev_b32_e32 v18, 16, v15
	v_and_b32_e32 v19, 0xffff0000, v15
	v_sub_f32_e32 v13, v13, v17
	v_sub_f32_e32 v16, v10, v18
	v_sub_f32_e32 v17, v11, v19
	v_cvt_pk_bf16_f32 v12, v12, v13
	v_cvt_pk_bf16_f32 v13, v16, v17
	ds_write_b64 v182, v[14:15]
	ds_write_b64 v183, v[12:13]
	global_store_dword v150, v79, s[0:1] offset:1792
	global_load_dwordx4 v[10:13], v[84:85], off
	global_load_dwordx4 v[14:17], v[74:75], off
	global_load_dwordx4 v[18:21], v[86:87], off
	global_load_dwordx4 v[22:25], v[76:77], off
	s_waitcnt lgkmcnt(0)
	s_barrier
; #define LAS __attribute__((address_space(3)))
; __device__ __forceinline__ void p6_router(Frame& F) {
;     ...
; #pragma unroll
;             for (int ks = 0; ks < 8; ++ks) {
;                 if (ks < 7) {
; #pragma unroll
;                     for (int n = 0; n < 2; ++n) { bh[(ks + 1) & 1][n] = *(const bf16x8*)(wbh + (size_t)(16 * n) * DM + (ks + 1) * 32); bl[(ks + 1) & 1][n] = *(const bf16x8*)(wbl + (size_t)(16 * n) * DM + (ks + 1) * 32); }
;                 }
;                 const LAS unsigned char* ap = F.lds + fr * 4096 + (((wave * 32 + ks * 4 + fq) ^ fr) << 4);
;                 const bf16x8 ah = *(const LAS bf16x8*)ap, al = *(const LAS bf16x8*)(ap + 65536);
; #pragma unroll
;                 for (int n = 0; n < 2; ++n) {
;                     cur[n] = __builtin_amdgcn_mfma_f32_16x16x32_bf16(ah, bh[ks & 1][n], cur[n], 0, 0, 0);
;                     cur[n] = __builtin_amdgcn_mfma_f32_16x16x32_bf16(ah, bl[ks & 1][n], cur[n], 0, 0, 0);
;                     cur[n] = __builtin_amdgcn_mfma_f32_16x16x32_bf16(al, bh[ks & 1][n], cur[n], 0, 0, 0);
;                 }
;                 __builtin_amdgcn_sched_barrier(0);
;             }
;             accp[0] = cur[0]; accp[1] = cur[1];
;             __syncthreads();
;         };
;         pass(0, acc[0]); pass(1, acc[1]);
;     }
;     LAS float* red = (LAS float*)F.lds;
;     LAS float* lg = red + 8 * 1024;
;     LAS int* aE = (LAS int*)(lg + 1024); LAS int* aP = aE + 128; LAS float* aW = (LAS float*)(aP + 128);
; #pragma unroll
;     for (int a = 0; a < 2; ++a)
; #pragma unroll
;         for (int n = 0; n < 2; ++n)
; #pragma unroll
;             for (int i = 0; i < 4; ++i) { const int m = 4 * fq + i; red[wave * 1024 + (4 * (m >> 1) + 2 * a + (m & 1)) * 32 + 16 * n + fr] = acc[a][n][i]; }
;     __syncthreads();
;     for (int i = tid; i < 1024; i += 512) { float s = F.in[I_BR][i & 31];
	ds_read_b128 v[26:29], v186
	ds_read_b128 v[30:33], v187
	s_waitcnt vmcnt(3) lgkmcnt(1)
	v_mfma_f32_16x16x32_bf16 v[34:37], v[26:29], v[10:13], 0
	s_waitcnt vmcnt(2)
	v_mfma_f32_16x16x32_bf16 v[38:41], v[26:29], v[14:17], 0
	s_waitcnt vmcnt(1)
	v_mfma_f32_16x16x32_bf16 v[18:21], v[26:29], v[18:21], v[34:37]
	s_waitcnt vmcnt(0)
	v_mfma_f32_16x16x32_bf16 v[22:25], v[26:29], v[22:25], v[38:41]
	global_load_dwordx4 v[26:29], v[80:81], off offset:64
	s_nop 0
	global_load_dwordx4 v[34:37], v[82:83], off offset:64
	s_waitcnt lgkmcnt(0)
	v_mfma_f32_16x16x32_bf16 v[10:13], v[30:33], v[10:13], v[18:21]
	s_nop 2
	global_load_dwordx4 v[18:21], v[74:75], off offset:64
	global_load_dwordx4 v[38:41], v[76:77], off offset:64
	v_mfma_f32_16x16x32_bf16 v[14:17], v[30:33], v[14:17], v[22:25]
	s_nop 2
	ds_read_b128 v[22:25], v188
	ds_read_b128 v[30:33], v189
	s_waitcnt vmcnt(3) lgkmcnt(1)
	v_mfma_f32_16x16x32_bf16 v[10:13], v[22:25], v[26:29], v[10:13]
	s_waitcnt vmcnt(1)
	v_mfma_f32_16x16x32_bf16 v[14:17], v[22:25], v[18:21], v[14:17]
	v_mfma_f32_16x16x32_bf16 v[10:13], v[22:25], v[34:37], v[10:13]
	s_waitcnt lgkmcnt(0)
	v_mfma_f32_16x16x32_bf16 v[10:13], v[30:33], v[26:29], v[10:13]
	global_load_dwordx4 v[26:29], v[80:81], off offset:128
	global_load_dwordx4 v[34:37], v[82:83], off offset:128
	s_waitcnt vmcnt(2)
	v_mfma_f32_16x16x32_bf16 v[14:17], v[22:25], v[38:41], v[14:17]
	global_load_dwordx4 v[22:25], v[74:75], off offset:128
	global_load_dwordx4 v[38:41], v[76:77], off offset:128
	v_mfma_f32_16x16x32_bf16 v[14:17], v[30:33], v[18:21], v[14:17]
	ds_read_b128 v[18:21], v190
	ds_read_b128 v[30:33], v191
	s_waitcnt vmcnt(3) lgkmcnt(1)
	v_mfma_f32_16x16x32_bf16 v[10:13], v[18:21], v[26:29], v[10:13]
	s_waitcnt vmcnt(1)
	v_mfma_f32_16x16x32_bf16 v[14:17], v[18:21], v[22:25], v[14:17]
	v_mfma_f32_16x16x32_bf16 v[10:13], v[18:21], v[34:37], v[10:13]
	s_waitcnt lgkmcnt(0)
	v_mfma_f32_16x16x32_bf16 v[10:13], v[30:33], v[26:29], v[10:13]
	global_load_dwordx4 v[26:29], v[80:81], off offset:192
	global_load_dwordx4 v[34:37], v[82:83], off offset:192
	s_waitcnt vmcnt(2)
	v_mfma_f32_16x16x32_bf16 v[14:17], v[18:21], v[38:41], v[14:17]
	global_load_dwordx4 v[18:21], v[74:75], off offset:192
	global_load_dwordx4 v[38:41], v[76:77], off offset:192
	v_mfma_f32_16x16x32_bf16 v[14:17], v[30:33], v[22:25], v[14:17]
	ds_read_b128 v[22:25], v192
	ds_read_b128 v[30:33], v193
	s_waitcnt vmcnt(3) lgkmcnt(1)
	v_mfma_f32_16x16x32_bf16 v[10:13], v[22:25], v[26:29], v[10:13]
	s_waitcnt vmcnt(1)
	v_mfma_f32_16x16x32_bf16 v[14:17], v[22:25], v[18:21], v[14:17]
	v_mfma_f32_16x16x32_bf16 v[10:13], v[22:25], v[34:37], v[10:13]
	s_waitcnt lgkmcnt(0)
	v_mfma_f32_16x16x32_bf16 v[10:13], v[30:33], v[26:29], v[10:13]
	global_load_dwordx4 v[26:29], v[80:81], off offset:256
	global_load_dwordx4 v[34:37], v[82:83], off offset:256
	s_waitcnt vmcnt(2)
	v_mfma_f32_16x16x32_bf16 v[14:17], v[22:25], v[38:41], v[14:17]
	global_load_dwordx4 v[22:25], v[74:75], off offset:256
	global_load_dwordx4 v[38:41], v[76:77], off offset:256
	v_mfma_f32_16x16x32_bf16 v[14:17], v[30:33], v[18:21], v[14:17]
	ds_read_b128 v[18:21], v194
	ds_read_b128 v[30:33], v195
	s_waitcnt vmcnt(3) lgkmcnt(1)
	v_mfma_f32_16x16x32_bf16 v[10:13], v[18:21], v[26:29], v[10:13]
	s_waitcnt vmcnt(1)
	v_mfma_f32_16x16x32_bf16 v[14:17], v[18:21], v[22:25], v[14:17]
	v_mfma_f32_16x16x32_bf16 v[10:13], v[18:21], v[34:37], v[10:13]
	s_waitcnt lgkmcnt(0)
	v_mfma_f32_16x16x32_bf16 v[10:13], v[30:33], v[26:29], v[10:13]
	global_load_dwordx4 v[26:29], v[80:81], off offset:320
	global_load_dwordx4 v[34:37], v[82:83], off offset:320
	s_waitcnt vmcnt(2)
	v_mfma_f32_16x16x32_bf16 v[14:17], v[18:21], v[38:41], v[14:17]
	global_load_dwordx4 v[18:21], v[74:75], off offset:320
	global_load_dwordx4 v[38:41], v[76:77], off offset:320
	v_mfma_f32_16x16x32_bf16 v[14:17], v[30:33], v[22:25], v[14:17]
	ds_read_b128 v[22:25], v196
	ds_read_b128 v[30:33], v197
	s_waitcnt vmcnt(3) lgkmcnt(1)
	v_mfma_f32_16x16x32_bf16 v[10:13], v[22:25], v[26:29], v[10:13]
	s_waitcnt vmcnt(1)
	v_mfma_f32_16x16x32_bf16 v[14:17], v[22:25], v[18:21], v[14:17]
	v_mfma_f32_16x16x32_bf16 v[10:13], v[22:25], v[34:37], v[10:13]
	s_waitcnt lgkmcnt(0)
	v_mfma_f32_16x16x32_bf16 v[10:13], v[30:33], v[26:29], v[10:13]
	global_load_dwordx4 v[26:29], v[80:81], off offset:384
	global_load_dwordx4 v[34:37], v[82:83], off offset:384
	s_waitcnt vmcnt(2)
	v_mfma_f32_16x16x32_bf16 v[14:17], v[22:25], v[38:41], v[14:17]
	global_load_dwordx4 v[22:25], v[74:75], off offset:384
	global_load_dwordx4 v[38:41], v[76:77], off offset:384
	v_mfma_f32_16x16x32_bf16 v[14:17], v[30:33], v[18:21], v[14:17]
	ds_read_b128 v[18:21], v199
	ds_read_b128 v[30:33], v201
	s_waitcnt vmcnt(3) lgkmcnt(1)
	v_mfma_f32_16x16x32_bf16 v[10:13], v[18:21], v[26:29], v[10:13]
	s_waitcnt vmcnt(1)
	v_mfma_f32_16x16x32_bf16 v[14:17], v[18:21], v[22:25], v[14:17]
	v_mfma_f32_16x16x32_bf16 v[10:13], v[18:21], v[34:37], v[10:13]
	s_waitcnt lgkmcnt(0)
	v_mfma_f32_16x16x32_bf16 v[10:13], v[30:33], v[26:29], v[10:13]
	global_load_dwordx4 v[26:29], v[80:81], off offset:448
	global_load_dwordx4 v[34:37], v[82:83], off offset:448
	s_waitcnt vmcnt(2)
	v_mfma_f32_16x16x32_bf16 v[14:17], v[18:21], v[38:41], v[14:17]
	global_load_dwordx4 v[18:21], v[74:75], off offset:448
	global_load_dwordx4 v[38:41], v[76:77], off offset:448
	v_mfma_f32_16x16x32_bf16 v[14:17], v[30:33], v[22:25], v[14:17]
	ds_read_b128 v[22:25], v198
	ds_read_b128 v[30:33], v200
	s_waitcnt vmcnt(3) lgkmcnt(1)
	v_mfma_f32_16x16x32_bf16 v[10:13], v[22:25], v[26:29], v[10:13]
	s_waitcnt vmcnt(1)
	v_mfma_f32_16x16x32_bf16 v[14:17], v[22:25], v[18:21], v[14:17]
	v_mfma_f32_16x16x32_bf16 v[10:13], v[22:25], v[34:37], v[10:13]
	s_waitcnt vmcnt(0)
	v_mfma_f32_16x16x32_bf16 v[14:17], v[22:25], v[38:41], v[14:17]
	s_waitcnt lgkmcnt(0)
	v_mfma_f32_16x16x32_bf16 v[10:13], v[30:33], v[26:29], v[10:13]
	v_mfma_f32_16x16x32_bf16 v[14:17], v[30:33], v[18:21], v[14:17]
	s_lshl_b32 s0, s46, 12
	v_lshlrev_b32_e32 v18, 10, v154
	s_add_i32 s0, s0, 0
	v_lshlrev_b32_e32 v19, 2, v151
	v_add3_u32 v18, s0, v18, v19
	s_barrier
	ds_write2_b32 v18, v2, v6 offset1:16
	ds_write2_b32 v18, v3, v7 offset0:32 offset1:48
	ds_write2_b32 v18, v4, v8 offset0:128 offset1:144
	ds_write2_b32 v18, v5, v9 offset0:160 offset1:176
	ds_write2_b32 v18, v10, v14 offset0:64 offset1:80
	ds_write2_b32 v18, v11, v15 offset0:96 offset1:112
	ds_write2_b32 v18, v12, v16 offset0:192 offset1:208
	ds_write2_b32 v18, v13, v17 offset0:224 offset1:240
	v_and_b32_e32 v5, 31, v0
	v_lshlrev_b32_e32 v2, 2, v5
	s_waitcnt lgkmcnt(0)
	s_barrier
	global_load_dword v2, v2, s[14:15]
	v_or_b32_e32 v3, 0xfffffe00, v0
	v_lshl_add_u32 v4, v0, 2, 0
	s_mov_b64 s[0:1], 0

; __device__ __forceinline__ float bf_lo(unsigned w) { return __uint_as_float(w << 16); }
; __device__ __forceinline__ float bf_hi(unsigned w) { return __uint_as_float(w & 0xffff0000u); }
; __device__ __forceinline__ void p9_final(Frame& F) {
;     ...
;     for (int t = gw; t < NTOK; t += NGW) {
;         const int b = t >> 12;
;         const i32x4 ae = ae_n, ap = ap_n; const f32x4 aw = aw_n;
;         { const int tn = (t + NGW < NTOK) ? t + NGW : t;
;           ae_n = ((const i32x4*)(F.ws + WS_ASG_E))[tn]; ap_n = ((const i32x4*)(F.ws + WS_ASG_P))[tn]; aw_n = ((const f32x4*)(F.ws + WS_ASG_W))[tn]; }
;         const u32x2* yr[4];
; #pragma unroll
;         for (int k = 0; k < 4; ++k) yr[k] = (const u32x2*)(Y + ((size_t)tab[352 + ae[k]] * 256 + ap[k]) * DM) + lane;
;         u32x2 q[4][8]; f32x4 x1[8];
; #pragma unroll
;         for (int k = 0; k < 4; ++k)
; #pragma unroll
;             for (int j = 0; j < 8; ++j) q[k][j] = yr[k][64 * j];
; #pragma unroll
;         for (int j = 0; j < 8; ++j) { const u32x2 xb = ((const u32x2*)(X1 + (size_t)t * DM))[lane + 64 * j]; x1[j] = (f32x4){bf_lo(xb.x), bf_hi(xb.x), bf_lo(xb.y), bf_hi(xb.y)}; }
;         float s = 0.f; f32x4 v[8];
; #pragma unroll
;         for (int j = 0; j < 8; ++j) { f32x4 y = {0.f, 0.f, 0.f, 0.f};
; #pragma unroll
;             for (int k = 0; k < 4; ++k) { const float w = aw[k]; y[0] += w * bf_lo(q[k][j].x); y[1] += w * bf_hi(q[k][j].x); y[2] += w * bf_lo(q[k][j].y); y[3] += w * bf_hi(q[k][j].y); }
;             v[j] = x1[j] * DN_ALPHA + ((const f32x4*)(mod + (size_t)b * 12288 + 10240))[lane + 64 * j] * y; s += (v[j][0] + v[j][1]) + (v[j][2] + v[j][3]); }
.LBB0_1211:
	global_load_dwordx2 v[50:51], v[48:49], off nt
	global_load_dwordx2 v[52:53], v[48:49], off offset:512 nt
	global_load_dwordx2 v[54:55], v[48:49], off offset:1024 nt
	global_load_dwordx2 v[56:57], v[48:49], off offset:1536 nt
	global_load_dwordx2 v[58:59], v[48:49], off offset:2048 nt
	global_load_dwordx2 v[60:61], v[48:49], off offset:2560 nt
	global_load_dwordx2 v[62:63], v[48:49], off offset:3072 nt
	global_load_dwordx2 v[64:65], v[48:49], off offset:3584 nt
	s_add_i32 s28, s14, s4
	s_cmpk_lt_i32 s28, 0x2000
	s_cselect_b64 s[24:25], -1, 0
	v_lshlrev_b32_e32 v4, 2, v4
	v_lshlrev_b32_e32 v6, 2, v6
	s_and_b64 s[30:31], s[24:25], exec
	v_lshlrev_b32_e32 v5, 2, v5
	v_lshlrev_b32_e32 v7, 2, v7
	v_add_u32_e32 v4, s5, v4
	v_add_u32_e32 v8, s5, v6
	s_cselect_b32 s30, s28, s14
	global_load_dwordx4 v[16:19], v[26:27], off
	global_load_dwordx4 v[20:23], v[28:29], off
	v_add_u32_e32 v5, s5, v5
	v_add_u32_e32 v7, s5, v7
	ds_read_b32 v4, v4
	ds_read_b32 v6, v5
	ds_read_b32 v8, v8
	ds_read_b32 v10, v7
	s_ashr_i32 s31, s30, 31
	s_lshl_b64 s[30:31], s[30:31], 4
	s_add_u32 s36, s34, s30
	s_waitcnt lgkmcnt(3)
	v_ashrrev_i32_e32 v5, 31, v4
	s_waitcnt lgkmcnt(2)
	v_ashrrev_i32_e32 v7, 31, v6
	s_addc_u32 s37, s35, s31
	v_lshlrev_b64 v[12:13], 20, v[4:5]
	v_lshlrev_b64 v[14:15], 20, v[6:7]
	global_load_dwordx4 v[4:7], v25, s[36:37]
	s_add_u32 s36, s27, s30
	s_addc_u32 s37, s33, s31
	s_add_u32 s30, s13, s30
	s_mov_b32 s16, s0
	s_waitcnt lgkmcnt(1)
	v_ashrrev_i32_e32 v9, 31, v8
	s_waitcnt lgkmcnt(0)
	v_ashrrev_i32_e32 v11, 31, v10
	s_addc_u32 s31, s26, s31
	s_ashr_i32 s17, s0, 31
	s_mov_b32 s18, s1
	s_mov_b32 s20, s2
	s_mov_b32 s22, s3
	v_lshlrev_b64 v[8:9], 20, v[8:9]
	v_lshlrev_b64 v[10:11], 20, v[10:11]
	v_lshl_add_u64 v[84:85], s[6:7], 0, v[12:13]
	s_ashr_i32 s19, s1, 31
	s_ashr_i32 s21, s2, 31
	s_ashr_i32 s23, s3, 31
	s_lshl_b64 s[0:1], s[16:17], 12
	v_lshl_add_u64 v[86:87], s[6:7], 0, v[14:15]
	v_lshl_add_u64 v[88:89], s[6:7], 0, v[8:9]
	v_lshl_add_u64 v[90:91], s[6:7], 0, v[10:11]
	s_lshl_b64 s[2:3], s[18:19], 12
	s_lshl_b64 s[16:17], s[20:21], 12
	s_lshl_b64 s[18:19], s[22:23], 12
	v_lshl_add_u64 v[84:85], v[84:85], 0, s[0:1]
	v_lshlrev_b32_e32 v81, 3, v170
	v_lshl_add_u64 v[86:87], v[86:87], 0, s[2:3]
	v_lshl_add_u64 v[88:89], v[88:89], 0, s[16:17]
	v_lshl_add_u64 v[90:91], v[90:91], 0, s[18:19]
	v_readfirstlane_b32 s0, v84
	v_readfirstlane_b32 s1, v85
	global_load_dwordx4 v[8:11], v25, s[36:37]
	global_load_dwordx4 v[12:15], v25, s[30:31]
	v_readfirstlane_b32 s2, v86
	v_readfirstlane_b32 s3, v87
	v_readfirstlane_b32 s16, v88
	v_readfirstlane_b32 s17, v89
	v_readfirstlane_b32 s18, v90
	v_readfirstlane_b32 s19, v91
	global_load_dwordx2 v[102:103], v81, s[0:1] nt
	global_load_dwordx2 v[104:105], v81, s[2:3] nt
	s_nop 0
	global_load_dwordx2 v[106:107], v81, s[16:17] nt
	s_nop 0
	global_load_dwordx2 v[108:109], v81, s[18:19] nt
	global_load_dwordx2 v[110:111], v81, s[0:1] offset:512 nt
	global_load_dwordx2 v[112:113], v81, s[0:1] offset:1024 nt
	global_load_dwordx2 v[114:115], v81, s[0:1] offset:1536 nt
	global_load_dwordx2 v[116:117], v81, s[2:3] offset:512 nt
	global_load_dwordx2 v[118:119], v81, s[16:17] offset:512 nt
	global_load_dwordx2 v[120:121], v81, s[0:1] offset:2048 nt
	global_load_dwordx2 v[122:123], v81, s[0:1] offset:2560 nt
	global_load_dwordx2 v[124:125], v81, s[0:1] offset:3072 nt
	global_load_dwordx2 v[126:127], v81, s[0:1] offset:3584 nt
	global_load_dwordx2 v[128:129], v81, s[18:19] offset:512 nt
	global_load_dwordx2 v[130:131], v81, s[2:3] offset:1024 nt
	global_load_dwordx2 v[132:133], v81, s[2:3] offset:1536 nt
	global_load_dwordx2 v[134:135], v81, s[2:3] offset:2048 nt
	global_load_dwordx2 v[136:137], v81, s[2:3] offset:2560 nt
	global_load_dwordx2 v[138:139], v81, s[2:3] offset:3072 nt
	global_load_dwordx2 v[140:141], v81, s[2:3] offset:3584 nt
	global_load_dwordx2 v[142:143], v81, s[16:17] offset:1024 nt
	global_load_dwordx2 v[144:145], v81, s[16:17] offset:1536 nt
	global_load_dwordx2 v[146:147], v81, s[16:17] offset:2048 nt
	global_load_dwordx2 v[148:149], v81, s[16:17] offset:2560 nt
	global_load_dwordx2 v[150:151], v81, s[16:17] offset:3072 nt
	global_load_dwordx2 v[152:153], v81, s[16:17] offset:3584 nt
	global_load_dwordx2 v[154:155], v81, s[18:19] offset:1024 nt
	global_load_dwordx2 v[156:157], v81, s[18:19] offset:1536 nt
	global_load_dwordx2 v[158:159], v81, s[18:19] offset:2048 nt
	global_load_dwordx2 v[160:161], v81, s[18:19] offset:2560 nt
	global_load_dwordx2 v[162:163], v81, s[18:19] offset:3072 nt
	global_load_dwordx2 v[164:165], v81, s[18:19] offset:3584 nt
	s_ashr_i32 s14, s14, 12
	s_mul_hi_i32 s20, s14, 0xc000
	s_mul_i32 s14, s14, 0xc000
	s_add_u32 s14, s82, s14
	s_addc_u32 s20, s83, s20
	s_add_u32 s0, s14, 0x10a000
	v_lshlrev_b32_e32 v82, 4, v170
	s_addc_u32 s1, s20, 0
	s_waitcnt vmcnt(44)
	v_lshlrev_b32_e32 v166, 16, v50
	v_and_b32_e32 v167, 0xffff0000, v50
	v_lshlrev_b32_e32 v168, 16, v51
	v_and_b32_e32 v169, 0xffff0000, v51
	s_waitcnt vmcnt(40)
	v_lshlrev_b32_e32 v184, 16, v58
	v_and_b32_e32 v185, 0xffff0000, v58
	v_lshlrev_b32_e32 v186, 16, v59
	v_and_b32_e32 v187, 0xffff0000, v59
	v_lshlrev_b32_e32 v176, 16, v54
	v_and_b32_e32 v177, 0xffff0000, v54
	v_lshlrev_b32_e32 v178, 16, v55
	v_and_b32_e32 v179, 0xffff0000, v55
	s_waitcnt vmcnt(39)
	v_lshlrev_b32_e32 v188, 16, v60
	v_and_b32_e32 v189, 0xffff0000, v60
	v_lshlrev_b32_e32 v190, 16, v61
	v_and_b32_e32 v191, 0xffff0000, v61
	v_lshlrev_b32_e32 v172, 16, v52
	v_and_b32_e32 v173, 0xffff0000, v52
	v_lshlrev_b32_e32 v174, 16, v53
	v_and_b32_e32 v175, 0xffff0000, v53
	v_lshlrev_b32_e32 v180, 16, v56
	v_and_b32_e32 v181, 0xffff0000, v56
	v_lshlrev_b32_e32 v182, 16, v57
	v_and_b32_e32 v183, 0xffff0000, v57
	global_load_dwordx4 v[82:85], v82, s[0:1]
	s_nop 0
	global_load_dwordx4 v[86:89], v72, s[0:1]
	global_load_dwordx4 v[90:93], v73, s[0:1]
	global_load_dwordx4 v[94:97], v74, s[0:1]
	global_load_dwordx4 v[98:101], v75, s[0:1]
	v_mov_b32_e32 v24, v3
	s_waitcnt vmcnt(43)
; __device__ __forceinline__ float bf_lo(unsigned w) { return __uint_as_float(w << 16); }
; __device__ __forceinline__ float bf_hi(unsigned w) { return __uint_as_float(w & 0xffff0000u); }
; __device__ __forceinline__ void p9_final(Frame& F) {
;     ...
;         float s = 0.f; f32x4 v[8];
; #pragma unroll
;         for (int j = 0; j < 8; ++j) { f32x4 y = {0.f, 0.f, 0.f, 0.f};
; #pragma unroll
;             for (int k = 0; k < 4; ++k) { const float w = aw[k]; y[0] += w * bf_lo(q[k][j].x); y[1] += w * bf_hi(q[k][j].x); y[2] += w * bf_lo(q[k][j].y); y[3] += w * bf_hi(q[k][j].y); }
;             v[j] = x1[j] * DN_ALPHA + ((const f32x4*)(mod + (size_t)b * 12288 + 10240))[lane + 64 * j] * y; s += (v[j][0] + v[j][1]) + (v[j][2] + v[j][3]); }
	v_lshlrev_b32_e32 v192, 16, v62
	v_and_b32_e32 v193, 0xffff0000, v62
	v_lshlrev_b32_e32 v62, 16, v63
	v_and_b32_e32 v63, 0xffff0000, v63
	s_waitcnt vmcnt(42)
	v_lshlrev_b32_e32 v194, 16, v64
	v_and_b32_e32 v195, 0xffff0000, v64
	v_lshlrev_b32_e32 v64, 16, v65
	v_and_b32_e32 v65, 0xffff0000, v65
	v_lshl_add_u64 v[48:49], v[48:49], 0, s[10:11]
	s_mov_b32 s14, s28
	s_waitcnt vmcnt(36)
	v_lshlrev_b32_e32 v50, 16, v102
	v_and_b32_e32 v51, 0xffff0000, v102
	v_lshlrev_b32_e32 v54, 16, v103
	v_and_b32_e32 v55, 0xffff0000, v103
	s_waitcnt vmcnt(32)
	v_lshlrev_b32_e32 v58, 16, v110
	v_and_b32_e32 v59, 0xffff0000, v110
	v_lshlrev_b32_e32 v110, 16, v111
	s_waitcnt vmcnt(29)
	v_lshlrev_b32_e32 v60, 16, v116
	v_and_b32_e32 v61, 0xffff0000, v116
	v_and_b32_e32 v111, 0xffff0000, v111
	v_lshlrev_b32_e32 v200, 16, v112
	v_and_b32_e32 v201, 0xffff0000, v112
	v_pk_fma_f32 v[58:59], v[0:1], v[58:59], 0 op_sel_hi:[0,1,0]
	v_lshlrev_b32_e32 v52, 16, v104
	v_and_b32_e32 v53, 0xffff0000, v104
	v_lshlrev_b32_e32 v56, 16, v105
	v_and_b32_e32 v57, 0xffff0000, v105
	v_lshlrev_b32_e32 v116, 16, v117
	v_and_b32_e32 v117, 0xffff0000, v117
	s_waitcnt vmcnt(22)
	v_lshlrev_b32_e32 v202, 16, v130
	v_and_b32_e32 v203, 0xffff0000, v130
	v_pk_fma_f32 v[50:51], v[0:1], v[50:51], 0 op_sel_hi:[0,1,0]
	v_pk_fma_f32 v[54:55], v[0:1], v[54:55], 0 op_sel_hi:[0,1,0]
	v_pk_fma_f32 v[252:253], v[0:1], v[60:61], v[58:59] op_sel:[1,0,0]
	v_pk_fma_f32 v[58:59], v[0:1], v[110:111], 0 op_sel_hi:[0,1,0]
	v_pk_fma_f32 v[60:61], v[0:1], v[200:201], 0 op_sel_hi:[0,1,0]
	v_pk_fma_f32 v[248:249], v[0:1], v[52:53], v[50:51] op_sel:[1,0,0]
	global_load_dwordx4 v[50:53], v76, s[0:1]
	v_pk_fma_f32 v[250:251], v[0:1], v[56:57], v[54:55] op_sel:[1,0,0]
	global_load_dwordx4 v[54:57], v77, s[0:1]
	v_pk_fma_f32 v[110:111], v[0:1], v[116:117], v[58:59] op_sel:[1,0,0]
	v_pk_fma_f32 v[116:117], v[0:1], v[202:203], v[60:61] op_sel:[1,0,0]
	global_load_dwordx4 v[58:61], v78, s[0:1]
	v_lshlrev_b32_e32 v112, 16, v113
	v_and_b32_e32 v113, 0xffff0000, v113
	v_lshlrev_b32_e32 v208, 16, v114
	v_and_b32_e32 v209, 0xffff0000, v114
	v_lshlrev_b32_e32 v114, 16, v115
	v_and_b32_e32 v115, 0xffff0000, v115
	v_lshlrev_b32_e32 v216, 16, v120
	v_and_b32_e32 v217, 0xffff0000, v120
	v_lshlrev_b32_e32 v120, 16, v121
	v_and_b32_e32 v121, 0xffff0000, v121
	v_lshlrev_b32_e32 v224, 16, v122
	v_and_b32_e32 v225, 0xffff0000, v122
	v_lshlrev_b32_e32 v122, 16, v123
	v_and_b32_e32 v123, 0xffff0000, v123
	v_lshlrev_b32_e32 v232, 16, v124
	v_and_b32_e32 v233, 0xffff0000, v124
	v_lshlrev_b32_e32 v124, 16, v125
	v_and_b32_e32 v125, 0xffff0000, v125
	v_lshlrev_b32_e32 v240, 16, v126
	v_and_b32_e32 v241, 0xffff0000, v126
	v_lshlrev_b32_e32 v126, 16, v127
	v_and_b32_e32 v127, 0xffff0000, v127
	v_lshlrev_b32_e32 v196, 16, v106
	v_and_b32_e32 v197, 0xffff0000, v106
	v_lshlrev_b32_e32 v102, 16, v107
	v_and_b32_e32 v103, 0xffff0000, v107
	v_lshlrev_b32_e32 v106, 16, v118
	v_and_b32_e32 v107, 0xffff0000, v118
	v_lshlrev_b32_e32 v118, 16, v119
	v_and_b32_e32 v119, 0xffff0000, v119
	v_lshlrev_b32_e32 v130, 16, v131
	v_and_b32_e32 v131, 0xffff0000, v131
	s_waitcnt vmcnt(24)
	v_lshlrev_b32_e32 v210, 16, v132
	v_and_b32_e32 v211, 0xffff0000, v132
	v_lshlrev_b32_e32 v132, 16, v133
	v_and_b32_e32 v133, 0xffff0000, v133
	s_waitcnt vmcnt(23)
	v_lshlrev_b32_e32 v218, 16, v134
	v_and_b32_e32 v219, 0xffff0000, v134
	v_lshlrev_b32_e32 v134, 16, v135
	v_and_b32_e32 v135, 0xffff0000, v135
	s_waitcnt vmcnt(22)
	v_lshlrev_b32_e32 v226, 16, v136
	v_and_b32_e32 v227, 0xffff0000, v136
	v_lshlrev_b32_e32 v136, 16, v137
	v_and_b32_e32 v137, 0xffff0000, v137
	s_waitcnt vmcnt(21)
	v_lshlrev_b32_e32 v234, 16, v138
	v_and_b32_e32 v235, 0xffff0000, v138
	v_lshlrev_b32_e32 v138, 16, v139
	v_and_b32_e32 v139, 0xffff0000, v139
	s_waitcnt vmcnt(20)
	v_lshlrev_b32_e32 v242, 16, v140
	v_and_b32_e32 v243, 0xffff0000, v140
	v_lshlrev_b32_e32 v140, 16, v141
	v_and_b32_e32 v141, 0xffff0000, v141
	v_pk_fma_f32 v[112:113], v[0:1], v[112:113], 0 op_sel_hi:[0,1,0]
	v_pk_fma_f32 v[200:201], v[0:1], v[208:209], 0 op_sel_hi:[0,1,0]
	v_pk_fma_f32 v[114:115], v[0:1], v[114:115], 0 op_sel_hi:[0,1,0]
	v_pk_fma_f32 v[202:203], v[0:1], v[216:217], 0 op_sel_hi:[0,1,0]
	v_pk_fma_f32 v[120:121], v[0:1], v[120:121], 0 op_sel_hi:[0,1,0]
	v_pk_fma_f32 v[208:209], v[0:1], v[224:225], 0 op_sel_hi:[0,1,0]
	v_pk_fma_f32 v[122:123], v[0:1], v[122:123], 0 op_sel_hi:[0,1,0]
	v_pk_fma_f32 v[216:217], v[0:1], v[232:233], 0 op_sel_hi:[0,1,0]
	v_pk_fma_f32 v[124:125], v[0:1], v[124:125], 0 op_sel_hi:[0,1,0]
	v_pk_fma_f32 v[224:225], v[0:1], v[240:241], 0 op_sel_hi:[0,1,0]
	v_pk_fma_f32 v[126:127], v[0:1], v[126:127], 0 op_sel_hi:[0,1,0]
	v_lshlrev_b32_e32 v198, 16, v108
	v_and_b32_e32 v199, 0xffff0000, v108
	v_lshlrev_b32_e32 v104, 16, v109
	v_and_b32_e32 v105, 0xffff0000, v109
	v_lshlrev_b32_e32 v108, 16, v128
	v_and_b32_e32 v109, 0xffff0000, v128
	v_lshlrev_b32_e32 v128, 16, v129
	v_and_b32_e32 v129, 0xffff0000, v129
	s_waitcnt vmcnt(19)
	v_lshlrev_b32_e32 v204, 16, v142
	v_and_b32_e32 v205, 0xffff0000, v142
	v_lshlrev_b32_e32 v142, 16, v143
	v_and_b32_e32 v143, 0xffff0000, v143
	s_waitcnt vmcnt(18)
	v_lshlrev_b32_e32 v212, 16, v144
	v_and_b32_e32 v213, 0xffff0000, v144
	v_lshlrev_b32_e32 v144, 16, v145
	v_and_b32_e32 v145, 0xffff0000, v145
	s_waitcnt vmcnt(17)
	v_lshlrev_b32_e32 v220, 16, v146
	v_and_b32_e32 v221, 0xffff0000, v146
	v_lshlrev_b32_e32 v146, 16, v147
	v_and_b32_e32 v147, 0xffff0000, v147
	s_waitcnt vmcnt(16)
	v_lshlrev_b32_e32 v228, 16, v148
	v_and_b32_e32 v229, 0xffff0000, v148
	v_lshlrev_b32_e32 v148, 16, v149
	v_and_b32_e32 v149, 0xffff0000, v149
	s_waitcnt vmcnt(15)
; __device__ __forceinline__ float bf_lo(unsigned w) { return __uint_as_float(w << 16); }
; __device__ __forceinline__ float bf_hi(unsigned w) { return __uint_as_float(w & 0xffff0000u); }
; __device__ __forceinline__ void p9_final(Frame& F) {
;     ...
;         for (int j = 0; j < 8; ++j) { f32x4 y = {0.f, 0.f, 0.f, 0.f};
; #pragma unroll
;             for (int k = 0; k < 4; ++k) { const float w = aw[k]; y[0] += w * bf_lo(q[k][j].x); y[1] += w * bf_hi(q[k][j].x); y[2] += w * bf_lo(q[k][j].y); y[3] += w * bf_hi(q[k][j].y); }
;             v[j] = x1[j] * DN_ALPHA + ((const f32x4*)(mod + (size_t)b * 12288 + 10240))[lane + 64 * j] * y; s += (v[j][0] + v[j][1]) + (v[j][2] + v[j][3]); }
	v_lshlrev_b32_e32 v236, 16, v150
	v_and_b32_e32 v237, 0xffff0000, v150
	v_lshlrev_b32_e32 v150, 16, v151
	v_and_b32_e32 v151, 0xffff0000, v151
	s_waitcnt vmcnt(14)
	v_lshlrev_b32_e32 v244, 16, v152
	v_and_b32_e32 v245, 0xffff0000, v152
	v_lshlrev_b32_e32 v152, 16, v153
	v_and_b32_e32 v153, 0xffff0000, v153
	v_pk_fma_f32 v[112:113], v[0:1], v[130:131], v[112:113] op_sel:[1,0,0]
	v_pk_fma_f32 v[130:131], v[0:1], v[210:211], v[200:201] op_sel:[1,0,0]
	v_pk_fma_f32 v[114:115], v[0:1], v[132:133], v[114:115] op_sel:[1,0,0]
	v_pk_fma_f32 v[132:133], v[0:1], v[218:219], v[202:203] op_sel:[1,0,0]
	v_pk_fma_f32 v[120:121], v[0:1], v[134:135], v[120:121] op_sel:[1,0,0]
	v_pk_fma_f32 v[134:135], v[0:1], v[226:227], v[208:209] op_sel:[1,0,0]
	v_pk_fma_f32 v[122:123], v[0:1], v[136:137], v[122:123] op_sel:[1,0,0]
	v_pk_fma_f32 v[136:137], v[0:1], v[234:235], v[216:217] op_sel:[1,0,0]
	v_pk_fma_f32 v[124:125], v[0:1], v[138:139], v[124:125] op_sel:[1,0,0]
	v_pk_fma_f32 v[138:139], v[0:1], v[242:243], v[224:225] op_sel:[1,0,0]
	v_pk_fma_f32 v[0:1], v[0:1], v[140:141], v[126:127] op_sel:[1,0,0]
	v_pk_fma_f32 v[126:127], v[2:3], v[196:197], v[248:249] op_sel_hi:[0,1,1]
	v_pk_fma_f32 v[102:103], v[2:3], v[102:103], v[250:251] op_sel_hi:[0,1,1]
	v_pk_fma_f32 v[106:107], v[2:3], v[106:107], v[252:253] op_sel_hi:[0,1,1]
	v_pk_fma_f32 v[110:111], v[2:3], v[118:119], v[110:111] op_sel_hi:[0,1,1]
	s_waitcnt vmcnt(13)
	v_lshlrev_b32_e32 v206, 16, v154
	v_and_b32_e32 v207, 0xffff0000, v154
	v_lshlrev_b32_e32 v154, 16, v155
	v_and_b32_e32 v155, 0xffff0000, v155
	s_waitcnt vmcnt(12)
	v_lshlrev_b32_e32 v214, 16, v156
	v_and_b32_e32 v215, 0xffff0000, v156
	v_lshlrev_b32_e32 v156, 16, v157
	v_and_b32_e32 v157, 0xffff0000, v157
	s_waitcnt vmcnt(11)
	v_lshlrev_b32_e32 v222, 16, v158
	v_and_b32_e32 v223, 0xffff0000, v158
	v_lshlrev_b32_e32 v158, 16, v159
	v_and_b32_e32 v159, 0xffff0000, v159
	s_waitcnt vmcnt(10)
	v_lshlrev_b32_e32 v230, 16, v160
	v_and_b32_e32 v231, 0xffff0000, v160
	v_lshlrev_b32_e32 v160, 16, v161
	v_and_b32_e32 v161, 0xffff0000, v161
	s_waitcnt vmcnt(9)
	v_lshlrev_b32_e32 v238, 16, v162
	v_and_b32_e32 v239, 0xffff0000, v162
	v_lshlrev_b32_e32 v162, 16, v163
	v_and_b32_e32 v163, 0xffff0000, v163
	s_waitcnt vmcnt(8)
	v_lshlrev_b32_e32 v246, 16, v164
	v_and_b32_e32 v247, 0xffff0000, v164
	v_lshlrev_b32_e32 v164, 16, v165
	v_and_b32_e32 v165, 0xffff0000, v165
	v_pk_fma_f32 v[116:117], v[2:3], v[204:205], v[116:117] op_sel_hi:[0,1,1]
	v_pk_fma_f32 v[112:113], v[2:3], v[142:143], v[112:113] op_sel_hi:[0,1,1]
	v_pk_fma_f32 v[118:119], v[2:3], v[212:213], v[130:131] op_sel_hi:[0,1,1]
	v_pk_fma_f32 v[114:115], v[2:3], v[144:145], v[114:115] op_sel_hi:[0,1,1]
	v_pk_fma_f32 v[130:131], v[2:3], v[220:221], v[132:133] op_sel_hi:[0,1,1]
	v_pk_fma_f32 v[120:121], v[2:3], v[146:147], v[120:121] op_sel_hi:[0,1,1]
	v_pk_fma_f32 v[132:133], v[2:3], v[228:229], v[134:135] op_sel_hi:[0,1,1]
	v_pk_fma_f32 v[122:123], v[2:3], v[148:149], v[122:123] op_sel_hi:[0,1,1]
	v_pk_fma_f32 v[134:135], v[2:3], v[236:237], v[136:137] op_sel_hi:[0,1,1]
	v_pk_fma_f32 v[124:125], v[2:3], v[150:151], v[124:125] op_sel_hi:[0,1,1]
	v_pk_fma_f32 v[136:137], v[2:3], v[244:245], v[138:139] op_sel_hi:[0,1,1]
	v_pk_fma_f32 v[0:1], v[2:3], v[152:153], v[0:1] op_sel_hi:[0,1,1]
	v_pk_fma_f32 v[2:3], v[24:25], v[198:199], v[126:127] op_sel_hi:[0,1,1]
	v_pk_fma_f32 v[102:103], v[24:25], v[104:105], v[102:103] op_sel_hi:[0,1,1]
	v_pk_fma_f32 v[104:105], v[24:25], v[108:109], v[106:107] op_sel_hi:[0,1,1]
	v_pk_fma_f32 v[106:107], v[24:25], v[128:129], v[110:111] op_sel_hi:[0,1,1]
	v_pk_fma_f32 v[108:109], v[24:25], v[206:207], v[116:117] op_sel_hi:[0,1,1]
	v_pk_fma_f32 v[110:111], v[24:25], v[154:155], v[112:113] op_sel_hi:[0,1,1]
	v_pk_fma_f32 v[112:113], v[24:25], v[214:215], v[118:119] op_sel_hi:[0,1,1]
	v_pk_fma_f32 v[114:115], v[24:25], v[156:157], v[114:115] op_sel_hi:[0,1,1]
	v_pk_fma_f32 v[116:117], v[24:25], v[222:223], v[130:131] op_sel_hi:[0,1,1]
	v_pk_fma_f32 v[118:119], v[24:25], v[158:159], v[120:121] op_sel_hi:[0,1,1]
	v_pk_fma_f32 v[122:123], v[24:25], v[160:161], v[122:123] op_sel_hi:[0,1,1]
	v_pk_fma_f32 v[124:125], v[24:25], v[162:163], v[124:125] op_sel_hi:[0,1,1]
	v_pk_fma_f32 v[0:1], v[24:25], v[164:165], v[0:1] op_sel_hi:[0,1,1]
	s_waitcnt vmcnt(7)
	v_pk_mul_f32 v[2:3], v[2:3], v[82:83]
	v_pk_mul_f32 v[82:83], v[102:103], v[84:85]
	s_waitcnt vmcnt(6)
	v_pk_mul_f32 v[84:85], v[104:105], v[86:87]
	v_pk_mul_f32 v[86:87], v[106:107], v[88:89]
	v_pk_fma_f32 v[126:127], v[24:25], v[238:239], v[134:135] op_sel_hi:[0,1,1]
	v_pk_fma_f32 v[128:129], v[24:25], v[246:247], v[136:137] op_sel_hi:[0,1,1]
	s_waitcnt vmcnt(5)
	v_pk_mul_f32 v[88:89], v[108:109], v[90:91]
	v_pk_mul_f32 v[90:91], v[110:111], v[92:93]
	s_waitcnt vmcnt(4)
	v_pk_mul_f32 v[92:93], v[112:113], v[94:95]
	v_pk_mul_f32 v[94:95], v[114:115], v[96:97]
	s_waitcnt vmcnt(3)
	v_pk_mul_f32 v[96:97], v[116:117], v[98:99]
	v_pk_mul_f32 v[98:99], v[118:119], v[100:101]
	s_waitcnt vmcnt(2)
	v_pk_mul_f32 v[52:53], v[122:123], v[52:53]
	s_waitcnt vmcnt(1)
	v_pk_mul_f32 v[102:103], v[124:125], v[56:57]
	s_waitcnt vmcnt(0)
; __device__ __forceinline__ void p9_final(Frame& F) {
;     ...
;             v[j] = x1[j] * DN_ALPHA + ((const f32x4*)(mod + (size_t)b * 12288 + 10240))[lane + 64 * j] * y; s += (v[j][0] + v[j][1]) + (v[j][2] + v[j][3]); }
;         const float mean = wave_sum(s) * (1.f / DM); float s2 = 0.f;
; #pragma unroll
;         for (int j = 0; j < 8; ++j) { v[j] = v[j] - mean; s2 += (v[j][0] * v[j][0] + v[j][1] * v[j][1]) + (v[j][2] * v[j][2] + v[j][3] * v[j][3]); }
	v_pk_mul_f32 v[106:107], v[0:1], v[60:61]
	v_pk_fma_f32 v[82:83], v[168:169], s[12:13], v[82:83] op_sel_hi:[1,0,1]
	v_pk_fma_f32 v[108:109], v[166:167], s[12:13], v[2:3] op_sel_hi:[1,0,1]
	v_pk_fma_f32 v[86:87], v[174:175], s[12:13], v[86:87] op_sel_hi:[1,0,1]
	v_pk_fma_f32 v[84:85], v[172:173], s[12:13], v[84:85] op_sel_hi:[1,0,1]
	v_pk_mul_f32 v[100:101], v[126:127], v[54:55]
	v_pk_mul_f32 v[104:105], v[128:129], v[58:59]
	v_pk_fma_f32 v[90:91], v[178:179], s[12:13], v[90:91] op_sel_hi:[1,0,1]
	v_pk_fma_f32 v[88:89], v[176:177], s[12:13], v[88:89] op_sel_hi:[1,0,1]
	v_pk_fma_f32 v[60:61], v[186:187], s[12:13], v[98:99] op_sel_hi:[1,0,1]
	v_pk_fma_f32 v[58:59], v[184:185], s[12:13], v[96:97] op_sel_hi:[1,0,1]
	v_pk_fma_f32 v[56:57], v[190:191], s[12:13], v[52:53] op_sel_hi:[1,0,1]
	v_pk_fma_f32 v[2:3], v[62:63], s[12:13], v[102:103] op_sel_hi:[1,0,1]
	v_pk_fma_f32 v[52:53], v[64:65], s[12:13], v[106:107] op_sel_hi:[1,0,1]
	v_mov_b32_e32 v62, v108
	v_mov_b32_e32 v63, v84
	v_mov_b32_e32 v64, v109
	v_mov_b32_e32 v65, v85
	v_mov_b32_e32 v96, v82
	v_mov_b32_e32 v97, v86
	v_mov_b32_e32 v98, v83
	v_mov_b32_e32 v99, v87
	v_pk_fma_f32 v[0:1], v[192:193], s[12:13], v[100:101] op_sel_hi:[1,0,1]
	v_pk_mov_b32 v[100:101], v[88:89], v[90:91] op_sel:[1,0]
	v_mov_b32_e32 v102, v88
	v_mov_b32_e32 v103, v91
	v_pk_add_f32 v[62:63], v[62:63], v[64:65]
	v_pk_add_f32 v[64:65], v[96:97], v[98:99]
	v_pk_fma_f32 v[120:121], v[24:25], v[230:231], v[132:133] op_sel_hi:[0,1,1]
	v_pk_add_f32 v[96:97], v[100:101], v[102:103]
	v_pk_add_f32 v[62:63], v[62:63], v[64:65]
	v_pk_mul_f32 v[50:51], v[120:121], v[50:51]
	v_pk_fma_f32 v[94:95], v[182:183], s[12:13], v[94:95] op_sel_hi:[1,0,1]
	v_pk_fma_f32 v[92:93], v[180:181], s[12:13], v[92:93] op_sel_hi:[1,0,1]
	v_pk_add_f32 v[64:65], v[96:97], v[96:97] op_sel:[0,1] op_sel_hi:[1,0]
	v_add_f32_e32 v24, 0, v62
	v_pk_fma_f32 v[54:55], v[188:189], s[12:13], v[50:51] op_sel_hi:[1,0,1]
	v_pk_fma_f32 v[50:51], v[194:195], s[12:13], v[104:105] op_sel_hi:[1,0,1]
	v_add_f32_e32 v104, v92, v93
	v_add_f32_e32 v106, v94, v95
	v_mov_b32_e32 v111, v58
	v_mov_b32_e32 v105, v60
	v_mov_b32_e32 v107, v61
	v_mov_b32_e32 v65, v59
	v_add_f32_e32 v110, v24, v63
	v_pk_mov_b32 v[112:113], v[54:55], v[56:57] op_sel:[1,0]
	v_mov_b32_e32 v114, v54
	v_mov_b32_e32 v115, v57
	v_pk_add_f32 v[98:99], v[104:105], v[106:107]
	v_pk_add_f32 v[62:63], v[110:111], v[64:65]
	v_pk_add_f32 v[100:101], v[112:113], v[114:115]
	v_pk_add_f32 v[62:63], v[62:63], v[98:99]
	v_pk_add_f32 v[96:97], v[100:101], v[100:101] op_sel:[0,1] op_sel_hi:[1,0]
	v_pk_add_f32 v[62:63], v[62:63], v[62:63] op_sel:[0,1] op_sel_hi:[1,0]
	v_add_f32_e32 v116, v0, v1
	v_add_f32_e32 v118, v2, v3
	v_mov_b32_e32 v117, v52
	v_mov_b32_e32 v119, v53
	v_mov_b32_e32 v97, v51
	v_mov_b32_e32 v63, v50
	v_pk_add_f32 v[102:103], v[116:117], v[118:119]
	v_pk_add_f32 v[62:63], v[62:63], v[96:97]
	v_readfirstlane_b32 s2, v10
	v_pk_add_f32 v[62:63], v[62:63], v[102:103]
	v_readfirstlane_b32 s3, v11
	v_add_f32_e32 v24, v62, v63
	ds_bpermute_b32 v62, v66, v24
	s_waitcnt lgkmcnt(0)
	v_add_f32_e32 v24, v24, v62
	ds_bpermute_b32 v62, v67, v24
	s_waitcnt lgkmcnt(0)
	v_add_f32_e32 v24, v24, v62
	ds_bpermute_b32 v62, v68, v24
	s_waitcnt lgkmcnt(0)
	v_add_f32_e32 v24, v24, v62
	ds_bpermute_b32 v62, v69, v24
	s_waitcnt lgkmcnt(0)
	v_add_f32_e32 v24, v24, v62
	ds_bpermute_b32 v62, v70, v24
	s_waitcnt lgkmcnt(0)
	v_add_f32_e32 v24, v24, v62
	ds_bpermute_b32 v62, v71, v24
	s_waitcnt lgkmcnt(0)
	v_add_f32_e32 v24, v24, v62
	v_fmamk_f32 v83, v24, 0xba000000, v83
	v_fmamk_f32 v109, v24, 0xba000000, v109
	v_fmamk_f32 v87, v24, 0xba000000, v87
	v_fmamk_f32 v85, v24, 0xba000000, v85
	v_fmac_f32_e32 v82, 0xba000000, v24
	v_fmac_f32_e32 v108, 0xba000000, v24
	v_fmac_f32_e32 v86, 0xba000000, v24
	v_fmac_f32_e32 v84, 0xba000000, v24
	v_fmamk_f32 v89, v24, 0xba000000, v89
	v_fmac_f32_e32 v88, 0xba000000, v24
	v_fmamk_f32 v91, v24, 0xba000000, v91
	v_fmac_f32_e32 v90, 0xba000000, v24
	v_mov_b32_e32 v64, v109
	v_mov_b32_e32 v65, v85
	v_mov_b32_e32 v98, v83
	v_mov_b32_e32 v99, v87
	v_mov_b32_e32 v62, v108
	v_mov_b32_e32 v63, v84
	v_mov_b32_e32 v96, v82
	v_mov_b32_e32 v97, v86
	v_pk_mul_f32 v[100:101], v[90:91], v[90:91]
	v_pk_mul_f32 v[102:103], v[88:89], v[88:89]
	v_pk_mul_f32 v[64:65], v[64:65], v[64:65]
	v_pk_mul_f32 v[98:99], v[98:99], v[98:99]
	v_fmac_f32_e32 v92, 0xba000000, v24
	v_fmac_f32_e32 v94, 0xba000000, v24
	v_pk_mov_b32 v[116:117], v[102:103], v[100:101] op_sel:[1,0]
	v_mov_b32_e32 v103, v101
	v_pk_fma_f32 v[62:63], v[62:63], v[62:63], v[64:65]
	v_pk_fma_f32 v[64:65], v[96:97], v[96:97], v[98:99]
	v_fmamk_f32 v93, v24, 0xba000000, v93
	v_fmamk_f32 v95, v24, 0xba000000, v95
	v_fmamk_f32 v61, v24, 0xba000000, v61
	v_fmac_f32_e32 v60, 0xba000000, v24
	v_fmamk_f32 v59, v24, 0xba000000, v59
	v_fmac_f32_e32 v58, 0xba000000, v24
	v_fmamk_f32 v55, v24, 0xba000000, v55
	v_fmac_f32_e32 v54, 0xba000000, v24
	v_fmamk_f32 v57, v24, 0xba000000, v57
	v_fmac_f32_e32 v56, 0xba000000, v24
	v_fmamk_f32 v1, v24, 0xba000000, v1
	v_fmac_f32_e32 v0, 0xba000000, v24
	v_fmamk_f32 v3, v24, 0xba000000, v3
	v_fmac_f32_e32 v2, 0xba000000, v24
	v_fmamk_f32 v53, v24, 0xba000000, v53
	v_fmac_f32_e32 v52, 0xba000000, v24
	v_fmamk_f32 v51, v24, 0xba000000, v51
	v_fmac_f32_e32 v50, 0xba000000, v24
	v_mul_f32_e32 v24, v92, v92
	v_mul_f32_e32 v104, v94, v94
	v_pk_add_f32 v[96:97], v[116:117], v[102:103]
	v_pk_add_f32 v[62:63], v[62:63], v[64:65]
	v_pk_fma_f32 v[100:101], v[92:93], v[92:93], v[24:25] op_sel_hi:[1,1,0]
	v_pk_fma_f32 v[104:105], v[94:95], v[94:95], v[104:105] op_sel_hi:[1,1,0]
	v_pk_add_f32 v[64:65], v[96:97], v[96:97] op_sel_hi:[0,1]
	v_pk_add_f32 v[62:63], v[62:63], v[62:63] op_sel_hi:[0,1]
	v_pk_mul_f32 v[106:107], v[56:57], v[56:57]
	v_pk_mul_f32 v[110:111], v[54:55], v[54:55]
	v_mul_f32_e32 v100, v58, v58
	v_mul_f32_e32 v104, v59, v59
	v_mul_f32_e32 v64, v60, v60
	v_mul_f32_e32 v62, v61, v61
	v_pk_mov_b32 v[118:119], v[110:111], v[106:107] op_sel:[1,0]
	v_mov_b32_e32 v111, v107
	v_pk_add_f32 v[96:97], v[100:101], v[104:105]
	v_pk_add_f32 v[62:63], v[64:65], v[62:63]
	v_mul_f32_e32 v112, v0, v0
	v_mul_f32_e32 v114, v2, v2
	v_pk_add_f32 v[98:99], v[118:119], v[110:111]
	v_pk_add_f32 v[62:63], v[96:97], v[62:63]
	v_pk_fma_f32 v[106:107], v[0:1], v[0:1], v[112:113] op_sel_hi:[1,1,0]
	v_pk_fma_f32 v[112:113], v[2:3], v[2:3], v[114:115] op_sel_hi:[1,1,0]
	v_pk_add_f32 v[98:99], v[98:99], v[98:99] op_sel_hi:[0,1]
	v_pk_add_f32 v[62:63], v[62:63], v[62:63] op_sel_hi:[0,1]
	v_mul_f32_e32 v106, v50, v50
	v_mul_f32_e32 v112, v51, v51
	v_mul_f32_e32 v98, v52, v52
	v_mul_f32_e32 v62, v53, v53
	v_pk_add_f32 v[100:101], v[106:107], v[112:113]
	v_pk_add_f32 v[62:63], v[98:99], v[62:63]
	s_nop 0
	v_pk_add_f32 v[62:63], v[100:101], v[62:63]
	s_nop 0
	v_add_f32_e32 v24, v62, v63
	ds_bpermute_b32 v62, v66, v24
	s_waitcnt lgkmcnt(0)
; __device__ __forceinline__ void p9_final(Frame& F) {
;     ...
;         const float mean = wave_sum(s) * (1.f / DM); float s2 = 0.f;
; #pragma unroll
;         for (int j = 0; j < 8; ++j) { v[j] = v[j] - mean; s2 += (v[j][0] * v[j][0] + v[j][1] * v[j][1]) + (v[j][2] * v[j][2] + v[j][3] * v[j][3]); }
;         const float rstd = 1.f / sqrtf(wave_sum(s2) * (1.f / DM) + LN_EPS);
; #pragma unroll
;         for (int j = 0; j < 8; ++j) __builtin_nontemporal_store(v[j] * rstd * ((const f32x4*)F.in[I_LN2W])[lane + 64 * j] + ((const f32x4*)F.in[I_LN2B])[lane + 64 * j], (f32x4*)(F.out + (size_t)t * DM) + lane + 64 * j);
	v_add_f32_e32 v24, v24, v62
	ds_bpermute_b32 v62, v67, v24
	s_waitcnt lgkmcnt(0)
	v_add_f32_e32 v24, v24, v62
	ds_bpermute_b32 v62, v68, v24
	s_waitcnt lgkmcnt(0)
	v_add_f32_e32 v24, v24, v62
	ds_bpermute_b32 v62, v69, v24
	s_waitcnt lgkmcnt(0)
	v_add_f32_e32 v24, v24, v62
	ds_bpermute_b32 v62, v70, v24
	s_waitcnt lgkmcnt(0)
	v_add_f32_e32 v24, v24, v62
	ds_bpermute_b32 v62, v71, v24
	s_waitcnt lgkmcnt(0)
	v_add_f32_e32 v24, v24, v62
	v_fmamk_f32 v24, v24, 0x3a000000, v79
	v_mul_f32_e32 v62, 0x4f800000, v24
	v_cmp_gt_f32_e32 vcc, s15, v24
	s_nop 1
	v_cndmask_b32_e32 v24, v24, v62, vcc
	v_sqrt_f32_e32 v62, v24
	s_nop 0
	v_add_u32_e32 v63, -1, v62
	v_add_u32_e32 v64, 1, v62
	v_fma_f32 v65, -v63, v62, v24
	v_fma_f32 v81, -v64, v62, v24
	v_cmp_ge_f32_e64 s[0:1], 0, v65
	s_nop 1
	v_cndmask_b32_e64 v62, v62, v63, s[0:1]
	v_cmp_lt_f32_e64 s[0:1], 0, v81
	s_nop 1
	v_cndmask_b32_e64 v62, v62, v64, s[0:1]
	v_mul_f32_e32 v63, 0x37800000, v62
	v_cndmask_b32_e32 v62, v62, v63, vcc
	v_cmp_class_f32_e32 vcc, v24, v80
	s_nop 1
	v_cndmask_b32_e32 v24, v62, v24, vcc
	v_div_scale_f32 v62, s[0:1], v24, v24, 1.0
	v_rcp_f32_e32 v64, v62
	v_div_scale_f32 v63, vcc, 1.0, v24, 1.0
	v_readfirstlane_b32 s0, v8
	v_fma_f32 v65, -v62, v64, 1.0
	v_fmac_f32_e32 v64, v65, v64
	v_mul_f32_e32 v65, v63, v64
	v_fma_f32 v81, -v62, v65, v63
	v_fmac_f32_e32 v65, v81, v64
	v_fma_f32 v62, -v62, v65, v63
	v_div_fmas_f32 v62, v62, v64, v65
	v_div_fixup_f32 v24, v62, v24, 1.0
	v_pk_mul_f32 v[62:63], v[108:109], v[24:25] op_sel_hi:[1,0]
	v_pk_mul_f32 v[64:65], v[82:83], v[24:25] op_sel_hi:[1,0]
	v_pk_fma_f32 v[16:17], v[16:17], v[62:63], v[20:21]
	v_pk_fma_f32 v[18:19], v[18:19], v[64:65], v[22:23]
	global_store_dwordx4 v[46:47], v[16:19], off offset:-4096 nt
	global_load_dwordx4 v[16:19], v[26:27], off offset:1024
	s_nop 0
	global_load_dwordx4 v[20:23], v[28:29], off offset:1024
	v_pk_mul_f32 v[62:63], v[86:87], v[24:25] op_sel_hi:[1,0]
	v_pk_mul_f32 v[64:65], v[84:85], v[24:25] op_sel_hi:[1,0]
	v_pk_mul_f32 v[60:61], v[60:61], v[24:25] op_sel_hi:[1,0]
	v_pk_mul_f32 v[58:59], v[58:59], v[24:25] op_sel_hi:[1,0]
	v_pk_mul_f32 v[56:57], v[56:57], v[24:25] op_sel_hi:[1,0]
	v_pk_mul_f32 v[54:55], v[54:55], v[24:25] op_sel_hi:[1,0]
	v_pk_mul_f32 v[2:3], v[2:3], v[24:25] op_sel_hi:[1,0]
	v_pk_mul_f32 v[0:1], v[0:1], v[24:25] op_sel_hi:[1,0]
	v_readfirstlane_b32 s1, v9
	v_pk_mul_f32 v[10:11], v[52:53], v[24:25] op_sel_hi:[1,0]
	v_pk_mul_f32 v[8:9], v[50:51], v[24:25] op_sel_hi:[1,0]
	s_and_b64 vcc, s[24:25], exec
	s_waitcnt vmcnt(0)
	v_pk_fma_f32 v[16:17], v[16:17], v[64:65], v[20:21]
	v_pk_fma_f32 v[18:19], v[18:19], v[62:63], v[22:23]
	global_store_dwordx4 v[46:47], v[16:19], off offset:-3072 nt
	global_load_dwordx4 v[16:19], v[26:27], off offset:2048
	s_nop 0
	global_load_dwordx4 v[20:23], v[28:29], off offset:2048
	v_pk_mul_f32 v[62:63], v[90:91], v[24:25] op_sel_hi:[1,0]
	v_pk_mul_f32 v[64:65], v[88:89], v[24:25] op_sel_hi:[1,0]
	s_waitcnt vmcnt(0)
	v_pk_fma_f32 v[18:19], v[18:19], v[62:63], v[22:23]
	v_pk_fma_f32 v[16:17], v[16:17], v[64:65], v[20:21]
	global_store_dwordx4 v[46:47], v[16:19], off offset:-2048 nt
	global_load_dwordx4 v[16:19], v[26:27], off offset:3072
	s_nop 0
	global_load_dwordx4 v[20:23], v[28:29], off offset:3072
	v_pk_mul_f32 v[62:63], v[94:95], v[24:25] op_sel_hi:[1,0]
	v_pk_mul_f32 v[64:65], v[92:93], v[24:25] op_sel_hi:[1,0]
	s_waitcnt vmcnt(0)
	v_pk_fma_f32 v[18:19], v[18:19], v[62:63], v[22:23]
	v_pk_fma_f32 v[16:17], v[16:17], v[64:65], v[20:21]
	global_store_dwordx4 v[46:47], v[16:19], off offset:-1024 nt
	global_load_dwordx4 v[16:19], v[30:31], off
	s_nop 0
	global_load_dwordx4 v[20:23], v[32:33], off
	s_waitcnt vmcnt(0)
	v_pk_fma_f32 v[16:17], v[16:17], v[58:59], v[20:21]
	v_pk_fma_f32 v[18:19], v[18:19], v[60:61], v[22:23]
	global_store_dwordx4 v[46:47], v[16:19], off nt
	global_load_dwordx4 v[16:19], v[34:35], off
	s_nop 0
	global_load_dwordx4 v[20:23], v[36:37], off
	s_waitcnt vmcnt(0)
	v_pk_fma_f32 v[16:17], v[54:55], v[16:17], v[20:21]
	v_pk_fma_f32 v[18:19], v[56:57], v[18:19], v[22:23]
	global_store_dwordx4 v[46:47], v[16:19], off offset:1024 nt
	global_load_dwordx4 v[16:19], v[38:39], off
	s_nop 0
	global_load_dwordx4 v[20:23], v[40:41], off
	s_waitcnt vmcnt(0)
	v_pk_fma_f32 v[0:1], v[0:1], v[16:17], v[20:21]
	v_pk_fma_f32 v[2:3], v[2:3], v[18:19], v[22:23]
	global_store_dwordx4 v[46:47], v[0:3], off offset:2048 nt
	global_load_dwordx4 v[16:19], v[42:43], off
	global_load_dwordx4 v[20:23], v[44:45], off
	v_mov_b64_e32 v[0:1], v[12:13]
	v_mov_b64_e32 v[2:3], v[14:15]
	s_waitcnt vmcnt(0)
	v_pk_fma_f32 v[8:9], v[8:9], v[16:17], v[20:21]
	v_pk_fma_f32 v[10:11], v[10:11], v[18:19], v[22:23]
	global_store_dwordx4 v[46:47], v[8:11], off offset:3072 nt
	v_lshl_add_u64 v[46:47], v[46:47], 0, s[8:9]
	s_cbranch_vccnz .LBB0_1211
